# speedup vs baseline: 1.0126x; 1.0126x over previous
_Z4k_k2ILb0EEvPKDF16_S1_PKfS3_S3_S1_S1_PfS3_S3_S1_PDF16_PKiS4_S4_:
	s_load_dwordx2 s[24:25], s[0:1], 0x58
	s_load_dwordx8 s[4:11], s[0:1], 0x38
	s_load_dwordx4 s[20:23], s[0:1], 0x0
	s_load_dwordx8 s[12:19], s[0:1], 0x18
	s_load_dwordx2 s[54:55], s[0:1], 0x10
	s_lshl_b32 s3, s2, 5
	s_and_b32 s3, s3, 0xe0
	s_lshr_b32 s26, s2, 3
	s_or_b32 s3, s3, s26
	s_movk_i32 s26, 0x100
	s_lshl_b32 s28, s3, 5
	v_cmp_gt_u32_e32 vcc, s26, v0
	v_mov_b32_e32 v67, 0
	v_lshlrev_b32_e32 v66, 4, v0
	s_and_saveexec_b64 s[26:27], vcc
	s_cbranch_execz .LBB5_2
	s_mov_b32 s29, 0
	s_lshl_b64 s[30:31], s[28:29], 7
	s_waitcnt lgkmcnt(0)
	s_add_u32 s0, s54, s30
	s_addc_u32 s1, s55, s31
	global_load_dwordx4 v[200:203], v66, s[0:1]
.LBB5_2:
	s_or_b64 exec, exec, s[26:27]
	s_lshl_b32 s0, s3, 1
	s_and_b32 s26, s0, 0xffffffe
	s_mov_b32 s27, 0
	s_waitcnt lgkmcnt(0)
	v_lshl_add_u64 v[2:3], s[16:17], 0, v[66:67]
	s_lshl_b64 s[0:1], s[26:27], 13
	s_or_b32 s26, s26, 1
	v_lshl_add_u64 v[4:5], v[2:3], 0, s[0:1]
	s_lshl_b64 s[0:1], s[26:27], 13
	v_lshl_add_u64 v[2:3], v[2:3], 0, s[0:1]
	global_load_dwordx4 v[68:71], v[4:5], off
	global_load_dwordx4 v[72:75], v[2:3], off
	v_lshl_add_u64 v[2:3], s[12:13], 0, v[66:67]
	s_movk_i32 s29, 0x2000
	v_add_co_u32_e32 v4, vcc, s29, v2
	s_movk_i32 s52, 0x4000
	s_nop 0
	v_addc_co_u32_e32 v5, vcc, 0, v3, vcc
	v_add_co_u32_e32 v18, vcc, s52, v2
	s_movk_i32 s33, 0x6000
	s_nop 0
	v_addc_co_u32_e32 v19, vcc, 0, v3, vcc
	s_lshl_b32 s26, s3, 2
	global_load_dwordx4 v[14:17], v66, s[12:13]
	global_load_dwordx4 v[10:13], v[4:5], off
	global_load_dwordx4 v[6:9], v[18:19], off
	v_add_co_u32_e32 v18, vcc, s33, v2
	s_add_u32 s0, s24, 0x800000
	s_nop 0
	v_addc_co_u32_e32 v19, vcc, 0, v3, vcc
	s_addc_u32 s1, s25, 0
	s_lshl_b64 s[12:13], s[26:27], 13
	v_lshlrev_b32_e32 v20, 2, v0
	global_load_dwordx4 v[2:5], v[18:19], off
	global_load_dword v1, v20, s[14:15]
	v_or_b32_e32 v18, s12, v66
	v_mov_b32_e32 v19, s13
	s_or_b32 s12, s26, 1
	s_mov_b32 s13, s27
	s_lshl_b64 s[12:13], s[12:13], 13
	v_lshl_add_u64 v[76:77], s[22:23], 0, v[18:19]
	v_lshl_add_u64 v[78:79], s[20:21], 0, v[18:19]
	v_lshl_add_u64 v[80:81], s[0:1], 0, v[18:19]
	v_or_b32_e32 v18, s12, v66
	v_mov_b32_e32 v19, s13
	s_or_b32 s12, s26, 2
	s_mov_b32 s13, s27
	s_lshl_b64 s[12:13], s[12:13], 13
	s_or_b32 s26, s26, 3
	v_lshl_add_u64 v[82:83], s[22:23], 0, v[18:19]
	v_lshl_add_u64 v[84:85], s[20:21], 0, v[18:19]
	v_lshl_add_u64 v[86:87], s[0:1], 0, v[18:19]
	v_or_b32_e32 v18, s12, v66
	v_mov_b32_e32 v19, s13
	s_lshl_b64 s[12:13], s[26:27], 13
	v_lshl_add_u64 v[88:89], s[22:23], 0, v[18:19]
	v_lshl_add_u64 v[90:91], s[20:21], 0, v[18:19]
	v_lshl_add_u64 v[92:93], s[0:1], 0, v[18:19]
	v_or_b32_e32 v18, s12, v66
	v_mov_b32_e32 v19, s13
	v_lshl_add_u64 v[94:95], s[22:23], 0, v[18:19]
	v_lshl_add_u64 v[96:97], s[20:21], 0, v[18:19]
	v_lshl_add_u64 v[98:99], s[0:1], 0, v[18:19]
	global_load_dwordx4 v[62:65], v[76:77], off
	global_load_dwordx4 v[54:57], v[78:79], off
	global_load_dwordx4 v[58:61], v[80:81], off
	global_load_dwordx4 v[50:53], v[82:83], off
	global_load_dwordx4 v[42:45], v[84:85], off
	global_load_dwordx4 v[46:49], v[86:87], off
	global_load_dwordx4 v[38:41], v[88:89], off
	global_load_dwordx4 v[30:33], v[90:91], off
	global_load_dwordx4 v[34:37], v[92:93], off
	global_load_dwordx4 v[26:29], v[94:95], off
	global_load_dwordx4 v[18:21], v[96:97], off
	global_load_dwordx4 v[22:25], v[98:99], off
	s_movk_i32 s56, 0x100
	v_cmp_gt_u32_e32 vcc, s56, v0
	s_nop 1
	s_and_saveexec_b64 s[56:57], vcc
	s_cbranch_execz .Lk2f_bc_done
	s_waitcnt vmcnt(19)
	ds_write_b128 v66, v[200:203]
.Lk2f_bc_done:
	s_or_b64 exec, exec, s[56:57]
	s_waitcnt lgkmcnt(0)
	s_barrier
	s_waitcnt vmcnt(18)
	v_cvt_f32_f16_e32 v134, v68
	v_cvt_f32_f16_sdwa v135, v68 dst_sel:DWORD dst_unused:UNUSED_PAD src0_sel:WORD_1
	v_cvt_f32_f16_e32 v136, v69
	v_cvt_f32_f16_sdwa v137, v69 dst_sel:DWORD dst_unused:UNUSED_PAD src0_sel:WORD_1
	v_cvt_f32_f16_e32 v138, v70
	v_cvt_f32_f16_sdwa v139, v70 dst_sel:DWORD dst_unused:UNUSED_PAD src0_sel:WORD_1
	v_cvt_f32_f16_e32 v140, v71
	v_cvt_f32_f16_sdwa v141, v71 dst_sel:DWORD dst_unused:UNUSED_PAD src0_sel:WORD_1
	s_waitcnt vmcnt(17)
	v_cvt_f32_f16_e32 v142, v72
	v_cvt_f32_f16_sdwa v143, v72 dst_sel:DWORD dst_unused:UNUSED_PAD src0_sel:WORD_1
	v_cvt_f32_f16_e32 v144, v73
	v_cvt_f32_f16_sdwa v145, v73 dst_sel:DWORD dst_unused:UNUSED_PAD src0_sel:WORD_1
	v_cvt_f32_f16_e32 v146, v74
	v_cvt_f32_f16_sdwa v147, v74 dst_sel:DWORD dst_unused:UNUSED_PAD src0_sel:WORD_1
	v_cvt_f32_f16_e32 v148, v75
	v_cvt_f32_f16_sdwa v149, v75 dst_sel:DWORD dst_unused:UNUSED_PAD src0_sel:WORD_1
	ds_read_b128 v[70:73], v67
	ds_read_b128 v[74:77], v67 offset:16
	ds_read_b128 v[78:81], v67 offset:32
	ds_read_b128 v[82:85], v67 offset:48
	ds_read_b128 v[86:89], v67 offset:64
	ds_read_b128 v[90:93], v67 offset:80
	ds_read_b128 v[94:97], v67 offset:96
	ds_read_b128 v[98:101], v67 offset:112
	ds_read_b128 v[102:105], v67 offset:128
	ds_read_b128 v[106:109], v67 offset:144
	ds_read_b128 v[110:113], v67 offset:160
	ds_read_b128 v[114:117], v67 offset:176
	ds_read_b128 v[118:121], v67 offset:192
	ds_read_b128 v[122:125], v67 offset:208
	ds_read_b128 v[126:129], v67 offset:224
	ds_read_b128 v[130:133], v67 offset:240
	v_lshlrev_b32_e32 v68, 1, v0
	s_waitcnt vmcnt(11)
	v_cvt_f32_f16_e32 v150, v62
	s_waitcnt vmcnt(10)
	v_cvt_f32_f16_e32 v69, v54
	v_pk_mul_f32 v[154:155], v[150:151], v[14:15] op_sel_hi:[0,1]
	v_exp_f32_e32 v154, v154
	v_exp_f32_e32 v155, v155
	v_pk_mul_f32 v[156:157], v[150:151], v[16:17] op_sel_hi:[0,1]
	v_exp_f32_e32 v156, v156
	v_exp_f32_e32 v157, v157
	v_mul_f32_e32 v152, v150, v69
	v_pk_mul_f32 v[134:135], v[154:155], v[134:135]
	s_waitcnt lgkmcnt(14)
	v_pk_fma_f32 v[134:135], v[152:153], v[70:71], v[134:135] op_sel_hi:[0,1,1]
	s_waitcnt lgkmcnt(11)
	v_pk_fma_f32 v[70:71], v[86:87], v[134:135], 0 op_sel_hi:[1,1,0]
	v_pk_mul_f32 v[86:87], v[156:157], v[136:137]
	s_nop 0
	v_pk_fma_f32 v[136:137], v[152:153], v[72:73], v[86:87] op_sel_hi:[0,1,1]
	v_pk_mul_f32 v[72:73], v[150:151], v[10:11] op_sel_hi:[0,1]
	v_exp_f32_e32 v72, v72
	v_exp_f32_e32 v73, v73
	v_pk_mul_f32 v[86:87], v[150:151], v[12:13] op_sel_hi:[0,1]
	v_exp_f32_e32 v86, v86
	v_exp_f32_e32 v87, v87
	v_pk_mul_f32 v[72:73], v[72:73], v[138:139]
	v_pk_fma_f32 v[70:71], v[88:89], v[136:137], v[70:71]
	v_pk_fma_f32 v[138:139], v[152:153], v[74:75], v[72:73] op_sel_hi:[0,1,1]
	v_pk_mul_f32 v[72:73], v[86:87], v[140:141]
	v_pk_mul_f32 v[74:75], v[150:151], v[8:9] op_sel_hi:[0,1]
	v_pk_fma_f32 v[140:141], v[152:153], v[76:77], v[72:73] op_sel_hi:[0,1,1]
	v_pk_mul_f32 v[72:73], v[150:151], v[6:7] op_sel_hi:[0,1]
	v_exp_f32_e32 v72, v72
	v_exp_f32_e32 v73, v73
	v_exp_f32_e32 v74, v74
	v_exp_f32_e32 v75, v75
	s_waitcnt lgkmcnt(10)
	v_pk_fma_f32 v[70:71], v[90:91], v[138:139], v[70:71]
	v_pk_mul_f32 v[72:73], v[72:73], v[142:143]
	v_pk_fma_f32 v[70:71], v[92:93], v[140:141], v[70:71]
	v_pk_fma_f32 v[142:143], v[152:153], v[78:79], v[72:73] op_sel_hi:[0,1,1]
	v_pk_mul_f32 v[72:73], v[74:75], v[144:145]
	v_pk_mul_f32 v[74:75], v[150:151], v[4:5] op_sel_hi:[0,1]
	v_pk_fma_f32 v[144:145], v[152:153], v[80:81], v[72:73] op_sel_hi:[0,1,1]
	v_pk_mul_f32 v[72:73], v[150:151], v[2:3] op_sel_hi:[0,1]
	v_exp_f32_e32 v72, v72
	v_exp_f32_e32 v73, v73
	v_exp_f32_e32 v74, v74
	v_exp_f32_e32 v75, v75
	s_waitcnt lgkmcnt(9)
	v_pk_fma_f32 v[70:71], v[94:95], v[142:143], v[70:71]
	v_pk_mul_f32 v[72:73], v[72:73], v[146:147]
	v_pk_fma_f32 v[70:71], v[96:97], v[144:145], v[70:71]
	v_pk_fma_f32 v[146:147], v[152:153], v[82:83], v[72:73] op_sel_hi:[0,1,1]
	v_pk_mul_f32 v[72:73], v[74:75], v[148:149]
	s_waitcnt lgkmcnt(8)
	v_pk_fma_f32 v[70:71], v[98:99], v[146:147], v[70:71]
	v_pk_fma_f32 v[148:149], v[152:153], v[84:85], v[72:73] op_sel_hi:[0,1,1]
	v_pk_fma_f32 v[70:71], v[100:101], v[148:149], v[70:71]
	s_nop 0
	v_add_f32_e32 v69, v70, v71
	v_fma_mix_f32 v69, v1, v54, v69 op_sel_hi:[0,1,0]
	s_waitcnt vmcnt(9)
	v_fma_mixlo_f16 v69, v69, v58, 0 op_sel_hi:[0,1,0]
	ds_write_b16 v68, v69 offset:4096
	ds_read_b128 v[70:73], v67 offset:256
	ds_read_b128 v[74:77], v67 offset:272
	ds_read_b128 v[78:81], v67 offset:288
	ds_read_b128 v[82:85], v67 offset:304
	ds_read_b128 v[86:89], v67 offset:320
	ds_read_b128 v[90:93], v67 offset:336
	ds_read_b128 v[94:97], v67 offset:352
	ds_read_b128 v[98:101], v67 offset:368
	v_cvt_f32_f16_sdwa v62, v62 dst_sel:DWORD dst_unused:UNUSED_PAD src0_sel:WORD_1
	v_cvt_f32_f16_sdwa v69, v54 dst_sel:DWORD dst_unused:UNUSED_PAD src0_sel:WORD_1
	v_pk_mul_f32 v[152:153], v[62:63], v[14:15] op_sel_hi:[0,1]
	v_exp_f32_e32 v152, v152
	v_exp_f32_e32 v153, v153
	v_pk_mul_f32 v[154:155], v[62:63], v[16:17] op_sel_hi:[0,1]
	v_exp_f32_e32 v154, v154
	v_exp_f32_e32 v155, v155
	v_mul_f32_e32 v150, v62, v69
	v_pk_mul_f32 v[134:135], v[152:153], v[134:135]
	s_waitcnt lgkmcnt(14)
	v_pk_fma_f32 v[134:135], v[150:151], v[102:103], v[134:135] op_sel_hi:[0,1,1]
	s_waitcnt lgkmcnt(12)
	v_pk_fma_f32 v[102:103], v[118:119], v[134:135], 0 op_sel_hi:[1,1,0]
	v_pk_mul_f32 v[118:119], v[154:155], v[136:137]
	s_nop 0
	v_pk_fma_f32 v[136:137], v[150:151], v[104:105], v[118:119] op_sel_hi:[0,1,1]
	v_pk_mul_f32 v[104:105], v[62:63], v[10:11] op_sel_hi:[0,1]
	v_exp_f32_e32 v104, v104
	v_exp_f32_e32 v105, v105
	v_pk_mul_f32 v[118:119], v[62:63], v[12:13] op_sel_hi:[0,1]
	v_exp_f32_e32 v118, v118
	v_exp_f32_e32 v119, v119
	v_pk_mul_f32 v[104:105], v[104:105], v[138:139]
	v_pk_fma_f32 v[102:103], v[120:121], v[136:137], v[102:103]
	v_pk_fma_f32 v[138:139], v[150:151], v[106:107], v[104:105] op_sel_hi:[0,1,1]
	v_pk_mul_f32 v[104:105], v[118:119], v[140:141]
	v_pk_mul_f32 v[106:107], v[62:63], v[8:9] op_sel_hi:[0,1]
	v_pk_fma_f32 v[140:141], v[150:151], v[108:109], v[104:105] op_sel_hi:[0,1,1]
	v_pk_mul_f32 v[104:105], v[62:63], v[6:7] op_sel_hi:[0,1]
	v_exp_f32_e32 v104, v104
	v_exp_f32_e32 v105, v105
	v_exp_f32_e32 v106, v106
	v_exp_f32_e32 v107, v107
	s_waitcnt lgkmcnt(11)
	v_pk_fma_f32 v[102:103], v[122:123], v[138:139], v[102:103]
	v_pk_mul_f32 v[104:105], v[104:105], v[142:143]
	v_pk_fma_f32 v[102:103], v[124:125], v[140:141], v[102:103]
	v_pk_fma_f32 v[142:143], v[150:151], v[110:111], v[104:105] op_sel_hi:[0,1,1]
	v_pk_mul_f32 v[104:105], v[106:107], v[144:145]
	v_pk_mul_f32 v[106:107], v[62:63], v[4:5] op_sel_hi:[0,1]
	v_pk_fma_f32 v[144:145], v[150:151], v[112:113], v[104:105] op_sel_hi:[0,1,1]
	v_pk_mul_f32 v[104:105], v[62:63], v[2:3] op_sel_hi:[0,1]
	v_exp_f32_e32 v104, v104
	v_exp_f32_e32 v105, v105
	v_exp_f32_e32 v106, v106
	v_exp_f32_e32 v107, v107
	s_waitcnt lgkmcnt(10)
	v_pk_fma_f32 v[102:103], v[126:127], v[142:143], v[102:103]
	v_pk_mul_f32 v[104:105], v[104:105], v[146:147]
	v_pk_fma_f32 v[102:103], v[128:129], v[144:145], v[102:103]
	v_pk_fma_f32 v[146:147], v[150:151], v[114:115], v[104:105] op_sel_hi:[0,1,1]
	v_pk_mul_f32 v[104:105], v[106:107], v[148:149]
	s_waitcnt lgkmcnt(9)
	v_pk_fma_f32 v[102:103], v[130:131], v[146:147], v[102:103]
	v_pk_fma_f32 v[148:149], v[150:151], v[116:117], v[104:105] op_sel_hi:[0,1,1]
	v_pk_fma_f32 v[102:103], v[132:133], v[148:149], v[102:103]
	s_nop 0
	v_add_f32_e32 v62, v102, v103
	v_fma_mix_f32 v54, v1, v54, v62 op_sel:[0,1,0] op_sel_hi:[0,1,0]
	v_fma_mixlo_f16 v54, v54, v58, 0 op_sel:[0,1,0] op_sel_hi:[0,1,0]
	ds_write_b16 v68, v54 offset:5136
	ds_read_b128 v[102:105], v67 offset:384
	ds_read_b128 v[106:109], v67 offset:400
	ds_read_b128 v[110:113], v67 offset:416
	ds_read_b128 v[114:117], v67 offset:432
	ds_read_b128 v[118:121], v67 offset:448
	ds_read_b128 v[122:125], v67 offset:464
	ds_read_b128 v[126:129], v67 offset:480
	ds_read_b128 v[130:133], v67 offset:496
	v_cvt_f32_f16_e32 v54, v63
	v_cvt_f32_f16_e32 v58, v55
	v_pk_mul_f32 v[150:151], v[54:55], v[14:15] op_sel_hi:[0,1]
	v_exp_f32_e32 v150, v150
	v_exp_f32_e32 v151, v151
	v_pk_mul_f32 v[152:153], v[54:55], v[16:17] op_sel_hi:[0,1]
	v_exp_f32_e32 v152, v152
	v_exp_f32_e32 v153, v153
	v_mul_f32_e32 v58, v54, v58
	v_pk_mul_f32 v[134:135], v[150:151], v[134:135]
	s_waitcnt lgkmcnt(14)
	v_pk_fma_f32 v[134:135], v[58:59], v[70:71], v[134:135] op_sel_hi:[0,1,1]
	s_waitcnt lgkmcnt(12)
	v_pk_fma_f32 v[70:71], v[86:87], v[134:135], 0 op_sel_hi:[1,1,0]
	v_pk_mul_f32 v[86:87], v[152:153], v[136:137]
	s_nop 0
	v_pk_fma_f32 v[136:137], v[58:59], v[72:73], v[86:87] op_sel_hi:[0,1,1]
	v_pk_mul_f32 v[72:73], v[54:55], v[10:11] op_sel_hi:[0,1]
	v_exp_f32_e32 v72, v72
	v_exp_f32_e32 v73, v73
	v_pk_mul_f32 v[86:87], v[54:55], v[12:13] op_sel_hi:[0,1]
	v_exp_f32_e32 v86, v86
	v_exp_f32_e32 v87, v87
	v_pk_mul_f32 v[72:73], v[72:73], v[138:139]
	v_pk_fma_f32 v[70:71], v[88:89], v[136:137], v[70:71]
	v_pk_fma_f32 v[138:139], v[58:59], v[74:75], v[72:73] op_sel_hi:[0,1,1]
	v_pk_mul_f32 v[72:73], v[86:87], v[140:141]
	v_pk_mul_f32 v[74:75], v[54:55], v[8:9] op_sel_hi:[0,1]
	v_pk_fma_f32 v[140:141], v[58:59], v[76:77], v[72:73] op_sel_hi:[0,1,1]
	v_pk_mul_f32 v[72:73], v[54:55], v[6:7] op_sel_hi:[0,1]
	v_exp_f32_e32 v72, v72
	v_exp_f32_e32 v73, v73
	v_exp_f32_e32 v74, v74
	v_exp_f32_e32 v75, v75
	s_waitcnt lgkmcnt(11)
	v_pk_fma_f32 v[70:71], v[90:91], v[138:139], v[70:71]
	v_pk_mul_f32 v[72:73], v[72:73], v[142:143]
	v_pk_fma_f32 v[70:71], v[92:93], v[140:141], v[70:71]
	v_pk_fma_f32 v[142:143], v[58:59], v[78:79], v[72:73] op_sel_hi:[0,1,1]
	v_pk_mul_f32 v[72:73], v[74:75], v[144:145]
	v_pk_mul_f32 v[74:75], v[54:55], v[4:5] op_sel_hi:[0,1]
	v_pk_fma_f32 v[144:145], v[58:59], v[80:81], v[72:73] op_sel_hi:[0,1,1]
	v_pk_mul_f32 v[72:73], v[54:55], v[2:3] op_sel_hi:[0,1]
	v_exp_f32_e32 v72, v72
	v_exp_f32_e32 v73, v73
	v_exp_f32_e32 v74, v74
	v_exp_f32_e32 v75, v75
	s_waitcnt lgkmcnt(10)
	v_pk_fma_f32 v[70:71], v[94:95], v[142:143], v[70:71]
	v_pk_mul_f32 v[72:73], v[72:73], v[146:147]
	v_pk_fma_f32 v[70:71], v[96:97], v[144:145], v[70:71]
	v_pk_fma_f32 v[146:147], v[58:59], v[82:83], v[72:73] op_sel_hi:[0,1,1]
	v_pk_mul_f32 v[72:73], v[74:75], v[148:149]
	s_waitcnt lgkmcnt(9)
	v_pk_fma_f32 v[70:71], v[98:99], v[146:147], v[70:71]
	v_pk_fma_f32 v[148:149], v[58:59], v[84:85], v[72:73] op_sel_hi:[0,1,1]
	v_pk_fma_f32 v[70:71], v[100:101], v[148:149], v[70:71]
	s_nop 0
	v_add_f32_e32 v54, v70, v71
	v_fma_mix_f32 v54, v1, v55, v54 op_sel_hi:[0,1,0]
	v_fma_mixlo_f16 v54, v54, v59, 0 op_sel_hi:[0,1,0]
	ds_write_b16 v68, v54 offset:6176
	ds_read_b128 v[70:73], v67 offset:512
	ds_read_b128 v[74:77], v67 offset:528
	ds_read_b128 v[78:81], v67 offset:544
	ds_read_b128 v[82:85], v67 offset:560
	ds_read_b128 v[86:89], v67 offset:576
	ds_read_b128 v[90:93], v67 offset:592
	ds_read_b128 v[94:97], v67 offset:608
	ds_read_b128 v[98:101], v67 offset:624
	v_cvt_f32_f16_sdwa v54, v63 dst_sel:DWORD dst_unused:UNUSED_PAD src0_sel:WORD_1
	v_cvt_f32_f16_sdwa v58, v55 dst_sel:DWORD dst_unused:UNUSED_PAD src0_sel:WORD_1
	v_pk_mul_f32 v[62:63], v[54:55], v[14:15] op_sel_hi:[0,1]
	v_exp_f32_e32 v62, v62
	v_exp_f32_e32 v63, v63
	v_pk_mul_f32 v[150:151], v[54:55], v[16:17] op_sel_hi:[0,1]
	v_exp_f32_e32 v150, v150
	v_exp_f32_e32 v151, v151
	v_mul_f32_e32 v58, v54, v58
	v_pk_mul_f32 v[62:63], v[62:63], v[134:135]
	s_waitcnt lgkmcnt(14)
	v_pk_fma_f32 v[62:63], v[58:59], v[102:103], v[62:63] op_sel_hi:[0,1,1]
	s_waitcnt lgkmcnt(12)
	v_pk_fma_f32 v[102:103], v[118:119], v[62:63], 0 op_sel_hi:[1,1,0]
	v_pk_mul_f32 v[118:119], v[150:151], v[136:137]
	s_nop 0
	v_pk_fma_f32 v[134:135], v[58:59], v[104:105], v[118:119] op_sel_hi:[0,1,1]
	v_pk_mul_f32 v[104:105], v[54:55], v[10:11] op_sel_hi:[0,1]
	v_exp_f32_e32 v104, v104
	v_exp_f32_e32 v105, v105
	v_pk_mul_f32 v[118:119], v[54:55], v[12:13] op_sel_hi:[0,1]
	v_exp_f32_e32 v118, v118
	v_exp_f32_e32 v119, v119
	v_pk_mul_f32 v[104:105], v[104:105], v[138:139]
	v_pk_fma_f32 v[102:103], v[120:121], v[134:135], v[102:103]
	v_pk_fma_f32 v[136:137], v[58:59], v[106:107], v[104:105] op_sel_hi:[0,1,1]
	v_pk_mul_f32 v[104:105], v[118:119], v[140:141]
	v_pk_mul_f32 v[106:107], v[54:55], v[8:9] op_sel_hi:[0,1]
	v_pk_fma_f32 v[138:139], v[58:59], v[108:109], v[104:105] op_sel_hi:[0,1,1]
	v_pk_mul_f32 v[104:105], v[54:55], v[6:7] op_sel_hi:[0,1]
	v_exp_f32_e32 v104, v104
	v_exp_f32_e32 v105, v105
	v_exp_f32_e32 v106, v106
	v_exp_f32_e32 v107, v107
	s_waitcnt lgkmcnt(11)
	v_pk_fma_f32 v[102:103], v[122:123], v[136:137], v[102:103]
	v_pk_mul_f32 v[104:105], v[104:105], v[142:143]
	v_pk_fma_f32 v[102:103], v[124:125], v[138:139], v[102:103]
	v_pk_fma_f32 v[140:141], v[58:59], v[110:111], v[104:105] op_sel_hi:[0,1,1]
	v_pk_mul_f32 v[104:105], v[106:107], v[144:145]
	v_pk_mul_f32 v[106:107], v[54:55], v[4:5] op_sel_hi:[0,1]
	v_pk_fma_f32 v[142:143], v[58:59], v[112:113], v[104:105] op_sel_hi:[0,1,1]
	v_pk_mul_f32 v[104:105], v[54:55], v[2:3] op_sel_hi:[0,1]
	v_exp_f32_e32 v104, v104
	v_exp_f32_e32 v105, v105
	v_exp_f32_e32 v106, v106
	v_exp_f32_e32 v107, v107
	s_waitcnt lgkmcnt(10)
	v_pk_fma_f32 v[102:103], v[126:127], v[140:141], v[102:103]
	v_pk_mul_f32 v[104:105], v[104:105], v[146:147]
	v_pk_fma_f32 v[102:103], v[128:129], v[142:143], v[102:103]
	v_pk_fma_f32 v[144:145], v[58:59], v[114:115], v[104:105] op_sel_hi:[0,1,1]
	v_pk_mul_f32 v[104:105], v[106:107], v[148:149]
	s_waitcnt lgkmcnt(9)
	v_pk_fma_f32 v[102:103], v[130:131], v[144:145], v[102:103]
	v_pk_fma_f32 v[146:147], v[58:59], v[116:117], v[104:105] op_sel_hi:[0,1,1]
	v_pk_fma_f32 v[102:103], v[132:133], v[146:147], v[102:103]
	s_nop 0
	v_add_f32_e32 v54, v102, v103
	v_fma_mix_f32 v54, v1, v55, v54 op_sel:[0,1,0] op_sel_hi:[0,1,0]
	v_fma_mixlo_f16 v54, v54, v59, 0 op_sel:[0,1,0] op_sel_hi:[0,1,0]
	ds_write_b16 v68, v54 offset:7216
	ds_read_b128 v[102:105], v67 offset:640
	ds_read_b128 v[106:109], v67 offset:656
	ds_read_b128 v[110:113], v67 offset:672
	ds_read_b128 v[114:117], v67 offset:688
	ds_read_b128 v[118:121], v67 offset:704
	ds_read_b128 v[122:125], v67 offset:720
	ds_read_b128 v[126:129], v67 offset:736
	ds_read_b128 v[130:133], v67 offset:752
	v_cvt_f32_f16_e32 v54, v64
	v_cvt_f32_f16_e32 v55, v56
	v_pk_mul_f32 v[148:149], v[54:55], v[14:15] op_sel_hi:[0,1]
	v_exp_f32_e32 v148, v148
	v_exp_f32_e32 v149, v149
	v_pk_mul_f32 v[150:151], v[54:55], v[16:17] op_sel_hi:[0,1]
	v_exp_f32_e32 v150, v150
	v_exp_f32_e32 v151, v151
	v_mul_f32_e32 v58, v54, v55
	v_pk_mul_f32 v[62:63], v[148:149], v[62:63]
	s_waitcnt lgkmcnt(14)
	v_pk_fma_f32 v[62:63], v[58:59], v[70:71], v[62:63] op_sel_hi:[0,1,1]
	s_waitcnt lgkmcnt(12)
	v_pk_fma_f32 v[70:71], v[86:87], v[62:63], 0 op_sel_hi:[1,1,0]
	v_pk_mul_f32 v[86:87], v[150:151], v[134:135]
	s_nop 0
	v_pk_fma_f32 v[134:135], v[58:59], v[72:73], v[86:87] op_sel_hi:[0,1,1]
	v_pk_mul_f32 v[72:73], v[54:55], v[10:11] op_sel_hi:[0,1]
	v_exp_f32_e32 v72, v72
	v_exp_f32_e32 v73, v73
	v_pk_mul_f32 v[86:87], v[54:55], v[12:13] op_sel_hi:[0,1]
	v_exp_f32_e32 v86, v86
	v_exp_f32_e32 v87, v87
	v_pk_mul_f32 v[72:73], v[72:73], v[136:137]
	v_pk_fma_f32 v[70:71], v[88:89], v[134:135], v[70:71]
	v_pk_fma_f32 v[136:137], v[58:59], v[74:75], v[72:73] op_sel_hi:[0,1,1]
	v_pk_mul_f32 v[72:73], v[86:87], v[138:139]
	v_pk_mul_f32 v[74:75], v[54:55], v[8:9] op_sel_hi:[0,1]
	v_pk_fma_f32 v[138:139], v[58:59], v[76:77], v[72:73] op_sel_hi:[0,1,1]
	v_pk_mul_f32 v[72:73], v[54:55], v[6:7] op_sel_hi:[0,1]
	v_exp_f32_e32 v72, v72
	v_exp_f32_e32 v73, v73
	v_exp_f32_e32 v74, v74
	v_exp_f32_e32 v75, v75
	s_waitcnt lgkmcnt(11)
	v_pk_fma_f32 v[70:71], v[90:91], v[136:137], v[70:71]
	v_pk_mul_f32 v[72:73], v[72:73], v[140:141]
	v_pk_fma_f32 v[70:71], v[92:93], v[138:139], v[70:71]
	v_pk_fma_f32 v[140:141], v[58:59], v[78:79], v[72:73] op_sel_hi:[0,1,1]
	v_pk_mul_f32 v[72:73], v[74:75], v[142:143]
	s_waitcnt lgkmcnt(10)
	v_pk_fma_f32 v[70:71], v[94:95], v[140:141], v[70:71]
	v_pk_fma_f32 v[142:143], v[58:59], v[80:81], v[72:73] op_sel_hi:[0,1,1]
	v_pk_mul_f32 v[72:73], v[54:55], v[2:3] op_sel_hi:[0,1]
	v_exp_f32_e32 v72, v72
	v_exp_f32_e32 v73, v73
	v_pk_mul_f32 v[54:55], v[54:55], v[4:5] op_sel_hi:[0,1]
	v_exp_f32_e32 v54, v54
	v_exp_f32_e32 v55, v55
	v_pk_mul_f32 v[72:73], v[72:73], v[144:145]
	v_pk_fma_f32 v[70:71], v[96:97], v[142:143], v[70:71]
	v_pk_fma_f32 v[144:145], v[58:59], v[82:83], v[72:73] op_sel_hi:[0,1,1]
	v_pk_mul_f32 v[54:55], v[54:55], v[146:147]
	s_waitcnt lgkmcnt(9)
	v_pk_fma_f32 v[70:71], v[98:99], v[144:145], v[70:71]
	v_pk_fma_f32 v[54:55], v[58:59], v[84:85], v[54:55] op_sel_hi:[0,1,1]
	v_pk_fma_f32 v[58:59], v[100:101], v[54:55], v[70:71]
	s_nop 0
	v_add_f32_e32 v58, v58, v59
	v_fma_mix_f32 v58, v1, v56, v58 op_sel_hi:[0,1,0]
	v_fma_mixlo_f16 v58, v58, v60, 0 op_sel_hi:[0,1,0]
	ds_write_b16 v68, v58 offset:8256
	ds_read_b128 v[70:73], v67 offset:768
	ds_read_b128 v[74:77], v67 offset:784
	ds_read_b128 v[78:81], v67 offset:800
	ds_read_b128 v[82:85], v67 offset:816
	ds_read_b128 v[86:89], v67 offset:832
	ds_read_b128 v[90:93], v67 offset:848
	ds_read_b128 v[94:97], v67 offset:864
	ds_read_b128 v[98:101], v67 offset:880
	v_cvt_f32_f16_sdwa v58, v64 dst_sel:DWORD dst_unused:UNUSED_PAD src0_sel:WORD_1
	v_cvt_f32_f16_sdwa v59, v56 dst_sel:DWORD dst_unused:UNUSED_PAD src0_sel:WORD_1
	v_pk_mul_f32 v[146:147], v[58:59], v[14:15] op_sel_hi:[0,1]
	v_exp_f32_e32 v146, v146
	v_exp_f32_e32 v147, v147
	v_pk_mul_f32 v[148:149], v[58:59], v[16:17] op_sel_hi:[0,1]
	v_exp_f32_e32 v148, v148
	v_exp_f32_e32 v149, v149
	v_mul_f32_e32 v64, v58, v59
	v_pk_mul_f32 v[62:63], v[146:147], v[62:63]
	s_waitcnt lgkmcnt(14)
	v_pk_fma_f32 v[62:63], v[64:65], v[102:103], v[62:63] op_sel_hi:[0,1,1]
	s_waitcnt lgkmcnt(12)
	v_pk_fma_f32 v[102:103], v[118:119], v[62:63], 0 op_sel_hi:[1,1,0]
	v_pk_mul_f32 v[118:119], v[148:149], v[134:135]
	s_nop 0
	v_pk_fma_f32 v[134:135], v[64:65], v[104:105], v[118:119] op_sel_hi:[0,1,1]
	v_pk_mul_f32 v[104:105], v[58:59], v[10:11] op_sel_hi:[0,1]
	v_exp_f32_e32 v104, v104
	v_exp_f32_e32 v105, v105
	v_pk_mul_f32 v[118:119], v[58:59], v[12:13] op_sel_hi:[0,1]
	v_exp_f32_e32 v118, v118
	v_exp_f32_e32 v119, v119
	v_pk_mul_f32 v[104:105], v[104:105], v[136:137]
	v_pk_fma_f32 v[102:103], v[120:121], v[134:135], v[102:103]
	v_pk_fma_f32 v[136:137], v[64:65], v[106:107], v[104:105] op_sel_hi:[0,1,1]
	v_pk_mul_f32 v[104:105], v[118:119], v[138:139]
	v_pk_mul_f32 v[106:107], v[58:59], v[8:9] op_sel_hi:[0,1]
	v_pk_fma_f32 v[138:139], v[64:65], v[108:109], v[104:105] op_sel_hi:[0,1,1]
	v_pk_mul_f32 v[104:105], v[58:59], v[6:7] op_sel_hi:[0,1]
	v_exp_f32_e32 v104, v104
	v_exp_f32_e32 v105, v105
	v_exp_f32_e32 v106, v106
	v_exp_f32_e32 v107, v107
	s_waitcnt lgkmcnt(11)
	v_pk_fma_f32 v[102:103], v[122:123], v[136:137], v[102:103]
	v_pk_mul_f32 v[104:105], v[104:105], v[140:141]
	v_pk_fma_f32 v[102:103], v[124:125], v[138:139], v[102:103]
	v_pk_fma_f32 v[140:141], v[64:65], v[110:111], v[104:105] op_sel_hi:[0,1,1]
	v_pk_mul_f32 v[104:105], v[106:107], v[142:143]
	s_waitcnt lgkmcnt(10)
	v_pk_fma_f32 v[102:103], v[126:127], v[140:141], v[102:103]
	v_pk_fma_f32 v[142:143], v[64:65], v[112:113], v[104:105] op_sel_hi:[0,1,1]
	v_pk_mul_f32 v[104:105], v[58:59], v[2:3] op_sel_hi:[0,1]
	v_exp_f32_e32 v104, v104
	v_exp_f32_e32 v105, v105
	v_pk_mul_f32 v[58:59], v[58:59], v[4:5] op_sel_hi:[0,1]
	v_exp_f32_e32 v58, v58
	v_exp_f32_e32 v59, v59
	v_pk_mul_f32 v[104:105], v[104:105], v[144:145]
	v_pk_fma_f32 v[102:103], v[128:129], v[142:143], v[102:103]
	v_pk_fma_f32 v[144:145], v[64:65], v[114:115], v[104:105] op_sel_hi:[0,1,1]
	v_pk_mul_f32 v[54:55], v[58:59], v[54:55]
	s_waitcnt lgkmcnt(9)
	v_pk_fma_f32 v[102:103], v[130:131], v[144:145], v[102:103]
	v_pk_fma_f32 v[54:55], v[64:65], v[116:117], v[54:55] op_sel_hi:[0,1,1]
	v_pk_fma_f32 v[58:59], v[132:133], v[54:55], v[102:103]
	s_nop 0
	v_add_f32_e32 v58, v58, v59
	v_fma_mix_f32 v56, v1, v56, v58 op_sel:[0,1,0] op_sel_hi:[0,1,0]
	v_fma_mixlo_f16 v56, v56, v60, 0 op_sel:[0,1,0] op_sel_hi:[0,1,0]
	ds_write_b16 v68, v56 offset:9296
	ds_read_b128 v[102:105], v67 offset:896
	ds_read_b128 v[106:109], v67 offset:912
	ds_read_b128 v[110:113], v67 offset:928
	ds_read_b128 v[114:117], v67 offset:944
	ds_read_b128 v[118:121], v67 offset:960
	ds_read_b128 v[122:125], v67 offset:976
	ds_read_b128 v[126:129], v67 offset:992
	ds_read_b128 v[130:133], v67 offset:1008
	v_cvt_f32_f16_e32 v56, v65
	v_cvt_f32_f16_e32 v58, v57
	v_pk_mul_f32 v[146:147], v[56:57], v[14:15] op_sel_hi:[0,1]
	v_exp_f32_e32 v146, v146
	v_exp_f32_e32 v147, v147
	v_pk_mul_f32 v[148:149], v[56:57], v[16:17] op_sel_hi:[0,1]
	v_exp_f32_e32 v148, v148
	v_exp_f32_e32 v149, v149
	v_mul_f32_e32 v58, v56, v58
	v_pk_mul_f32 v[62:63], v[146:147], v[62:63]
	s_waitcnt lgkmcnt(14)
	v_pk_fma_f32 v[62:63], v[58:59], v[70:71], v[62:63] op_sel_hi:[0,1,1]
	s_waitcnt lgkmcnt(12)
	v_pk_fma_f32 v[70:71], v[86:87], v[62:63], 0 op_sel_hi:[1,1,0]
	v_pk_mul_f32 v[86:87], v[148:149], v[134:135]
	s_nop 0
	v_pk_fma_f32 v[134:135], v[58:59], v[72:73], v[86:87] op_sel_hi:[0,1,1]
	v_pk_mul_f32 v[72:73], v[56:57], v[10:11] op_sel_hi:[0,1]
	v_exp_f32_e32 v72, v72
	v_exp_f32_e32 v73, v73
	v_pk_mul_f32 v[86:87], v[56:57], v[12:13] op_sel_hi:[0,1]
	v_exp_f32_e32 v86, v86
	v_exp_f32_e32 v87, v87
	v_pk_mul_f32 v[72:73], v[72:73], v[136:137]
	v_pk_fma_f32 v[70:71], v[88:89], v[134:135], v[70:71]
	v_pk_fma_f32 v[136:137], v[58:59], v[74:75], v[72:73] op_sel_hi:[0,1,1]
	v_pk_mul_f32 v[72:73], v[86:87], v[138:139]
	v_pk_mul_f32 v[74:75], v[56:57], v[8:9] op_sel_hi:[0,1]
	v_pk_fma_f32 v[138:139], v[58:59], v[76:77], v[72:73] op_sel_hi:[0,1,1]
	v_pk_mul_f32 v[72:73], v[56:57], v[6:7] op_sel_hi:[0,1]
	v_exp_f32_e32 v72, v72
	v_exp_f32_e32 v73, v73
	v_exp_f32_e32 v74, v74
	v_exp_f32_e32 v75, v75
	s_waitcnt lgkmcnt(11)
	v_pk_fma_f32 v[70:71], v[90:91], v[136:137], v[70:71]
	v_pk_mul_f32 v[72:73], v[72:73], v[140:141]
	v_pk_fma_f32 v[70:71], v[92:93], v[138:139], v[70:71]
	v_pk_fma_f32 v[140:141], v[58:59], v[78:79], v[72:73] op_sel_hi:[0,1,1]
	v_pk_mul_f32 v[72:73], v[74:75], v[142:143]
	v_pk_mul_f32 v[74:75], v[56:57], v[4:5] op_sel_hi:[0,1]
	v_pk_fma_f32 v[142:143], v[58:59], v[80:81], v[72:73] op_sel_hi:[0,1,1]
	v_pk_mul_f32 v[72:73], v[56:57], v[2:3] op_sel_hi:[0,1]
	v_exp_f32_e32 v72, v72
	v_exp_f32_e32 v73, v73
	v_exp_f32_e32 v74, v74
	v_exp_f32_e32 v75, v75
	s_waitcnt lgkmcnt(10)
	v_pk_fma_f32 v[70:71], v[94:95], v[140:141], v[70:71]
	v_pk_mul_f32 v[72:73], v[72:73], v[144:145]
	v_pk_fma_f32 v[70:71], v[96:97], v[142:143], v[70:71]
	v_pk_fma_f32 v[144:145], v[58:59], v[82:83], v[72:73] op_sel_hi:[0,1,1]
	v_pk_mul_f32 v[54:55], v[74:75], v[54:55]
	s_waitcnt lgkmcnt(9)
	v_pk_fma_f32 v[70:71], v[98:99], v[144:145], v[70:71]
	v_pk_fma_f32 v[54:55], v[58:59], v[84:85], v[54:55] op_sel_hi:[0,1,1]
	v_pk_fma_f32 v[58:59], v[100:101], v[54:55], v[70:71]
	s_nop 0
	v_add_f32_e32 v56, v58, v59
	v_fma_mix_f32 v56, v1, v57, v56 op_sel_hi:[0,1,0]
	v_fma_mixlo_f16 v56, v56, v61, 0 op_sel_hi:[0,1,0]
	ds_write_b16 v68, v56 offset:10336
	ds_read_b128 v[70:73], v67 offset:1024
	ds_read_b128 v[74:77], v67 offset:1040
	ds_read_b128 v[78:81], v67 offset:1056
	ds_read_b128 v[82:85], v67 offset:1072
	ds_read_b128 v[86:89], v67 offset:1088
	ds_read_b128 v[90:93], v67 offset:1104
	ds_read_b128 v[94:97], v67 offset:1120
	ds_read_b128 v[98:101], v67 offset:1136
	v_cvt_f32_f16_sdwa v56, v65 dst_sel:DWORD dst_unused:UNUSED_PAD src0_sel:WORD_1
	v_cvt_f32_f16_sdwa v58, v57 dst_sel:DWORD dst_unused:UNUSED_PAD src0_sel:WORD_1
	v_pk_mul_f32 v[64:65], v[56:57], v[14:15] op_sel_hi:[0,1]
	v_pk_mul_f32 v[146:147], v[56:57], v[16:17] op_sel_hi:[0,1]
	v_exp_f32_e32 v64, v64
	v_exp_f32_e32 v65, v65
	v_exp_f32_e32 v146, v146
	v_exp_f32_e32 v147, v147
	v_mul_f32_e32 v58, v56, v58
	v_pk_mul_f32 v[62:63], v[64:65], v[62:63]
	v_pk_mul_f32 v[64:65], v[146:147], v[134:135]
	s_waitcnt lgkmcnt(14)
	v_pk_fma_f32 v[134:135], v[58:59], v[104:105], v[64:65] op_sel_hi:[0,1,1]
	v_pk_mul_f32 v[64:65], v[56:57], v[10:11] op_sel_hi:[0,1]
	v_pk_fma_f32 v[148:149], v[58:59], v[102:103], v[62:63] op_sel_hi:[0,1,1]
	v_exp_f32_e32 v64, v64
	v_exp_f32_e32 v65, v65
	v_pk_mul_f32 v[102:103], v[56:57], v[12:13] op_sel_hi:[0,1]
	v_exp_f32_e32 v102, v102
	v_exp_f32_e32 v103, v103
	s_waitcnt lgkmcnt(12)
	v_pk_fma_f32 v[62:63], v[118:119], v[148:149], 0 op_sel_hi:[1,1,0]
	v_pk_mul_f32 v[64:65], v[64:65], v[136:137]
	v_pk_fma_f32 v[62:63], v[120:121], v[134:135], v[62:63]
	v_pk_fma_f32 v[136:137], v[58:59], v[106:107], v[64:65] op_sel_hi:[0,1,1]
	v_pk_mul_f32 v[64:65], v[102:103], v[138:139]
	s_waitcnt lgkmcnt(11)
	v_pk_fma_f32 v[62:63], v[122:123], v[136:137], v[62:63]
	v_pk_fma_f32 v[122:123], v[58:59], v[108:109], v[64:65] op_sel_hi:[0,1,1]
	v_pk_mul_f32 v[64:65], v[56:57], v[6:7] op_sel_hi:[0,1]
	v_exp_f32_e32 v64, v64
	v_exp_f32_e32 v65, v65
	v_pk_mul_f32 v[102:103], v[56:57], v[8:9] op_sel_hi:[0,1]
	v_exp_f32_e32 v102, v102
	v_exp_f32_e32 v103, v103
	v_pk_mul_f32 v[64:65], v[64:65], v[140:141]
	v_pk_fma_f32 v[62:63], v[124:125], v[122:123], v[62:63]
	v_pk_fma_f32 v[124:125], v[58:59], v[110:111], v[64:65] op_sel_hi:[0,1,1]
	v_pk_mul_f32 v[64:65], v[102:103], v[142:143]
	s_waitcnt lgkmcnt(10)
	v_pk_fma_f32 v[62:63], v[126:127], v[124:125], v[62:63]
	v_pk_fma_f32 v[126:127], v[58:59], v[112:113], v[64:65] op_sel_hi:[0,1,1]
	v_pk_mul_f32 v[64:65], v[56:57], v[2:3] op_sel_hi:[0,1]
	v_exp_f32_e32 v64, v64
	v_exp_f32_e32 v65, v65
	v_pk_mul_f32 v[102:103], v[56:57], v[4:5] op_sel_hi:[0,1]
	v_exp_f32_e32 v102, v102
	v_exp_f32_e32 v103, v103
	v_pk_mul_f32 v[64:65], v[64:65], v[144:145]
	v_pk_fma_f32 v[62:63], v[128:129], v[126:127], v[62:63]
	v_pk_fma_f32 v[128:129], v[58:59], v[114:115], v[64:65] op_sel_hi:[0,1,1]
	v_pk_mul_f32 v[54:55], v[102:103], v[54:55]
	s_waitcnt lgkmcnt(9)
	v_pk_fma_f32 v[62:63], v[130:131], v[128:129], v[62:63]
	v_pk_fma_f32 v[130:131], v[58:59], v[116:117], v[54:55] op_sel_hi:[0,1,1]
	v_pk_fma_f32 v[54:55], v[132:133], v[130:131], v[62:63]
	s_nop 0
	v_add_f32_e32 v54, v54, v55
	v_fma_mix_f32 v54, v1, v57, v54 op_sel:[0,1,0] op_sel_hi:[0,1,0]
	v_fma_mixlo_f16 v54, v54, v61, 0 op_sel:[0,1,0] op_sel_hi:[0,1,0]
	ds_write_b16 v68, v54 offset:11376
	ds_read_b128 v[54:57], v67 offset:1152
	ds_read_b128 v[58:61], v67 offset:1168
	ds_read_b128 v[62:65], v67 offset:1184
	ds_read_b128 v[102:105], v67 offset:1200
	ds_read_b128 v[106:109], v67 offset:1216
	ds_read_b128 v[110:113], v67 offset:1232
	ds_read_b128 v[114:117], v67 offset:1248
	ds_read_b128 v[118:121], v67 offset:1264
	s_waitcnt vmcnt(8)
	v_cvt_f32_f16_e32 v132, v50
	s_waitcnt vmcnt(7)
	v_cvt_f32_f16_e32 v69, v42
	v_pk_mul_f32 v[140:141], v[132:133], v[14:15] op_sel_hi:[0,1]
	v_exp_f32_e32 v140, v140
	v_exp_f32_e32 v141, v141
	v_pk_mul_f32 v[142:143], v[132:133], v[16:17] op_sel_hi:[0,1]
	v_exp_f32_e32 v142, v142
	v_exp_f32_e32 v143, v143
	v_mul_f32_e32 v138, v132, v69
	v_pk_mul_f32 v[140:141], v[140:141], v[148:149]
	s_waitcnt lgkmcnt(14)
	v_pk_fma_f32 v[140:141], v[138:139], v[70:71], v[140:141] op_sel_hi:[0,1,1]
	s_waitcnt lgkmcnt(12)
	v_pk_fma_f32 v[70:71], v[86:87], v[140:141], 0 op_sel_hi:[1,1,0]
	v_pk_mul_f32 v[86:87], v[142:143], v[134:135]
	s_nop 0
	v_pk_fma_f32 v[134:135], v[138:139], v[72:73], v[86:87] op_sel_hi:[0,1,1]
	v_pk_mul_f32 v[72:73], v[132:133], v[10:11] op_sel_hi:[0,1]
	v_exp_f32_e32 v72, v72
	v_exp_f32_e32 v73, v73
	v_pk_mul_f32 v[86:87], v[132:133], v[12:13] op_sel_hi:[0,1]
	v_exp_f32_e32 v86, v86
	v_exp_f32_e32 v87, v87
	v_pk_mul_f32 v[72:73], v[72:73], v[136:137]
	v_pk_fma_f32 v[70:71], v[88:89], v[134:135], v[70:71]
	v_pk_fma_f32 v[136:137], v[138:139], v[74:75], v[72:73] op_sel_hi:[0,1,1]
	v_pk_mul_f32 v[72:73], v[86:87], v[122:123]
	v_pk_mul_f32 v[74:75], v[132:133], v[8:9] op_sel_hi:[0,1]
	v_pk_fma_f32 v[122:123], v[138:139], v[76:77], v[72:73] op_sel_hi:[0,1,1]
	v_pk_mul_f32 v[72:73], v[132:133], v[6:7] op_sel_hi:[0,1]
	v_exp_f32_e32 v72, v72
	v_exp_f32_e32 v73, v73
	v_exp_f32_e32 v74, v74
	v_exp_f32_e32 v75, v75
	s_waitcnt lgkmcnt(11)
	v_pk_fma_f32 v[70:71], v[90:91], v[136:137], v[70:71]
	v_pk_mul_f32 v[72:73], v[72:73], v[124:125]
	v_pk_fma_f32 v[70:71], v[92:93], v[122:123], v[70:71]
	v_pk_fma_f32 v[124:125], v[138:139], v[78:79], v[72:73] op_sel_hi:[0,1,1]
	v_pk_mul_f32 v[72:73], v[74:75], v[126:127]
	v_pk_mul_f32 v[74:75], v[132:133], v[4:5] op_sel_hi:[0,1]
	v_pk_fma_f32 v[126:127], v[138:139], v[80:81], v[72:73] op_sel_hi:[0,1,1]
	v_pk_mul_f32 v[72:73], v[132:133], v[2:3] op_sel_hi:[0,1]
	v_exp_f32_e32 v72, v72
	v_exp_f32_e32 v73, v73
	v_exp_f32_e32 v74, v74
	v_exp_f32_e32 v75, v75
	s_waitcnt lgkmcnt(10)
	v_pk_fma_f32 v[70:71], v[94:95], v[124:125], v[70:71]
	v_pk_mul_f32 v[72:73], v[72:73], v[128:129]
	v_pk_fma_f32 v[70:71], v[96:97], v[126:127], v[70:71]
	v_pk_fma_f32 v[128:129], v[138:139], v[82:83], v[72:73] op_sel_hi:[0,1,1]
	v_pk_mul_f32 v[72:73], v[74:75], v[130:131]
	s_waitcnt lgkmcnt(9)
	v_pk_fma_f32 v[70:71], v[98:99], v[128:129], v[70:71]
	v_pk_fma_f32 v[130:131], v[138:139], v[84:85], v[72:73] op_sel_hi:[0,1,1]
	v_pk_fma_f32 v[70:71], v[100:101], v[130:131], v[70:71]
	s_nop 0
	v_add_f32_e32 v69, v70, v71
	v_fma_mix_f32 v69, v1, v42, v69 op_sel_hi:[0,1,0]
	s_waitcnt vmcnt(6)
	v_fma_mixlo_f16 v69, v69, v46, 0 op_sel_hi:[0,1,0]
	ds_write_b16 v68, v69 offset:12416
	ds_read_b128 v[70:73], v67 offset:1280
	ds_read_b128 v[74:77], v67 offset:1296
	ds_read_b128 v[78:81], v67 offset:1312
	ds_read_b128 v[82:85], v67 offset:1328
	ds_read_b128 v[86:89], v67 offset:1344
	ds_read_b128 v[90:93], v67 offset:1360
	ds_read_b128 v[94:97], v67 offset:1376
	ds_read_b128 v[98:101], v67 offset:1392
	v_cvt_f32_f16_sdwa v50, v50 dst_sel:DWORD dst_unused:UNUSED_PAD src0_sel:WORD_1
	v_cvt_f32_f16_sdwa v69, v42 dst_sel:DWORD dst_unused:UNUSED_PAD src0_sel:WORD_1
	v_pk_mul_f32 v[138:139], v[50:51], v[14:15] op_sel_hi:[0,1]
	v_exp_f32_e32 v138, v138
	v_exp_f32_e32 v139, v139
	v_pk_mul_f32 v[142:143], v[50:51], v[16:17] op_sel_hi:[0,1]
	v_exp_f32_e32 v142, v142
	v_exp_f32_e32 v143, v143
	v_mul_f32_e32 v132, v50, v69
	v_pk_mul_f32 v[138:139], v[138:139], v[140:141]
	s_waitcnt lgkmcnt(14)
	v_pk_fma_f32 v[138:139], v[132:133], v[54:55], v[138:139] op_sel_hi:[0,1,1]
	s_waitcnt lgkmcnt(12)
	v_pk_fma_f32 v[54:55], v[106:107], v[138:139], 0 op_sel_hi:[1,1,0]
	v_pk_mul_f32 v[106:107], v[142:143], v[134:135]
	s_nop 0
	v_pk_fma_f32 v[134:135], v[132:133], v[56:57], v[106:107] op_sel_hi:[0,1,1]
	v_pk_mul_f32 v[56:57], v[50:51], v[10:11] op_sel_hi:[0,1]
	v_exp_f32_e32 v56, v56
	v_exp_f32_e32 v57, v57
	v_pk_mul_f32 v[106:107], v[50:51], v[12:13] op_sel_hi:[0,1]
	v_exp_f32_e32 v106, v106
	v_exp_f32_e32 v107, v107
	v_pk_mul_f32 v[56:57], v[56:57], v[136:137]
	v_pk_fma_f32 v[54:55], v[108:109], v[134:135], v[54:55]
	v_pk_fma_f32 v[136:137], v[132:133], v[58:59], v[56:57] op_sel_hi:[0,1,1]
	v_pk_mul_f32 v[56:57], v[106:107], v[122:123]
	v_pk_mul_f32 v[58:59], v[50:51], v[8:9] op_sel_hi:[0,1]
	v_pk_fma_f32 v[122:123], v[132:133], v[60:61], v[56:57] op_sel_hi:[0,1,1]
	v_pk_mul_f32 v[56:57], v[50:51], v[6:7] op_sel_hi:[0,1]
	v_exp_f32_e32 v56, v56
	v_exp_f32_e32 v57, v57
	v_exp_f32_e32 v58, v58
	v_exp_f32_e32 v59, v59
	s_waitcnt lgkmcnt(11)
	v_pk_fma_f32 v[54:55], v[110:111], v[136:137], v[54:55]
	v_pk_mul_f32 v[56:57], v[56:57], v[124:125]
	v_pk_fma_f32 v[54:55], v[112:113], v[122:123], v[54:55]
	v_pk_fma_f32 v[124:125], v[132:133], v[62:63], v[56:57] op_sel_hi:[0,1,1]
	v_pk_mul_f32 v[56:57], v[58:59], v[126:127]
	v_pk_mul_f32 v[58:59], v[50:51], v[4:5] op_sel_hi:[0,1]
	v_pk_fma_f32 v[126:127], v[132:133], v[64:65], v[56:57] op_sel_hi:[0,1,1]
	v_pk_mul_f32 v[56:57], v[50:51], v[2:3] op_sel_hi:[0,1]
	v_exp_f32_e32 v56, v56
	v_exp_f32_e32 v57, v57
	v_exp_f32_e32 v58, v58
	v_exp_f32_e32 v59, v59
	s_waitcnt lgkmcnt(10)
	v_pk_fma_f32 v[54:55], v[114:115], v[124:125], v[54:55]
	v_pk_mul_f32 v[56:57], v[56:57], v[128:129]
	v_pk_fma_f32 v[54:55], v[116:117], v[126:127], v[54:55]
	v_pk_fma_f32 v[128:129], v[132:133], v[102:103], v[56:57] op_sel_hi:[0,1,1]
	v_pk_mul_f32 v[56:57], v[58:59], v[130:131]
	s_waitcnt lgkmcnt(9)
	v_pk_fma_f32 v[54:55], v[118:119], v[128:129], v[54:55]
	v_pk_fma_f32 v[130:131], v[132:133], v[104:105], v[56:57] op_sel_hi:[0,1,1]
	v_pk_fma_f32 v[54:55], v[120:121], v[130:131], v[54:55]
	s_nop 0
	v_add_f32_e32 v50, v54, v55
	v_fma_mix_f32 v42, v1, v42, v50 op_sel:[0,1,0] op_sel_hi:[0,1,0]
	v_fma_mixlo_f16 v42, v42, v46, 0 op_sel:[0,1,0] op_sel_hi:[0,1,0]
	ds_write_b16 v68, v42 offset:13456
	ds_read_b128 v[54:57], v67 offset:1408
	ds_read_b128 v[58:61], v67 offset:1424
	ds_read_b128 v[62:65], v67 offset:1440
	ds_read_b128 v[102:105], v67 offset:1456
	ds_read_b128 v[106:109], v67 offset:1472
	ds_read_b128 v[110:113], v67 offset:1488
	ds_read_b128 v[114:117], v67 offset:1504
	ds_read_b128 v[118:121], v67 offset:1520
	v_cvt_f32_f16_e32 v42, v51
	v_cvt_f32_f16_e32 v46, v43
	v_pk_mul_f32 v[132:133], v[42:43], v[14:15] op_sel_hi:[0,1]
	v_exp_f32_e32 v132, v132
	v_exp_f32_e32 v133, v133
	v_pk_mul_f32 v[140:141], v[42:43], v[16:17] op_sel_hi:[0,1]
	v_exp_f32_e32 v140, v140
	v_exp_f32_e32 v141, v141
	v_mul_f32_e32 v46, v42, v46
	v_pk_mul_f32 v[132:133], v[132:133], v[138:139]
	s_waitcnt lgkmcnt(14)
	v_pk_fma_f32 v[132:133], v[46:47], v[70:71], v[132:133] op_sel_hi:[0,1,1]
	s_waitcnt lgkmcnt(12)
	v_pk_fma_f32 v[70:71], v[86:87], v[132:133], 0 op_sel_hi:[1,1,0]
	v_pk_mul_f32 v[86:87], v[140:141], v[134:135]
	s_nop 0
	v_pk_fma_f32 v[134:135], v[46:47], v[72:73], v[86:87] op_sel_hi:[0,1,1]
	v_pk_mul_f32 v[72:73], v[42:43], v[10:11] op_sel_hi:[0,1]
	v_exp_f32_e32 v72, v72
	v_exp_f32_e32 v73, v73
	v_pk_mul_f32 v[86:87], v[42:43], v[12:13] op_sel_hi:[0,1]
	v_exp_f32_e32 v86, v86
	v_exp_f32_e32 v87, v87
	v_pk_mul_f32 v[72:73], v[72:73], v[136:137]
	v_pk_fma_f32 v[70:71], v[88:89], v[134:135], v[70:71]
	v_pk_fma_f32 v[136:137], v[46:47], v[74:75], v[72:73] op_sel_hi:[0,1,1]
	v_pk_mul_f32 v[72:73], v[86:87], v[122:123]
	v_pk_mul_f32 v[74:75], v[42:43], v[8:9] op_sel_hi:[0,1]
	v_pk_fma_f32 v[122:123], v[46:47], v[76:77], v[72:73] op_sel_hi:[0,1,1]
	v_pk_mul_f32 v[72:73], v[42:43], v[6:7] op_sel_hi:[0,1]
	v_exp_f32_e32 v72, v72
	v_exp_f32_e32 v73, v73
	v_exp_f32_e32 v74, v74
	v_exp_f32_e32 v75, v75
	s_waitcnt lgkmcnt(11)
	v_pk_fma_f32 v[70:71], v[90:91], v[136:137], v[70:71]
	v_pk_mul_f32 v[72:73], v[72:73], v[124:125]
	v_pk_fma_f32 v[70:71], v[92:93], v[122:123], v[70:71]
	v_pk_fma_f32 v[124:125], v[46:47], v[78:79], v[72:73] op_sel_hi:[0,1,1]
	v_pk_mul_f32 v[72:73], v[74:75], v[126:127]
	v_pk_mul_f32 v[74:75], v[42:43], v[4:5] op_sel_hi:[0,1]
	v_pk_fma_f32 v[126:127], v[46:47], v[80:81], v[72:73] op_sel_hi:[0,1,1]
	v_pk_mul_f32 v[72:73], v[42:43], v[2:3] op_sel_hi:[0,1]
	v_exp_f32_e32 v72, v72
	v_exp_f32_e32 v73, v73
	v_exp_f32_e32 v74, v74
	v_exp_f32_e32 v75, v75
	s_waitcnt lgkmcnt(10)
	v_pk_fma_f32 v[70:71], v[94:95], v[124:125], v[70:71]
	v_pk_mul_f32 v[72:73], v[72:73], v[128:129]
	v_pk_fma_f32 v[70:71], v[96:97], v[126:127], v[70:71]
	v_pk_fma_f32 v[128:129], v[46:47], v[82:83], v[72:73] op_sel_hi:[0,1,1]
	v_pk_mul_f32 v[72:73], v[74:75], v[130:131]
	s_waitcnt lgkmcnt(9)
	v_pk_fma_f32 v[70:71], v[98:99], v[128:129], v[70:71]
	v_pk_fma_f32 v[130:131], v[46:47], v[84:85], v[72:73] op_sel_hi:[0,1,1]
	v_pk_fma_f32 v[70:71], v[100:101], v[130:131], v[70:71]
	s_nop 0
	v_add_f32_e32 v42, v70, v71
	v_fma_mix_f32 v42, v1, v43, v42 op_sel_hi:[0,1,0]
	v_fma_mixlo_f16 v42, v42, v47, 0 op_sel_hi:[0,1,0]
	ds_write_b16 v68, v42 offset:14496
	ds_read_b128 v[70:73], v67 offset:1536
	ds_read_b128 v[74:77], v67 offset:1552
	ds_read_b128 v[78:81], v67 offset:1568
	ds_read_b128 v[82:85], v67 offset:1584
	ds_read_b128 v[86:89], v67 offset:1600
	ds_read_b128 v[90:93], v67 offset:1616
	ds_read_b128 v[94:97], v67 offset:1632
	ds_read_b128 v[98:101], v67 offset:1648
	v_cvt_f32_f16_sdwa v42, v51 dst_sel:DWORD dst_unused:UNUSED_PAD src0_sel:WORD_1
	v_cvt_f32_f16_sdwa v46, v43 dst_sel:DWORD dst_unused:UNUSED_PAD src0_sel:WORD_1
	v_pk_mul_f32 v[50:51], v[42:43], v[14:15] op_sel_hi:[0,1]
	v_exp_f32_e32 v50, v50
	v_exp_f32_e32 v51, v51
	v_pk_mul_f32 v[138:139], v[42:43], v[16:17] op_sel_hi:[0,1]
	v_exp_f32_e32 v138, v138
	v_exp_f32_e32 v139, v139
	v_mul_f32_e32 v46, v42, v46
	v_pk_mul_f32 v[50:51], v[50:51], v[132:133]
	s_waitcnt lgkmcnt(14)
	v_pk_fma_f32 v[50:51], v[46:47], v[54:55], v[50:51] op_sel_hi:[0,1,1]
	s_waitcnt lgkmcnt(12)
	v_pk_fma_f32 v[54:55], v[106:107], v[50:51], 0 op_sel_hi:[1,1,0]
	v_pk_mul_f32 v[106:107], v[138:139], v[134:135]
	s_nop 0
	v_pk_fma_f32 v[132:133], v[46:47], v[56:57], v[106:107] op_sel_hi:[0,1,1]
	v_pk_mul_f32 v[56:57], v[42:43], v[10:11] op_sel_hi:[0,1]
	v_exp_f32_e32 v56, v56
	v_exp_f32_e32 v57, v57
	v_pk_mul_f32 v[106:107], v[42:43], v[12:13] op_sel_hi:[0,1]
	v_exp_f32_e32 v106, v106
	v_exp_f32_e32 v107, v107
	v_pk_mul_f32 v[56:57], v[56:57], v[136:137]
	v_pk_fma_f32 v[54:55], v[108:109], v[132:133], v[54:55]
	v_pk_fma_f32 v[134:135], v[46:47], v[58:59], v[56:57] op_sel_hi:[0,1,1]
	v_pk_mul_f32 v[56:57], v[106:107], v[122:123]
	v_pk_mul_f32 v[58:59], v[42:43], v[8:9] op_sel_hi:[0,1]
	v_pk_fma_f32 v[122:123], v[46:47], v[60:61], v[56:57] op_sel_hi:[0,1,1]
	v_pk_mul_f32 v[56:57], v[42:43], v[6:7] op_sel_hi:[0,1]
	v_exp_f32_e32 v56, v56
	v_exp_f32_e32 v57, v57
	v_exp_f32_e32 v58, v58
	v_exp_f32_e32 v59, v59
	s_waitcnt lgkmcnt(11)
	v_pk_fma_f32 v[54:55], v[110:111], v[134:135], v[54:55]
	v_pk_mul_f32 v[56:57], v[56:57], v[124:125]
	v_pk_fma_f32 v[54:55], v[112:113], v[122:123], v[54:55]
	v_pk_fma_f32 v[124:125], v[46:47], v[62:63], v[56:57] op_sel_hi:[0,1,1]
	v_pk_mul_f32 v[56:57], v[58:59], v[126:127]
	v_pk_mul_f32 v[58:59], v[42:43], v[4:5] op_sel_hi:[0,1]
	v_pk_fma_f32 v[126:127], v[46:47], v[64:65], v[56:57] op_sel_hi:[0,1,1]
	v_pk_mul_f32 v[56:57], v[42:43], v[2:3] op_sel_hi:[0,1]
	v_exp_f32_e32 v56, v56
	v_exp_f32_e32 v57, v57
	v_exp_f32_e32 v58, v58
	v_exp_f32_e32 v59, v59
	s_waitcnt lgkmcnt(10)
	v_pk_fma_f32 v[54:55], v[114:115], v[124:125], v[54:55]
	v_pk_mul_f32 v[56:57], v[56:57], v[128:129]
	v_pk_fma_f32 v[54:55], v[116:117], v[126:127], v[54:55]
	v_pk_fma_f32 v[128:129], v[46:47], v[102:103], v[56:57] op_sel_hi:[0,1,1]
	v_pk_mul_f32 v[56:57], v[58:59], v[130:131]
	s_waitcnt lgkmcnt(9)
	v_pk_fma_f32 v[54:55], v[118:119], v[128:129], v[54:55]
	v_pk_fma_f32 v[130:131], v[46:47], v[104:105], v[56:57] op_sel_hi:[0,1,1]
	v_pk_fma_f32 v[54:55], v[120:121], v[130:131], v[54:55]
	s_nop 0
	v_add_f32_e32 v42, v54, v55
	v_fma_mix_f32 v42, v1, v43, v42 op_sel:[0,1,0] op_sel_hi:[0,1,0]
	v_fma_mixlo_f16 v42, v42, v47, 0 op_sel:[0,1,0] op_sel_hi:[0,1,0]
	ds_write_b16 v68, v42 offset:15536
	ds_read_b128 v[54:57], v67 offset:1664
	ds_read_b128 v[58:61], v67 offset:1680
	ds_read_b128 v[62:65], v67 offset:1696
	ds_read_b128 v[102:105], v67 offset:1712
	ds_read_b128 v[106:109], v67 offset:1728
	ds_read_b128 v[110:113], v67 offset:1744
	ds_read_b128 v[114:117], v67 offset:1760
	ds_read_b128 v[118:121], v67 offset:1776
	v_cvt_f32_f16_e32 v42, v52
	v_cvt_f32_f16_e32 v43, v44
	v_pk_mul_f32 v[136:137], v[42:43], v[14:15] op_sel_hi:[0,1]
	v_exp_f32_e32 v136, v136
	v_exp_f32_e32 v137, v137
	v_pk_mul_f32 v[138:139], v[42:43], v[16:17] op_sel_hi:[0,1]
	v_exp_f32_e32 v138, v138
	v_exp_f32_e32 v139, v139
	v_mul_f32_e32 v46, v42, v43
	v_pk_mul_f32 v[50:51], v[136:137], v[50:51]
	s_waitcnt lgkmcnt(14)
	v_pk_fma_f32 v[50:51], v[46:47], v[70:71], v[50:51] op_sel_hi:[0,1,1]
	s_waitcnt lgkmcnt(12)
	v_pk_fma_f32 v[70:71], v[86:87], v[50:51], 0 op_sel_hi:[1,1,0]
	v_pk_mul_f32 v[86:87], v[138:139], v[132:133]
	s_nop 0
	v_pk_fma_f32 v[132:133], v[46:47], v[72:73], v[86:87] op_sel_hi:[0,1,1]
	v_pk_mul_f32 v[72:73], v[42:43], v[10:11] op_sel_hi:[0,1]
	v_exp_f32_e32 v72, v72
	v_exp_f32_e32 v73, v73
	v_pk_mul_f32 v[86:87], v[42:43], v[12:13] op_sel_hi:[0,1]
	v_exp_f32_e32 v86, v86
	v_exp_f32_e32 v87, v87
	v_pk_mul_f32 v[72:73], v[72:73], v[134:135]
	v_pk_fma_f32 v[70:71], v[88:89], v[132:133], v[70:71]
	v_pk_fma_f32 v[134:135], v[46:47], v[74:75], v[72:73] op_sel_hi:[0,1,1]
	v_pk_mul_f32 v[72:73], v[86:87], v[122:123]
	v_pk_mul_f32 v[74:75], v[42:43], v[8:9] op_sel_hi:[0,1]
	v_pk_fma_f32 v[122:123], v[46:47], v[76:77], v[72:73] op_sel_hi:[0,1,1]
	v_pk_mul_f32 v[72:73], v[42:43], v[6:7] op_sel_hi:[0,1]
	v_exp_f32_e32 v72, v72
	v_exp_f32_e32 v73, v73
	v_exp_f32_e32 v74, v74
	v_exp_f32_e32 v75, v75
	s_waitcnt lgkmcnt(11)
	v_pk_fma_f32 v[70:71], v[90:91], v[134:135], v[70:71]
	v_pk_mul_f32 v[72:73], v[72:73], v[124:125]
	v_pk_fma_f32 v[70:71], v[92:93], v[122:123], v[70:71]
	v_pk_fma_f32 v[124:125], v[46:47], v[78:79], v[72:73] op_sel_hi:[0,1,1]
	v_pk_mul_f32 v[72:73], v[74:75], v[126:127]
	s_waitcnt lgkmcnt(10)
	v_pk_fma_f32 v[70:71], v[94:95], v[124:125], v[70:71]
	v_pk_fma_f32 v[126:127], v[46:47], v[80:81], v[72:73] op_sel_hi:[0,1,1]
	v_pk_mul_f32 v[72:73], v[42:43], v[2:3] op_sel_hi:[0,1]
	v_exp_f32_e32 v72, v72
	v_exp_f32_e32 v73, v73
	v_pk_mul_f32 v[42:43], v[42:43], v[4:5] op_sel_hi:[0,1]
	v_exp_f32_e32 v42, v42
	v_exp_f32_e32 v43, v43
	v_pk_mul_f32 v[72:73], v[72:73], v[128:129]
	v_pk_fma_f32 v[70:71], v[96:97], v[126:127], v[70:71]
	v_pk_fma_f32 v[128:129], v[46:47], v[82:83], v[72:73] op_sel_hi:[0,1,1]
	v_pk_mul_f32 v[42:43], v[42:43], v[130:131]
	s_waitcnt lgkmcnt(9)
	v_pk_fma_f32 v[70:71], v[98:99], v[128:129], v[70:71]
	v_pk_fma_f32 v[42:43], v[46:47], v[84:85], v[42:43] op_sel_hi:[0,1,1]
	v_pk_fma_f32 v[46:47], v[100:101], v[42:43], v[70:71]
	s_nop 0
	v_add_f32_e32 v46, v46, v47
	v_fma_mix_f32 v46, v1, v44, v46 op_sel_hi:[0,1,0]
	v_fma_mixlo_f16 v46, v46, v48, 0 op_sel_hi:[0,1,0]
	ds_write_b16 v68, v46 offset:16576
	ds_read_b128 v[70:73], v67 offset:1792
	ds_read_b128 v[74:77], v67 offset:1808
	ds_read_b128 v[78:81], v67 offset:1824
	ds_read_b128 v[82:85], v67 offset:1840
	ds_read_b128 v[86:89], v67 offset:1856
	ds_read_b128 v[90:93], v67 offset:1872
	ds_read_b128 v[94:97], v67 offset:1888
	ds_read_b128 v[98:101], v67 offset:1904
	v_cvt_f32_f16_sdwa v46, v52 dst_sel:DWORD dst_unused:UNUSED_PAD src0_sel:WORD_1
	v_cvt_f32_f16_sdwa v47, v44 dst_sel:DWORD dst_unused:UNUSED_PAD src0_sel:WORD_1
	v_pk_mul_f32 v[130:131], v[46:47], v[14:15] op_sel_hi:[0,1]
	v_exp_f32_e32 v130, v130
	v_exp_f32_e32 v131, v131
	v_pk_mul_f32 v[136:137], v[46:47], v[16:17] op_sel_hi:[0,1]
	v_exp_f32_e32 v136, v136
	v_exp_f32_e32 v137, v137
	v_mul_f32_e32 v52, v46, v47
	v_pk_mul_f32 v[50:51], v[130:131], v[50:51]
	s_waitcnt lgkmcnt(14)
	v_pk_fma_f32 v[50:51], v[52:53], v[54:55], v[50:51] op_sel_hi:[0,1,1]
	s_waitcnt lgkmcnt(12)
	v_pk_fma_f32 v[54:55], v[106:107], v[50:51], 0 op_sel_hi:[1,1,0]
	v_pk_mul_f32 v[106:107], v[136:137], v[132:133]
	s_nop 0
	v_pk_fma_f32 v[130:131], v[52:53], v[56:57], v[106:107] op_sel_hi:[0,1,1]
	v_pk_mul_f32 v[56:57], v[46:47], v[10:11] op_sel_hi:[0,1]
	v_exp_f32_e32 v56, v56
	v_exp_f32_e32 v57, v57
	v_pk_mul_f32 v[106:107], v[46:47], v[12:13] op_sel_hi:[0,1]
	v_exp_f32_e32 v106, v106
	v_exp_f32_e32 v107, v107
	v_pk_mul_f32 v[56:57], v[56:57], v[134:135]
	v_pk_fma_f32 v[54:55], v[108:109], v[130:131], v[54:55]
	v_pk_fma_f32 v[132:133], v[52:53], v[58:59], v[56:57] op_sel_hi:[0,1,1]
	v_pk_mul_f32 v[56:57], v[106:107], v[122:123]
	v_pk_mul_f32 v[58:59], v[46:47], v[8:9] op_sel_hi:[0,1]
	v_pk_fma_f32 v[122:123], v[52:53], v[60:61], v[56:57] op_sel_hi:[0,1,1]
	v_pk_mul_f32 v[56:57], v[46:47], v[6:7] op_sel_hi:[0,1]
	v_exp_f32_e32 v56, v56
	v_exp_f32_e32 v57, v57
	v_exp_f32_e32 v58, v58
	v_exp_f32_e32 v59, v59
	s_waitcnt lgkmcnt(11)
	v_pk_fma_f32 v[54:55], v[110:111], v[132:133], v[54:55]
	v_pk_mul_f32 v[56:57], v[56:57], v[124:125]
	v_pk_fma_f32 v[54:55], v[112:113], v[122:123], v[54:55]
	v_pk_fma_f32 v[124:125], v[52:53], v[62:63], v[56:57] op_sel_hi:[0,1,1]
	v_pk_mul_f32 v[56:57], v[58:59], v[126:127]
	s_waitcnt lgkmcnt(10)
	v_pk_fma_f32 v[54:55], v[114:115], v[124:125], v[54:55]
	v_pk_fma_f32 v[126:127], v[52:53], v[64:65], v[56:57] op_sel_hi:[0,1,1]
	v_pk_mul_f32 v[56:57], v[46:47], v[2:3] op_sel_hi:[0,1]
	v_exp_f32_e32 v56, v56
	v_exp_f32_e32 v57, v57
	v_pk_mul_f32 v[46:47], v[46:47], v[4:5] op_sel_hi:[0,1]
	v_exp_f32_e32 v46, v46
	v_exp_f32_e32 v47, v47
	v_pk_mul_f32 v[56:57], v[56:57], v[128:129]
	v_pk_fma_f32 v[54:55], v[116:117], v[126:127], v[54:55]
	v_pk_fma_f32 v[128:129], v[52:53], v[102:103], v[56:57] op_sel_hi:[0,1,1]
	v_pk_mul_f32 v[42:43], v[46:47], v[42:43]
	s_waitcnt lgkmcnt(9)
	v_pk_fma_f32 v[54:55], v[118:119], v[128:129], v[54:55]
	v_pk_fma_f32 v[42:43], v[52:53], v[104:105], v[42:43] op_sel_hi:[0,1,1]
	v_pk_fma_f32 v[46:47], v[120:121], v[42:43], v[54:55]
	s_nop 0
	v_add_f32_e32 v46, v46, v47
	v_fma_mix_f32 v44, v1, v44, v46 op_sel:[0,1,0] op_sel_hi:[0,1,0]
	v_fma_mixlo_f16 v44, v44, v48, 0 op_sel:[0,1,0] op_sel_hi:[0,1,0]
	ds_write_b16 v68, v44 offset:17616
	ds_read_b128 v[54:57], v67 offset:1920
	ds_read_b128 v[58:61], v67 offset:1936
	ds_read_b128 v[62:65], v67 offset:1952
	ds_read_b128 v[102:105], v67 offset:1968
	ds_read_b128 v[106:109], v67 offset:1984
	ds_read_b128 v[110:113], v67 offset:2000
	ds_read_b128 v[114:117], v67 offset:2016
	ds_read_b128 v[118:121], v67 offset:2032
	v_cvt_f32_f16_e32 v44, v53
	v_cvt_f32_f16_e32 v46, v45
	v_pk_mul_f32 v[134:135], v[44:45], v[14:15] op_sel_hi:[0,1]
	v_exp_f32_e32 v134, v134
	v_exp_f32_e32 v135, v135
	v_pk_mul_f32 v[136:137], v[44:45], v[16:17] op_sel_hi:[0,1]
	v_exp_f32_e32 v136, v136
	v_exp_f32_e32 v137, v137
	v_mul_f32_e32 v46, v44, v46
	v_pk_mul_f32 v[50:51], v[134:135], v[50:51]
	s_waitcnt lgkmcnt(14)
	v_pk_fma_f32 v[50:51], v[46:47], v[70:71], v[50:51] op_sel_hi:[0,1,1]
	s_waitcnt lgkmcnt(12)
	v_pk_fma_f32 v[70:71], v[86:87], v[50:51], 0 op_sel_hi:[1,1,0]
	v_pk_mul_f32 v[86:87], v[136:137], v[130:131]
	s_nop 0
	v_pk_fma_f32 v[130:131], v[46:47], v[72:73], v[86:87] op_sel_hi:[0,1,1]
	v_pk_mul_f32 v[72:73], v[44:45], v[10:11] op_sel_hi:[0,1]
	v_exp_f32_e32 v72, v72
	v_exp_f32_e32 v73, v73
	v_pk_mul_f32 v[86:87], v[44:45], v[12:13] op_sel_hi:[0,1]
	v_exp_f32_e32 v86, v86
	v_exp_f32_e32 v87, v87
	v_pk_mul_f32 v[72:73], v[72:73], v[132:133]
	v_pk_fma_f32 v[70:71], v[88:89], v[130:131], v[70:71]
	v_pk_fma_f32 v[132:133], v[46:47], v[74:75], v[72:73] op_sel_hi:[0,1,1]
	v_pk_mul_f32 v[72:73], v[86:87], v[122:123]
	v_pk_mul_f32 v[74:75], v[44:45], v[8:9] op_sel_hi:[0,1]
	v_pk_fma_f32 v[122:123], v[46:47], v[76:77], v[72:73] op_sel_hi:[0,1,1]
	v_pk_mul_f32 v[72:73], v[44:45], v[6:7] op_sel_hi:[0,1]
	v_exp_f32_e32 v72, v72
	v_exp_f32_e32 v73, v73
	v_exp_f32_e32 v74, v74
	v_exp_f32_e32 v75, v75
	s_waitcnt lgkmcnt(11)
	v_pk_fma_f32 v[70:71], v[90:91], v[132:133], v[70:71]
	v_pk_mul_f32 v[72:73], v[72:73], v[124:125]
	v_pk_fma_f32 v[70:71], v[92:93], v[122:123], v[70:71]
	v_pk_fma_f32 v[124:125], v[46:47], v[78:79], v[72:73] op_sel_hi:[0,1,1]
	v_pk_mul_f32 v[72:73], v[74:75], v[126:127]
	v_pk_mul_f32 v[74:75], v[44:45], v[4:5] op_sel_hi:[0,1]
	v_pk_fma_f32 v[126:127], v[46:47], v[80:81], v[72:73] op_sel_hi:[0,1,1]
	v_pk_mul_f32 v[72:73], v[44:45], v[2:3] op_sel_hi:[0,1]
	v_exp_f32_e32 v72, v72
	v_exp_f32_e32 v73, v73
	v_exp_f32_e32 v74, v74
	v_exp_f32_e32 v75, v75
	s_waitcnt lgkmcnt(10)
	v_pk_fma_f32 v[70:71], v[94:95], v[124:125], v[70:71]
	v_pk_mul_f32 v[72:73], v[72:73], v[128:129]
	v_pk_fma_f32 v[70:71], v[96:97], v[126:127], v[70:71]
	v_pk_fma_f32 v[128:129], v[46:47], v[82:83], v[72:73] op_sel_hi:[0,1,1]
	v_pk_mul_f32 v[42:43], v[74:75], v[42:43]
	s_waitcnt lgkmcnt(9)
	v_pk_fma_f32 v[70:71], v[98:99], v[128:129], v[70:71]
	v_pk_fma_f32 v[42:43], v[46:47], v[84:85], v[42:43] op_sel_hi:[0,1,1]
	v_pk_fma_f32 v[46:47], v[100:101], v[42:43], v[70:71]
	s_nop 0
	v_add_f32_e32 v44, v46, v47
	v_fma_mix_f32 v44, v1, v45, v44 op_sel_hi:[0,1,0]
	v_fma_mixlo_f16 v44, v44, v49, 0 op_sel_hi:[0,1,0]
	ds_write_b16 v68, v44 offset:18656
	ds_read_b128 v[70:73], v67 offset:2048
	ds_read_b128 v[74:77], v67 offset:2064
	ds_read_b128 v[78:81], v67 offset:2080
	ds_read_b128 v[82:85], v67 offset:2096
	ds_read_b128 v[86:89], v67 offset:2112
	ds_read_b128 v[90:93], v67 offset:2128
	ds_read_b128 v[94:97], v67 offset:2144
	ds_read_b128 v[98:101], v67 offset:2160
	v_cvt_f32_f16_sdwa v44, v53 dst_sel:DWORD dst_unused:UNUSED_PAD src0_sel:WORD_1
	v_cvt_f32_f16_sdwa v46, v45 dst_sel:DWORD dst_unused:UNUSED_PAD src0_sel:WORD_1
	v_pk_mul_f32 v[52:53], v[44:45], v[14:15] op_sel_hi:[0,1]
	v_pk_mul_f32 v[134:135], v[44:45], v[16:17] op_sel_hi:[0,1]
	v_exp_f32_e32 v52, v52
	v_exp_f32_e32 v53, v53
	v_exp_f32_e32 v134, v134
	v_exp_f32_e32 v135, v135
	v_mul_f32_e32 v46, v44, v46
	v_pk_mul_f32 v[50:51], v[52:53], v[50:51]
	v_pk_mul_f32 v[52:53], v[134:135], v[130:131]
	s_waitcnt lgkmcnt(14)
	v_pk_fma_f32 v[130:131], v[46:47], v[56:57], v[52:53] op_sel_hi:[0,1,1]
	v_pk_mul_f32 v[52:53], v[44:45], v[10:11] op_sel_hi:[0,1]
	v_pk_fma_f32 v[136:137], v[46:47], v[54:55], v[50:51] op_sel_hi:[0,1,1]
	v_exp_f32_e32 v52, v52
	v_exp_f32_e32 v53, v53
	v_pk_mul_f32 v[54:55], v[44:45], v[12:13] op_sel_hi:[0,1]
	v_exp_f32_e32 v54, v54
	v_exp_f32_e32 v55, v55
	s_waitcnt lgkmcnt(12)
	v_pk_fma_f32 v[50:51], v[106:107], v[136:137], 0 op_sel_hi:[1,1,0]
	v_pk_mul_f32 v[52:53], v[52:53], v[132:133]
	v_pk_fma_f32 v[50:51], v[108:109], v[130:131], v[50:51]
	v_pk_fma_f32 v[132:133], v[46:47], v[58:59], v[52:53] op_sel_hi:[0,1,1]
	v_pk_mul_f32 v[52:53], v[54:55], v[122:123]
	s_waitcnt lgkmcnt(11)
	v_pk_fma_f32 v[50:51], v[110:111], v[132:133], v[50:51]
	v_pk_fma_f32 v[110:111], v[46:47], v[60:61], v[52:53] op_sel_hi:[0,1,1]
	v_pk_mul_f32 v[52:53], v[44:45], v[6:7] op_sel_hi:[0,1]
	v_exp_f32_e32 v52, v52
	v_exp_f32_e32 v53, v53
	v_pk_mul_f32 v[54:55], v[44:45], v[8:9] op_sel_hi:[0,1]
	v_exp_f32_e32 v54, v54
	v_exp_f32_e32 v55, v55
	v_pk_mul_f32 v[52:53], v[52:53], v[124:125]
	v_pk_fma_f32 v[50:51], v[112:113], v[110:111], v[50:51]
	v_pk_fma_f32 v[112:113], v[46:47], v[62:63], v[52:53] op_sel_hi:[0,1,1]
	v_pk_mul_f32 v[52:53], v[54:55], v[126:127]
	s_waitcnt lgkmcnt(10)
	v_pk_fma_f32 v[50:51], v[114:115], v[112:113], v[50:51]
	v_pk_fma_f32 v[114:115], v[46:47], v[64:65], v[52:53] op_sel_hi:[0,1,1]
	v_pk_mul_f32 v[52:53], v[44:45], v[2:3] op_sel_hi:[0,1]
	v_exp_f32_e32 v52, v52
	v_exp_f32_e32 v53, v53
	v_pk_mul_f32 v[54:55], v[44:45], v[4:5] op_sel_hi:[0,1]
	v_exp_f32_e32 v54, v54
	v_exp_f32_e32 v55, v55
	v_pk_mul_f32 v[52:53], v[52:53], v[128:129]
	v_pk_fma_f32 v[50:51], v[116:117], v[114:115], v[50:51]
	v_pk_fma_f32 v[116:117], v[46:47], v[102:103], v[52:53] op_sel_hi:[0,1,1]
	v_pk_mul_f32 v[42:43], v[54:55], v[42:43]
	s_waitcnt lgkmcnt(9)
	v_pk_fma_f32 v[50:51], v[118:119], v[116:117], v[50:51]
	v_pk_fma_f32 v[118:119], v[46:47], v[104:105], v[42:43] op_sel_hi:[0,1,1]
	v_pk_fma_f32 v[42:43], v[120:121], v[118:119], v[50:51]
	s_nop 0
	v_add_f32_e32 v42, v42, v43
	v_fma_mix_f32 v42, v1, v45, v42 op_sel:[0,1,0] op_sel_hi:[0,1,0]
	v_fma_mixlo_f16 v42, v42, v49, 0 op_sel:[0,1,0] op_sel_hi:[0,1,0]
	ds_write_b16 v68, v42 offset:19696
	ds_read_b128 v[42:45], v67 offset:2176
	ds_read_b128 v[46:49], v67 offset:2192
	ds_read_b128 v[50:53], v67 offset:2208
	ds_read_b128 v[54:57], v67 offset:2224
	ds_read_b128 v[58:61], v67 offset:2240
	ds_read_b128 v[62:65], v67 offset:2256
	ds_read_b128 v[102:105], v67 offset:2272
	ds_read_b128 v[106:109], v67 offset:2288
	s_waitcnt vmcnt(5)
	v_cvt_f32_f16_e32 v120, v38
	s_waitcnt vmcnt(4)
	v_cvt_f32_f16_e32 v69, v30
	v_pk_mul_f32 v[124:125], v[120:121], v[14:15] op_sel_hi:[0,1]
	v_exp_f32_e32 v124, v124
	v_exp_f32_e32 v125, v125
	v_pk_mul_f32 v[126:127], v[120:121], v[16:17] op_sel_hi:[0,1]
	v_exp_f32_e32 v126, v126
	v_exp_f32_e32 v127, v127
	v_mul_f32_e32 v122, v120, v69
	v_pk_mul_f32 v[124:125], v[124:125], v[136:137]
	s_waitcnt lgkmcnt(14)
	v_pk_fma_f32 v[124:125], v[122:123], v[70:71], v[124:125] op_sel_hi:[0,1,1]
	s_waitcnt lgkmcnt(12)
	v_pk_fma_f32 v[70:71], v[86:87], v[124:125], 0 op_sel_hi:[1,1,0]
	v_pk_mul_f32 v[86:87], v[126:127], v[130:131]
	s_nop 0
	v_pk_fma_f32 v[126:127], v[122:123], v[72:73], v[86:87] op_sel_hi:[0,1,1]
	v_pk_mul_f32 v[72:73], v[120:121], v[10:11] op_sel_hi:[0,1]
	v_exp_f32_e32 v72, v72
	v_exp_f32_e32 v73, v73
	v_pk_mul_f32 v[86:87], v[120:121], v[12:13] op_sel_hi:[0,1]
	v_exp_f32_e32 v86, v86
	v_exp_f32_e32 v87, v87
	v_pk_mul_f32 v[72:73], v[72:73], v[132:133]
	v_pk_fma_f32 v[70:71], v[88:89], v[126:127], v[70:71]
	v_pk_fma_f32 v[128:129], v[122:123], v[74:75], v[72:73] op_sel_hi:[0,1,1]
	v_pk_mul_f32 v[72:73], v[86:87], v[110:111]
	v_pk_mul_f32 v[74:75], v[120:121], v[8:9] op_sel_hi:[0,1]
	v_pk_fma_f32 v[110:111], v[122:123], v[76:77], v[72:73] op_sel_hi:[0,1,1]
	v_pk_mul_f32 v[72:73], v[120:121], v[6:7] op_sel_hi:[0,1]
	v_exp_f32_e32 v72, v72
	v_exp_f32_e32 v73, v73
	v_exp_f32_e32 v74, v74
	v_exp_f32_e32 v75, v75
	s_waitcnt lgkmcnt(11)
	v_pk_fma_f32 v[70:71], v[90:91], v[128:129], v[70:71]
	v_pk_mul_f32 v[72:73], v[72:73], v[112:113]
	v_pk_fma_f32 v[70:71], v[92:93], v[110:111], v[70:71]
	v_pk_fma_f32 v[112:113], v[122:123], v[78:79], v[72:73] op_sel_hi:[0,1,1]
	v_pk_mul_f32 v[72:73], v[74:75], v[114:115]
	v_pk_mul_f32 v[74:75], v[120:121], v[4:5] op_sel_hi:[0,1]
	v_pk_fma_f32 v[114:115], v[122:123], v[80:81], v[72:73] op_sel_hi:[0,1,1]
	v_pk_mul_f32 v[72:73], v[120:121], v[2:3] op_sel_hi:[0,1]
	v_exp_f32_e32 v72, v72
	v_exp_f32_e32 v73, v73
	v_exp_f32_e32 v74, v74
	v_exp_f32_e32 v75, v75
	s_waitcnt lgkmcnt(10)
	v_pk_fma_f32 v[70:71], v[94:95], v[112:113], v[70:71]
	v_pk_mul_f32 v[72:73], v[72:73], v[116:117]
	v_pk_fma_f32 v[70:71], v[96:97], v[114:115], v[70:71]
	v_pk_fma_f32 v[116:117], v[122:123], v[82:83], v[72:73] op_sel_hi:[0,1,1]
	v_pk_mul_f32 v[72:73], v[74:75], v[118:119]
	s_waitcnt lgkmcnt(9)
	v_pk_fma_f32 v[70:71], v[98:99], v[116:117], v[70:71]
	v_pk_fma_f32 v[118:119], v[122:123], v[84:85], v[72:73] op_sel_hi:[0,1,1]
	v_pk_fma_f32 v[70:71], v[100:101], v[118:119], v[70:71]
	s_nop 0
	v_add_f32_e32 v69, v70, v71
	v_fma_mix_f32 v69, v1, v30, v69 op_sel_hi:[0,1,0]
	s_waitcnt vmcnt(3)
	v_fma_mixlo_f16 v69, v69, v34, 0 op_sel_hi:[0,1,0]
	ds_write_b16 v68, v69 offset:20736
	ds_read_b128 v[70:73], v67 offset:2304
	ds_read_b128 v[74:77], v67 offset:2320
	ds_read_b128 v[78:81], v67 offset:2336
	ds_read_b128 v[82:85], v67 offset:2352
	ds_read_b128 v[86:89], v67 offset:2368
	ds_read_b128 v[90:93], v67 offset:2384
	ds_read_b128 v[94:97], v67 offset:2400
	ds_read_b128 v[98:101], v67 offset:2416
	v_cvt_f32_f16_sdwa v38, v38 dst_sel:DWORD dst_unused:UNUSED_PAD src0_sel:WORD_1
	v_cvt_f32_f16_sdwa v69, v30 dst_sel:DWORD dst_unused:UNUSED_PAD src0_sel:WORD_1
	v_pk_mul_f32 v[122:123], v[38:39], v[14:15] op_sel_hi:[0,1]
	v_exp_f32_e32 v122, v122
	v_exp_f32_e32 v123, v123
	v_pk_mul_f32 v[130:131], v[38:39], v[16:17] op_sel_hi:[0,1]
	v_exp_f32_e32 v130, v130
	v_exp_f32_e32 v131, v131
	v_mul_f32_e32 v120, v38, v69
	v_pk_mul_f32 v[122:123], v[122:123], v[124:125]
	s_waitcnt lgkmcnt(14)
	v_pk_fma_f32 v[122:123], v[120:121], v[42:43], v[122:123] op_sel_hi:[0,1,1]
	s_waitcnt lgkmcnt(12)
	v_pk_fma_f32 v[42:43], v[58:59], v[122:123], 0 op_sel_hi:[1,1,0]
	v_pk_mul_f32 v[58:59], v[130:131], v[126:127]
	s_nop 0
	v_pk_fma_f32 v[124:125], v[120:121], v[44:45], v[58:59] op_sel_hi:[0,1,1]
	v_pk_mul_f32 v[44:45], v[38:39], v[10:11] op_sel_hi:[0,1]
	v_exp_f32_e32 v44, v44
	v_exp_f32_e32 v45, v45
	v_pk_mul_f32 v[58:59], v[38:39], v[12:13] op_sel_hi:[0,1]
	v_exp_f32_e32 v58, v58
	v_exp_f32_e32 v59, v59
	v_pk_mul_f32 v[44:45], v[44:45], v[128:129]
	v_pk_fma_f32 v[42:43], v[60:61], v[124:125], v[42:43]
	v_pk_fma_f32 v[126:127], v[120:121], v[46:47], v[44:45] op_sel_hi:[0,1,1]
	v_pk_mul_f32 v[44:45], v[58:59], v[110:111]
	v_pk_mul_f32 v[46:47], v[38:39], v[8:9] op_sel_hi:[0,1]
	v_pk_fma_f32 v[110:111], v[120:121], v[48:49], v[44:45] op_sel_hi:[0,1,1]
	v_pk_mul_f32 v[44:45], v[38:39], v[6:7] op_sel_hi:[0,1]
	v_exp_f32_e32 v44, v44
	v_exp_f32_e32 v45, v45
	v_exp_f32_e32 v46, v46
	v_exp_f32_e32 v47, v47
	s_waitcnt lgkmcnt(11)
	v_pk_fma_f32 v[42:43], v[62:63], v[126:127], v[42:43]
	v_pk_mul_f32 v[44:45], v[44:45], v[112:113]
	v_pk_fma_f32 v[42:43], v[64:65], v[110:111], v[42:43]
	v_pk_fma_f32 v[112:113], v[120:121], v[50:51], v[44:45] op_sel_hi:[0,1,1]
	v_pk_mul_f32 v[44:45], v[46:47], v[114:115]
	v_pk_mul_f32 v[46:47], v[38:39], v[4:5] op_sel_hi:[0,1]
	v_pk_fma_f32 v[114:115], v[120:121], v[52:53], v[44:45] op_sel_hi:[0,1,1]
	v_pk_mul_f32 v[44:45], v[38:39], v[2:3] op_sel_hi:[0,1]
	v_exp_f32_e32 v44, v44
	v_exp_f32_e32 v45, v45
	v_exp_f32_e32 v46, v46
	v_exp_f32_e32 v47, v47
	s_waitcnt lgkmcnt(10)
	v_pk_fma_f32 v[42:43], v[102:103], v[112:113], v[42:43]
	v_pk_mul_f32 v[44:45], v[44:45], v[116:117]
	v_pk_fma_f32 v[42:43], v[104:105], v[114:115], v[42:43]
	v_pk_fma_f32 v[116:117], v[120:121], v[54:55], v[44:45] op_sel_hi:[0,1,1]
	v_pk_mul_f32 v[44:45], v[46:47], v[118:119]
	s_waitcnt lgkmcnt(9)
	v_pk_fma_f32 v[42:43], v[106:107], v[116:117], v[42:43]
	v_pk_fma_f32 v[118:119], v[120:121], v[56:57], v[44:45] op_sel_hi:[0,1,1]
	v_pk_fma_f32 v[42:43], v[108:109], v[118:119], v[42:43]
	s_nop 0
	v_add_f32_e32 v38, v42, v43
	v_fma_mix_f32 v30, v1, v30, v38 op_sel:[0,1,0] op_sel_hi:[0,1,0]
	v_fma_mixlo_f16 v30, v30, v34, 0 op_sel:[0,1,0] op_sel_hi:[0,1,0]
	ds_write_b16 v68, v30 offset:21776
	ds_read_b128 v[42:45], v67 offset:2432
	ds_read_b128 v[46:49], v67 offset:2448
	ds_read_b128 v[50:53], v67 offset:2464
	ds_read_b128 v[54:57], v67 offset:2480
	ds_read_b128 v[58:61], v67 offset:2496
	ds_read_b128 v[62:65], v67 offset:2512
	ds_read_b128 v[102:105], v67 offset:2528
	ds_read_b128 v[106:109], v67 offset:2544
	v_cvt_f32_f16_e32 v30, v39
	v_cvt_f32_f16_e32 v34, v31
	v_pk_mul_f32 v[120:121], v[30:31], v[14:15] op_sel_hi:[0,1]
	v_exp_f32_e32 v120, v120
	v_exp_f32_e32 v121, v121
	v_pk_mul_f32 v[128:129], v[30:31], v[16:17] op_sel_hi:[0,1]
	v_exp_f32_e32 v128, v128
	v_exp_f32_e32 v129, v129
	v_mul_f32_e32 v34, v30, v34
	v_pk_mul_f32 v[120:121], v[120:121], v[122:123]
	s_waitcnt lgkmcnt(14)
	v_pk_fma_f32 v[120:121], v[34:35], v[70:71], v[120:121] op_sel_hi:[0,1,1]
	s_waitcnt lgkmcnt(12)
	v_pk_fma_f32 v[70:71], v[86:87], v[120:121], 0 op_sel_hi:[1,1,0]
	v_pk_mul_f32 v[86:87], v[128:129], v[124:125]
	s_nop 0
	v_pk_fma_f32 v[122:123], v[34:35], v[72:73], v[86:87] op_sel_hi:[0,1,1]
	v_pk_mul_f32 v[72:73], v[30:31], v[10:11] op_sel_hi:[0,1]
	v_exp_f32_e32 v72, v72
	v_exp_f32_e32 v73, v73
	v_pk_mul_f32 v[86:87], v[30:31], v[12:13] op_sel_hi:[0,1]
	v_exp_f32_e32 v86, v86
	v_exp_f32_e32 v87, v87
	v_pk_mul_f32 v[72:73], v[72:73], v[126:127]
	v_pk_fma_f32 v[70:71], v[88:89], v[122:123], v[70:71]
	v_pk_fma_f32 v[124:125], v[34:35], v[74:75], v[72:73] op_sel_hi:[0,1,1]
	v_pk_mul_f32 v[72:73], v[86:87], v[110:111]
	v_pk_mul_f32 v[74:75], v[30:31], v[8:9] op_sel_hi:[0,1]
	v_pk_fma_f32 v[110:111], v[34:35], v[76:77], v[72:73] op_sel_hi:[0,1,1]
	v_pk_mul_f32 v[72:73], v[30:31], v[6:7] op_sel_hi:[0,1]
	v_exp_f32_e32 v72, v72
	v_exp_f32_e32 v73, v73
	v_exp_f32_e32 v74, v74
	v_exp_f32_e32 v75, v75
	s_waitcnt lgkmcnt(11)
	v_pk_fma_f32 v[70:71], v[90:91], v[124:125], v[70:71]
	v_pk_mul_f32 v[72:73], v[72:73], v[112:113]
	v_pk_fma_f32 v[70:71], v[92:93], v[110:111], v[70:71]
	v_pk_fma_f32 v[112:113], v[34:35], v[78:79], v[72:73] op_sel_hi:[0,1,1]
	v_pk_mul_f32 v[72:73], v[74:75], v[114:115]
	v_pk_mul_f32 v[74:75], v[30:31], v[4:5] op_sel_hi:[0,1]
	v_pk_fma_f32 v[114:115], v[34:35], v[80:81], v[72:73] op_sel_hi:[0,1,1]
	v_pk_mul_f32 v[72:73], v[30:31], v[2:3] op_sel_hi:[0,1]
	v_exp_f32_e32 v72, v72
	v_exp_f32_e32 v73, v73
	v_exp_f32_e32 v74, v74
	v_exp_f32_e32 v75, v75
	s_waitcnt lgkmcnt(10)
	v_pk_fma_f32 v[70:71], v[94:95], v[112:113], v[70:71]
	v_pk_mul_f32 v[72:73], v[72:73], v[116:117]
	v_pk_fma_f32 v[70:71], v[96:97], v[114:115], v[70:71]
	v_pk_fma_f32 v[116:117], v[34:35], v[82:83], v[72:73] op_sel_hi:[0,1,1]
	v_pk_mul_f32 v[72:73], v[74:75], v[118:119]
	s_waitcnt lgkmcnt(9)
	v_pk_fma_f32 v[70:71], v[98:99], v[116:117], v[70:71]
	v_pk_fma_f32 v[118:119], v[34:35], v[84:85], v[72:73] op_sel_hi:[0,1,1]
	v_pk_fma_f32 v[70:71], v[100:101], v[118:119], v[70:71]
	s_nop 0
	v_add_f32_e32 v30, v70, v71
	v_fma_mix_f32 v30, v1, v31, v30 op_sel_hi:[0,1,0]
	v_fma_mixlo_f16 v30, v30, v35, 0 op_sel_hi:[0,1,0]
	ds_write_b16 v68, v30 offset:22816
	ds_read_b128 v[70:73], v67 offset:2560
	ds_read_b128 v[74:77], v67 offset:2576
	ds_read_b128 v[78:81], v67 offset:2592
	ds_read_b128 v[82:85], v67 offset:2608
	ds_read_b128 v[86:89], v67 offset:2624
	ds_read_b128 v[90:93], v67 offset:2640
	ds_read_b128 v[94:97], v67 offset:2656
	ds_read_b128 v[98:101], v67 offset:2672
	v_cvt_f32_f16_sdwa v30, v39 dst_sel:DWORD dst_unused:UNUSED_PAD src0_sel:WORD_1
	v_cvt_f32_f16_sdwa v34, v31 dst_sel:DWORD dst_unused:UNUSED_PAD src0_sel:WORD_1
	v_pk_mul_f32 v[38:39], v[30:31], v[14:15] op_sel_hi:[0,1]
	v_exp_f32_e32 v38, v38
	v_exp_f32_e32 v39, v39
	v_pk_mul_f32 v[126:127], v[30:31], v[16:17] op_sel_hi:[0,1]
	v_exp_f32_e32 v126, v126
	v_exp_f32_e32 v127, v127
	v_mul_f32_e32 v34, v30, v34
	v_pk_mul_f32 v[38:39], v[38:39], v[120:121]
	s_waitcnt lgkmcnt(14)
	v_pk_fma_f32 v[38:39], v[34:35], v[42:43], v[38:39] op_sel_hi:[0,1,1]
	s_waitcnt lgkmcnt(12)
	v_pk_fma_f32 v[42:43], v[58:59], v[38:39], 0 op_sel_hi:[1,1,0]
	v_pk_mul_f32 v[58:59], v[126:127], v[122:123]
	s_nop 0
	v_pk_fma_f32 v[120:121], v[34:35], v[44:45], v[58:59] op_sel_hi:[0,1,1]
	v_pk_mul_f32 v[44:45], v[30:31], v[10:11] op_sel_hi:[0,1]
	v_exp_f32_e32 v44, v44
	v_exp_f32_e32 v45, v45
	v_pk_mul_f32 v[58:59], v[30:31], v[12:13] op_sel_hi:[0,1]
	v_exp_f32_e32 v58, v58
	v_exp_f32_e32 v59, v59
	v_pk_mul_f32 v[44:45], v[44:45], v[124:125]
	v_pk_fma_f32 v[42:43], v[60:61], v[120:121], v[42:43]
	v_pk_fma_f32 v[122:123], v[34:35], v[46:47], v[44:45] op_sel_hi:[0,1,1]
	v_pk_mul_f32 v[44:45], v[58:59], v[110:111]
	v_pk_mul_f32 v[46:47], v[30:31], v[8:9] op_sel_hi:[0,1]
	v_pk_fma_f32 v[110:111], v[34:35], v[48:49], v[44:45] op_sel_hi:[0,1,1]
	v_pk_mul_f32 v[44:45], v[30:31], v[6:7] op_sel_hi:[0,1]
	v_exp_f32_e32 v44, v44
	v_exp_f32_e32 v45, v45
	v_exp_f32_e32 v46, v46
	v_exp_f32_e32 v47, v47
	s_waitcnt lgkmcnt(11)
	v_pk_fma_f32 v[42:43], v[62:63], v[122:123], v[42:43]
	v_pk_mul_f32 v[44:45], v[44:45], v[112:113]
	v_pk_fma_f32 v[42:43], v[64:65], v[110:111], v[42:43]
	v_pk_fma_f32 v[112:113], v[34:35], v[50:51], v[44:45] op_sel_hi:[0,1,1]
	v_pk_mul_f32 v[44:45], v[46:47], v[114:115]
	v_pk_mul_f32 v[46:47], v[30:31], v[4:5] op_sel_hi:[0,1]
	v_pk_fma_f32 v[114:115], v[34:35], v[52:53], v[44:45] op_sel_hi:[0,1,1]
	v_pk_mul_f32 v[44:45], v[30:31], v[2:3] op_sel_hi:[0,1]
	v_exp_f32_e32 v44, v44
	v_exp_f32_e32 v45, v45
	v_exp_f32_e32 v46, v46
	v_exp_f32_e32 v47, v47
	s_waitcnt lgkmcnt(10)
	v_pk_fma_f32 v[42:43], v[102:103], v[112:113], v[42:43]
	v_pk_mul_f32 v[44:45], v[44:45], v[116:117]
	v_pk_fma_f32 v[42:43], v[104:105], v[114:115], v[42:43]
	v_pk_fma_f32 v[116:117], v[34:35], v[54:55], v[44:45] op_sel_hi:[0,1,1]
	v_pk_mul_f32 v[44:45], v[46:47], v[118:119]
	s_waitcnt lgkmcnt(9)
	v_pk_fma_f32 v[42:43], v[106:107], v[116:117], v[42:43]
	v_pk_fma_f32 v[118:119], v[34:35], v[56:57], v[44:45] op_sel_hi:[0,1,1]
	v_pk_fma_f32 v[42:43], v[108:109], v[118:119], v[42:43]
	s_nop 0
	v_add_f32_e32 v30, v42, v43
	v_fma_mix_f32 v30, v1, v31, v30 op_sel:[0,1,0] op_sel_hi:[0,1,0]
	v_fma_mixlo_f16 v30, v30, v35, 0 op_sel:[0,1,0] op_sel_hi:[0,1,0]
	ds_write_b16 v68, v30 offset:23856
	ds_read_b128 v[42:45], v67 offset:2688
	ds_read_b128 v[46:49], v67 offset:2704
	ds_read_b128 v[50:53], v67 offset:2720
	ds_read_b128 v[54:57], v67 offset:2736
	ds_read_b128 v[58:61], v67 offset:2752
	ds_read_b128 v[62:65], v67 offset:2768
	ds_read_b128 v[102:105], v67 offset:2784
	ds_read_b128 v[106:109], v67 offset:2800
	v_cvt_f32_f16_e32 v30, v40
	v_cvt_f32_f16_e32 v31, v32
	v_pk_mul_f32 v[124:125], v[30:31], v[14:15] op_sel_hi:[0,1]
	v_exp_f32_e32 v124, v124
	v_exp_f32_e32 v125, v125
	v_pk_mul_f32 v[126:127], v[30:31], v[16:17] op_sel_hi:[0,1]
	v_exp_f32_e32 v126, v126
	v_exp_f32_e32 v127, v127
	v_mul_f32_e32 v34, v30, v31
	v_pk_mul_f32 v[38:39], v[124:125], v[38:39]
	s_waitcnt lgkmcnt(14)
	v_pk_fma_f32 v[38:39], v[34:35], v[70:71], v[38:39] op_sel_hi:[0,1,1]
	s_waitcnt lgkmcnt(12)
	v_pk_fma_f32 v[70:71], v[86:87], v[38:39], 0 op_sel_hi:[1,1,0]
	v_pk_mul_f32 v[86:87], v[126:127], v[120:121]
	s_nop 0
	v_pk_fma_f32 v[120:121], v[34:35], v[72:73], v[86:87] op_sel_hi:[0,1,1]
	v_pk_mul_f32 v[72:73], v[30:31], v[10:11] op_sel_hi:[0,1]
	v_exp_f32_e32 v72, v72
	v_exp_f32_e32 v73, v73
	v_pk_mul_f32 v[86:87], v[30:31], v[12:13] op_sel_hi:[0,1]
	v_exp_f32_e32 v86, v86
	v_exp_f32_e32 v87, v87
	v_pk_mul_f32 v[72:73], v[72:73], v[122:123]
	v_pk_fma_f32 v[70:71], v[88:89], v[120:121], v[70:71]
	v_pk_fma_f32 v[122:123], v[34:35], v[74:75], v[72:73] op_sel_hi:[0,1,1]
	v_pk_mul_f32 v[72:73], v[86:87], v[110:111]
	v_pk_mul_f32 v[74:75], v[30:31], v[8:9] op_sel_hi:[0,1]
	v_pk_fma_f32 v[110:111], v[34:35], v[76:77], v[72:73] op_sel_hi:[0,1,1]
	v_pk_mul_f32 v[72:73], v[30:31], v[6:7] op_sel_hi:[0,1]
	v_exp_f32_e32 v72, v72
	v_exp_f32_e32 v73, v73
	v_exp_f32_e32 v74, v74
	v_exp_f32_e32 v75, v75
	s_waitcnt lgkmcnt(11)
	v_pk_fma_f32 v[70:71], v[90:91], v[122:123], v[70:71]
	v_pk_mul_f32 v[72:73], v[72:73], v[112:113]
	v_pk_fma_f32 v[70:71], v[92:93], v[110:111], v[70:71]
	v_pk_fma_f32 v[112:113], v[34:35], v[78:79], v[72:73] op_sel_hi:[0,1,1]
	v_pk_mul_f32 v[72:73], v[74:75], v[114:115]
	s_waitcnt lgkmcnt(10)
	v_pk_fma_f32 v[70:71], v[94:95], v[112:113], v[70:71]
	v_pk_fma_f32 v[114:115], v[34:35], v[80:81], v[72:73] op_sel_hi:[0,1,1]
	v_pk_mul_f32 v[72:73], v[30:31], v[2:3] op_sel_hi:[0,1]
	v_exp_f32_e32 v72, v72
	v_exp_f32_e32 v73, v73
	v_pk_mul_f32 v[30:31], v[30:31], v[4:5] op_sel_hi:[0,1]
	v_exp_f32_e32 v30, v30
	v_exp_f32_e32 v31, v31
	v_pk_mul_f32 v[72:73], v[72:73], v[116:117]
	v_pk_fma_f32 v[70:71], v[96:97], v[114:115], v[70:71]
	v_pk_fma_f32 v[116:117], v[34:35], v[82:83], v[72:73] op_sel_hi:[0,1,1]
	v_pk_mul_f32 v[30:31], v[30:31], v[118:119]
	s_waitcnt lgkmcnt(9)
	v_pk_fma_f32 v[70:71], v[98:99], v[116:117], v[70:71]
	v_pk_fma_f32 v[30:31], v[34:35], v[84:85], v[30:31] op_sel_hi:[0,1,1]
	v_pk_fma_f32 v[34:35], v[100:101], v[30:31], v[70:71]
	s_nop 0
	v_add_f32_e32 v34, v34, v35
	v_fma_mix_f32 v34, v1, v32, v34 op_sel_hi:[0,1,0]
	v_fma_mixlo_f16 v34, v34, v36, 0 op_sel_hi:[0,1,0]
	ds_write_b16 v68, v34 offset:24896
	ds_read_b128 v[70:73], v67 offset:2816
	ds_read_b128 v[74:77], v67 offset:2832
	ds_read_b128 v[78:81], v67 offset:2848
	ds_read_b128 v[82:85], v67 offset:2864
	ds_read_b128 v[86:89], v67 offset:2880
	ds_read_b128 v[90:93], v67 offset:2896
	ds_read_b128 v[94:97], v67 offset:2912
	ds_read_b128 v[98:101], v67 offset:2928
	v_cvt_f32_f16_sdwa v34, v40 dst_sel:DWORD dst_unused:UNUSED_PAD src0_sel:WORD_1
	v_cvt_f32_f16_sdwa v35, v32 dst_sel:DWORD dst_unused:UNUSED_PAD src0_sel:WORD_1
	v_pk_mul_f32 v[118:119], v[34:35], v[14:15] op_sel_hi:[0,1]
	v_exp_f32_e32 v118, v118
	v_exp_f32_e32 v119, v119
	v_pk_mul_f32 v[124:125], v[34:35], v[16:17] op_sel_hi:[0,1]
	v_exp_f32_e32 v124, v124
	v_exp_f32_e32 v125, v125
	v_mul_f32_e32 v40, v34, v35
	v_pk_mul_f32 v[38:39], v[118:119], v[38:39]
	s_waitcnt lgkmcnt(14)
	v_pk_fma_f32 v[38:39], v[40:41], v[42:43], v[38:39] op_sel_hi:[0,1,1]
	s_waitcnt lgkmcnt(12)
	v_pk_fma_f32 v[42:43], v[58:59], v[38:39], 0 op_sel_hi:[1,1,0]
	v_pk_mul_f32 v[58:59], v[124:125], v[120:121]
	s_nop 0
	v_pk_fma_f32 v[118:119], v[40:41], v[44:45], v[58:59] op_sel_hi:[0,1,1]
	v_pk_mul_f32 v[44:45], v[34:35], v[10:11] op_sel_hi:[0,1]
	v_exp_f32_e32 v44, v44
	v_exp_f32_e32 v45, v45
	v_pk_mul_f32 v[58:59], v[34:35], v[12:13] op_sel_hi:[0,1]
	v_exp_f32_e32 v58, v58
	v_exp_f32_e32 v59, v59
	v_pk_mul_f32 v[44:45], v[44:45], v[122:123]
	v_pk_fma_f32 v[42:43], v[60:61], v[118:119], v[42:43]
	v_pk_fma_f32 v[120:121], v[40:41], v[46:47], v[44:45] op_sel_hi:[0,1,1]
	v_pk_mul_f32 v[44:45], v[58:59], v[110:111]
	v_pk_mul_f32 v[46:47], v[34:35], v[8:9] op_sel_hi:[0,1]
	v_pk_fma_f32 v[110:111], v[40:41], v[48:49], v[44:45] op_sel_hi:[0,1,1]
	v_pk_mul_f32 v[44:45], v[34:35], v[6:7] op_sel_hi:[0,1]
	v_exp_f32_e32 v44, v44
	v_exp_f32_e32 v45, v45
	v_exp_f32_e32 v46, v46
	v_exp_f32_e32 v47, v47
	s_waitcnt lgkmcnt(11)
	v_pk_fma_f32 v[42:43], v[62:63], v[120:121], v[42:43]
	v_pk_mul_f32 v[44:45], v[44:45], v[112:113]
	v_pk_fma_f32 v[42:43], v[64:65], v[110:111], v[42:43]
	v_pk_fma_f32 v[112:113], v[40:41], v[50:51], v[44:45] op_sel_hi:[0,1,1]
	v_pk_mul_f32 v[44:45], v[46:47], v[114:115]
	s_waitcnt lgkmcnt(10)
	v_pk_fma_f32 v[42:43], v[102:103], v[112:113], v[42:43]
	v_pk_fma_f32 v[114:115], v[40:41], v[52:53], v[44:45] op_sel_hi:[0,1,1]
	v_pk_mul_f32 v[44:45], v[34:35], v[2:3] op_sel_hi:[0,1]
	v_exp_f32_e32 v44, v44
	v_exp_f32_e32 v45, v45
	v_pk_mul_f32 v[34:35], v[34:35], v[4:5] op_sel_hi:[0,1]
	v_exp_f32_e32 v34, v34
	v_exp_f32_e32 v35, v35
	v_pk_mul_f32 v[44:45], v[44:45], v[116:117]
	v_pk_fma_f32 v[42:43], v[104:105], v[114:115], v[42:43]
	v_pk_fma_f32 v[116:117], v[40:41], v[54:55], v[44:45] op_sel_hi:[0,1,1]
	v_pk_mul_f32 v[30:31], v[34:35], v[30:31]
	s_waitcnt lgkmcnt(9)
	v_pk_fma_f32 v[42:43], v[106:107], v[116:117], v[42:43]
	v_pk_fma_f32 v[30:31], v[40:41], v[56:57], v[30:31] op_sel_hi:[0,1,1]
	v_pk_fma_f32 v[34:35], v[108:109], v[30:31], v[42:43]
	s_nop 0
	v_add_f32_e32 v34, v34, v35
	v_fma_mix_f32 v32, v1, v32, v34 op_sel:[0,1,0] op_sel_hi:[0,1,0]
	v_fma_mixlo_f16 v32, v32, v36, 0 op_sel:[0,1,0] op_sel_hi:[0,1,0]
	ds_write_b16 v68, v32 offset:25936
	ds_read_b128 v[42:45], v67 offset:2944
	ds_read_b128 v[46:49], v67 offset:2960
	ds_read_b128 v[50:53], v67 offset:2976
	ds_read_b128 v[54:57], v67 offset:2992
	ds_read_b128 v[58:61], v67 offset:3008
	ds_read_b128 v[62:65], v67 offset:3024
	ds_read_b128 v[102:105], v67 offset:3040
	ds_read_b128 v[106:109], v67 offset:3056
	v_cvt_f32_f16_e32 v32, v41
	v_cvt_f32_f16_e32 v34, v33
	v_pk_mul_f32 v[122:123], v[32:33], v[14:15] op_sel_hi:[0,1]
	v_exp_f32_e32 v122, v122
	v_exp_f32_e32 v123, v123
	v_pk_mul_f32 v[124:125], v[32:33], v[16:17] op_sel_hi:[0,1]
	v_exp_f32_e32 v124, v124
	v_exp_f32_e32 v125, v125
	v_mul_f32_e32 v34, v32, v34
	v_pk_mul_f32 v[38:39], v[122:123], v[38:39]
	s_waitcnt lgkmcnt(14)
	v_pk_fma_f32 v[38:39], v[34:35], v[70:71], v[38:39] op_sel_hi:[0,1,1]
	s_waitcnt lgkmcnt(12)
	v_pk_fma_f32 v[70:71], v[86:87], v[38:39], 0 op_sel_hi:[1,1,0]
	v_pk_mul_f32 v[86:87], v[124:125], v[118:119]
	s_nop 0
	v_pk_fma_f32 v[118:119], v[34:35], v[72:73], v[86:87] op_sel_hi:[0,1,1]
	v_pk_mul_f32 v[72:73], v[32:33], v[10:11] op_sel_hi:[0,1]
	v_exp_f32_e32 v72, v72
	v_exp_f32_e32 v73, v73
	v_pk_mul_f32 v[86:87], v[32:33], v[12:13] op_sel_hi:[0,1]
	v_exp_f32_e32 v86, v86
	v_exp_f32_e32 v87, v87
	v_pk_mul_f32 v[72:73], v[72:73], v[120:121]
	v_pk_fma_f32 v[70:71], v[88:89], v[118:119], v[70:71]
	v_pk_fma_f32 v[120:121], v[34:35], v[74:75], v[72:73] op_sel_hi:[0,1,1]
	v_pk_mul_f32 v[72:73], v[86:87], v[110:111]
	v_pk_mul_f32 v[74:75], v[32:33], v[8:9] op_sel_hi:[0,1]
	v_pk_fma_f32 v[110:111], v[34:35], v[76:77], v[72:73] op_sel_hi:[0,1,1]
	v_pk_mul_f32 v[72:73], v[32:33], v[6:7] op_sel_hi:[0,1]
	v_exp_f32_e32 v72, v72
	v_exp_f32_e32 v73, v73
	v_exp_f32_e32 v74, v74
	v_exp_f32_e32 v75, v75
	s_waitcnt lgkmcnt(11)
	v_pk_fma_f32 v[70:71], v[90:91], v[120:121], v[70:71]
	v_pk_mul_f32 v[72:73], v[72:73], v[112:113]
	v_pk_fma_f32 v[70:71], v[92:93], v[110:111], v[70:71]
	v_pk_fma_f32 v[112:113], v[34:35], v[78:79], v[72:73] op_sel_hi:[0,1,1]
	v_pk_mul_f32 v[72:73], v[74:75], v[114:115]
	v_pk_mul_f32 v[74:75], v[32:33], v[4:5] op_sel_hi:[0,1]
	v_pk_fma_f32 v[114:115], v[34:35], v[80:81], v[72:73] op_sel_hi:[0,1,1]
	v_pk_mul_f32 v[72:73], v[32:33], v[2:3] op_sel_hi:[0,1]
	v_exp_f32_e32 v72, v72
	v_exp_f32_e32 v73, v73
	v_exp_f32_e32 v74, v74
	v_exp_f32_e32 v75, v75
	s_waitcnt lgkmcnt(10)
	v_pk_fma_f32 v[70:71], v[94:95], v[112:113], v[70:71]
	v_pk_mul_f32 v[72:73], v[72:73], v[116:117]
	v_pk_fma_f32 v[70:71], v[96:97], v[114:115], v[70:71]
	v_pk_fma_f32 v[116:117], v[34:35], v[82:83], v[72:73] op_sel_hi:[0,1,1]
	v_pk_mul_f32 v[30:31], v[74:75], v[30:31]
	s_waitcnt lgkmcnt(9)
	v_pk_fma_f32 v[70:71], v[98:99], v[116:117], v[70:71]
	v_pk_fma_f32 v[30:31], v[34:35], v[84:85], v[30:31] op_sel_hi:[0,1,1]
	v_pk_fma_f32 v[34:35], v[100:101], v[30:31], v[70:71]
	s_nop 0
	v_add_f32_e32 v32, v34, v35
	v_fma_mix_f32 v32, v1, v33, v32 op_sel_hi:[0,1,0]
	v_fma_mixlo_f16 v32, v32, v37, 0 op_sel_hi:[0,1,0]
	ds_write_b16 v68, v32 offset:26976
	ds_read_b128 v[70:73], v67 offset:3072
	ds_read_b128 v[74:77], v67 offset:3088
	ds_read_b128 v[78:81], v67 offset:3104
	ds_read_b128 v[82:85], v67 offset:3120
	ds_read_b128 v[86:89], v67 offset:3136
	ds_read_b128 v[90:93], v67 offset:3152
	ds_read_b128 v[94:97], v67 offset:3168
	ds_read_b128 v[98:101], v67 offset:3184
	v_cvt_f32_f16_sdwa v32, v41 dst_sel:DWORD dst_unused:UNUSED_PAD src0_sel:WORD_1
	v_cvt_f32_f16_sdwa v34, v33 dst_sel:DWORD dst_unused:UNUSED_PAD src0_sel:WORD_1
	v_pk_mul_f32 v[40:41], v[32:33], v[14:15] op_sel_hi:[0,1]
	v_pk_mul_f32 v[122:123], v[32:33], v[16:17] op_sel_hi:[0,1]
	v_exp_f32_e32 v40, v40
	v_exp_f32_e32 v41, v41
	v_exp_f32_e32 v122, v122
	v_exp_f32_e32 v123, v123
	v_mul_f32_e32 v34, v32, v34
	v_pk_mul_f32 v[38:39], v[40:41], v[38:39]
	v_pk_mul_f32 v[40:41], v[122:123], v[118:119]
	s_waitcnt lgkmcnt(14)
	v_pk_fma_f32 v[118:119], v[34:35], v[44:45], v[40:41] op_sel_hi:[0,1,1]
	v_pk_mul_f32 v[40:41], v[32:33], v[10:11] op_sel_hi:[0,1]
	v_pk_fma_f32 v[124:125], v[34:35], v[42:43], v[38:39] op_sel_hi:[0,1,1]
	v_exp_f32_e32 v40, v40
	v_exp_f32_e32 v41, v41
	v_pk_mul_f32 v[42:43], v[32:33], v[12:13] op_sel_hi:[0,1]
	v_exp_f32_e32 v42, v42
	v_exp_f32_e32 v43, v43
	s_waitcnt lgkmcnt(12)
	v_pk_fma_f32 v[38:39], v[58:59], v[124:125], 0 op_sel_hi:[1,1,0]
	v_pk_mul_f32 v[40:41], v[40:41], v[120:121]
	v_pk_fma_f32 v[38:39], v[60:61], v[118:119], v[38:39]
	v_pk_fma_f32 v[120:121], v[34:35], v[46:47], v[40:41] op_sel_hi:[0,1,1]
	v_pk_mul_f32 v[40:41], v[42:43], v[110:111]
	s_waitcnt lgkmcnt(11)
	v_pk_fma_f32 v[38:39], v[62:63], v[120:121], v[38:39]
	v_pk_fma_f32 v[62:63], v[34:35], v[48:49], v[40:41] op_sel_hi:[0,1,1]
	v_pk_mul_f32 v[40:41], v[32:33], v[6:7] op_sel_hi:[0,1]
	v_exp_f32_e32 v40, v40
	v_exp_f32_e32 v41, v41
	v_pk_mul_f32 v[42:43], v[32:33], v[8:9] op_sel_hi:[0,1]
	v_exp_f32_e32 v42, v42
	v_exp_f32_e32 v43, v43
	v_pk_mul_f32 v[40:41], v[40:41], v[112:113]
	v_pk_fma_f32 v[38:39], v[64:65], v[62:63], v[38:39]
	v_pk_fma_f32 v[64:65], v[34:35], v[50:51], v[40:41] op_sel_hi:[0,1,1]
	v_pk_mul_f32 v[40:41], v[42:43], v[114:115]
	s_waitcnt lgkmcnt(10)
	v_pk_fma_f32 v[38:39], v[102:103], v[64:65], v[38:39]
	v_pk_fma_f32 v[102:103], v[34:35], v[52:53], v[40:41] op_sel_hi:[0,1,1]
	v_pk_mul_f32 v[40:41], v[32:33], v[2:3] op_sel_hi:[0,1]
	v_exp_f32_e32 v40, v40
	v_exp_f32_e32 v41, v41
	v_pk_mul_f32 v[42:43], v[32:33], v[4:5] op_sel_hi:[0,1]
	v_exp_f32_e32 v42, v42
	v_exp_f32_e32 v43, v43
	v_pk_mul_f32 v[40:41], v[40:41], v[116:117]
	v_pk_fma_f32 v[38:39], v[104:105], v[102:103], v[38:39]
	v_pk_fma_f32 v[104:105], v[34:35], v[54:55], v[40:41] op_sel_hi:[0,1,1]
	v_pk_mul_f32 v[30:31], v[42:43], v[30:31]
	s_waitcnt lgkmcnt(9)
	v_pk_fma_f32 v[38:39], v[106:107], v[104:105], v[38:39]
	v_pk_fma_f32 v[106:107], v[34:35], v[56:57], v[30:31] op_sel_hi:[0,1,1]
	v_pk_fma_f32 v[30:31], v[108:109], v[106:107], v[38:39]
	s_nop 0
	v_add_f32_e32 v30, v30, v31
	v_fma_mix_f32 v30, v1, v33, v30 op_sel:[0,1,0] op_sel_hi:[0,1,0]
	v_fma_mixlo_f16 v30, v30, v37, 0 op_sel:[0,1,0] op_sel_hi:[0,1,0]
	ds_write_b16 v68, v30 offset:28016
	ds_read_b128 v[30:33], v67 offset:3200
	ds_read_b128 v[34:37], v67 offset:3216
	ds_read_b128 v[38:41], v67 offset:3232
	ds_read_b128 v[42:45], v67 offset:3248
	ds_read_b128 v[46:49], v67 offset:3264
	ds_read_b128 v[50:53], v67 offset:3280
	ds_read_b128 v[54:57], v67 offset:3296
	ds_read_b128 v[58:61], v67 offset:3312
	s_waitcnt vmcnt(2)
	v_cvt_f32_f16_e32 v108, v26
	s_waitcnt vmcnt(1)
	v_cvt_f32_f16_e32 v69, v18
	v_pk_mul_f32 v[112:113], v[108:109], v[14:15] op_sel_hi:[0,1]
	v_exp_f32_e32 v112, v112
	v_exp_f32_e32 v113, v113
	v_pk_mul_f32 v[114:115], v[108:109], v[16:17] op_sel_hi:[0,1]
	v_exp_f32_e32 v114, v114
	v_exp_f32_e32 v115, v115
	v_mul_f32_e32 v110, v108, v69
	v_pk_mul_f32 v[112:113], v[112:113], v[124:125]
	s_waitcnt lgkmcnt(14)
	v_pk_fma_f32 v[112:113], v[110:111], v[70:71], v[112:113] op_sel_hi:[0,1,1]
	s_waitcnt lgkmcnt(12)
	v_pk_fma_f32 v[70:71], v[86:87], v[112:113], 0 op_sel_hi:[1,1,0]
	v_pk_mul_f32 v[86:87], v[114:115], v[118:119]
	s_nop 0
	v_pk_fma_f32 v[114:115], v[110:111], v[72:73], v[86:87] op_sel_hi:[0,1,1]
	v_pk_mul_f32 v[72:73], v[108:109], v[10:11] op_sel_hi:[0,1]
	v_exp_f32_e32 v72, v72
	v_exp_f32_e32 v73, v73
	v_pk_mul_f32 v[86:87], v[108:109], v[12:13] op_sel_hi:[0,1]
	v_exp_f32_e32 v86, v86
	v_exp_f32_e32 v87, v87
	v_pk_mul_f32 v[72:73], v[72:73], v[120:121]
	v_pk_fma_f32 v[70:71], v[88:89], v[114:115], v[70:71]
	v_pk_fma_f32 v[116:117], v[110:111], v[74:75], v[72:73] op_sel_hi:[0,1,1]
	v_pk_mul_f32 v[62:63], v[86:87], v[62:63]
	s_waitcnt lgkmcnt(11)
	v_pk_fma_f32 v[70:71], v[90:91], v[116:117], v[70:71]
	v_pk_fma_f32 v[118:119], v[110:111], v[76:77], v[62:63] op_sel_hi:[0,1,1]
	v_pk_fma_f32 v[62:63], v[92:93], v[118:119], v[70:71]
	v_pk_mul_f32 v[70:71], v[108:109], v[6:7] op_sel_hi:[0,1]
	v_exp_f32_e32 v70, v70
	v_exp_f32_e32 v71, v71
	v_pk_mul_f32 v[72:73], v[108:109], v[8:9] op_sel_hi:[0,1]
	v_exp_f32_e32 v72, v72
	v_exp_f32_e32 v73, v73
	v_pk_mul_f32 v[64:65], v[70:71], v[64:65]
	v_pk_mul_f32 v[70:71], v[108:109], v[4:5] op_sel_hi:[0,1]
	v_pk_fma_f32 v[120:121], v[110:111], v[78:79], v[64:65] op_sel_hi:[0,1,1]
	v_pk_mul_f32 v[64:65], v[72:73], v[102:103]
	v_exp_f32_e32 v70, v70
	v_pk_fma_f32 v[102:103], v[110:111], v[80:81], v[64:65] op_sel_hi:[0,1,1]
	v_pk_mul_f32 v[64:65], v[108:109], v[2:3] op_sel_hi:[0,1]
	v_exp_f32_e32 v64, v64
	v_exp_f32_e32 v65, v65
	v_exp_f32_e32 v71, v71
	s_waitcnt lgkmcnt(10)
	v_pk_fma_f32 v[62:63], v[94:95], v[120:121], v[62:63]
	v_pk_mul_f32 v[64:65], v[64:65], v[104:105]
	v_pk_fma_f32 v[62:63], v[96:97], v[102:103], v[62:63]
	v_pk_fma_f32 v[104:105], v[110:111], v[82:83], v[64:65] op_sel_hi:[0,1,1]
	v_pk_mul_f32 v[64:65], v[70:71], v[106:107]
	s_waitcnt lgkmcnt(9)
	v_pk_fma_f32 v[62:63], v[98:99], v[104:105], v[62:63]
	v_pk_fma_f32 v[98:99], v[110:111], v[84:85], v[64:65] op_sel_hi:[0,1,1]
	v_pk_fma_f32 v[62:63], v[100:101], v[98:99], v[62:63]
	s_nop 0
	v_add_f32_e32 v62, v62, v63
	v_fma_mix_f32 v62, v1, v18, v62 op_sel_hi:[0,1,0]
	s_waitcnt vmcnt(0)
	v_fma_mixlo_f16 v62, v62, v22, 0 op_sel_hi:[0,1,0]
	ds_write_b16 v68, v62 offset:29056
	v_lshrrev_b32_e32 v196, 6, v0
	v_and_b32_e32 v197, 48, v0
	v_lshl_or_b32 v196, v196, 7, v197
	v_and_b32_e32 v197, 15, v0
	v_or_b32_e32 v197, s28, v197
	v_lshl_or_b32 v196, v197, 10, v196
	v_add_u32_e32 v197, 0x4000, v196
	global_load_dwordx4 v[180:183], v196, s[4:5]
	global_load_dwordx4 v[184:187], v196, s[4:5] offset:64
	global_load_dwordx4 v[188:191], v197, s[4:5]
	global_load_dwordx4 v[192:195], v197, s[4:5] offset:64
	v_and_b32_e32 v196, 63, v0
	v_lshlrev_b32_e32 v196, 4, v196
	global_load_dwordx4 v[204:207], v196, s[6:7]
	global_load_dwordx4 v[208:211], v196, s[8:9]
	ds_read_b128 v[62:65], v67 offset:3328
	ds_read_b128 v[70:73], v67 offset:3344
	ds_read_b128 v[74:77], v67 offset:3360
	ds_read_b128 v[78:81], v67 offset:3376
	ds_read_b128 v[82:85], v67 offset:3392
	ds_read_b128 v[86:89], v67 offset:3408
	ds_read_b128 v[90:93], v67 offset:3424
	ds_read_b128 v[94:97], v67 offset:3440
	v_cvt_f32_f16_sdwa v26, v26 dst_sel:DWORD dst_unused:UNUSED_PAD src0_sel:WORD_1
	v_cvt_f32_f16_sdwa v69, v18 dst_sel:DWORD dst_unused:UNUSED_PAD src0_sel:WORD_1
	v_pk_mul_f32 v[106:107], v[26:27], v[14:15] op_sel_hi:[0,1]
	v_exp_f32_e32 v106, v106
	v_exp_f32_e32 v107, v107
	v_pk_mul_f32 v[108:109], v[26:27], v[16:17] op_sel_hi:[0,1]
	v_exp_f32_e32 v108, v108
	v_exp_f32_e32 v109, v109
	v_mul_f32_e32 v100, v26, v69
	v_pk_mul_f32 v[106:107], v[106:107], v[112:113]
	s_waitcnt lgkmcnt(14)
	v_pk_fma_f32 v[106:107], v[100:101], v[30:31], v[106:107] op_sel_hi:[0,1,1]
	s_waitcnt lgkmcnt(12)
	v_pk_fma_f32 v[30:31], v[46:47], v[106:107], 0 op_sel_hi:[1,1,0]
	v_pk_mul_f32 v[46:47], v[108:109], v[114:115]
	s_nop 0
	v_pk_fma_f32 v[108:109], v[100:101], v[32:33], v[46:47] op_sel_hi:[0,1,1]
	v_pk_mul_f32 v[32:33], v[26:27], v[10:11] op_sel_hi:[0,1]
	v_exp_f32_e32 v32, v32
	v_exp_f32_e32 v33, v33
	v_pk_mul_f32 v[46:47], v[26:27], v[12:13] op_sel_hi:[0,1]
	v_exp_f32_e32 v46, v46
	v_exp_f32_e32 v47, v47
	v_pk_mul_f32 v[32:33], v[32:33], v[116:117]
	v_pk_fma_f32 v[30:31], v[48:49], v[108:109], v[30:31]
	v_pk_fma_f32 v[110:111], v[100:101], v[34:35], v[32:33] op_sel_hi:[0,1,1]
	v_pk_mul_f32 v[32:33], v[46:47], v[118:119]
	v_pk_mul_f32 v[34:35], v[26:27], v[8:9] op_sel_hi:[0,1]
	v_pk_fma_f32 v[112:113], v[100:101], v[36:37], v[32:33] op_sel_hi:[0,1,1]
	v_pk_mul_f32 v[32:33], v[26:27], v[6:7] op_sel_hi:[0,1]
	v_exp_f32_e32 v32, v32
	v_exp_f32_e32 v33, v33
	v_exp_f32_e32 v34, v34
	v_exp_f32_e32 v35, v35
	s_waitcnt lgkmcnt(11)
	v_pk_fma_f32 v[30:31], v[50:51], v[110:111], v[30:31]
	v_pk_mul_f32 v[32:33], v[32:33], v[120:121]
	v_pk_fma_f32 v[30:31], v[52:53], v[112:113], v[30:31]
	v_pk_fma_f32 v[114:115], v[100:101], v[38:39], v[32:33] op_sel_hi:[0,1,1]
	v_pk_mul_f32 v[32:33], v[34:35], v[102:103]
	v_pk_mul_f32 v[34:35], v[26:27], v[4:5] op_sel_hi:[0,1]
	v_pk_fma_f32 v[102:103], v[100:101], v[40:41], v[32:33] op_sel_hi:[0,1,1]
	v_pk_mul_f32 v[32:33], v[26:27], v[2:3] op_sel_hi:[0,1]
	v_exp_f32_e32 v32, v32
	v_exp_f32_e32 v33, v33
	v_exp_f32_e32 v34, v34
	v_exp_f32_e32 v35, v35
	s_waitcnt lgkmcnt(10)
	v_pk_fma_f32 v[30:31], v[54:55], v[114:115], v[30:31]
	v_pk_mul_f32 v[32:33], v[32:33], v[104:105]
	v_pk_fma_f32 v[30:31], v[56:57], v[102:103], v[30:31]
	v_pk_fma_f32 v[104:105], v[100:101], v[42:43], v[32:33] op_sel_hi:[0,1,1]
	v_pk_mul_f32 v[32:33], v[34:35], v[98:99]
	s_waitcnt lgkmcnt(9)
	v_pk_fma_f32 v[30:31], v[58:59], v[104:105], v[30:31]
	v_pk_fma_f32 v[98:99], v[100:101], v[44:45], v[32:33] op_sel_hi:[0,1,1]
	v_pk_fma_f32 v[30:31], v[60:61], v[98:99], v[30:31]
	s_nop 0
	v_add_f32_e32 v26, v30, v31
	v_fma_mix_f32 v18, v1, v18, v26 op_sel:[0,1,0] op_sel_hi:[0,1,0]
	v_fma_mixlo_f16 v18, v18, v22, 0 op_sel:[0,1,0] op_sel_hi:[0,1,0]
	ds_write_b16 v68, v18 offset:30096
	ds_read_b128 v[30:33], v67 offset:3456
	ds_read_b128 v[34:37], v67 offset:3472
	ds_read_b128 v[38:41], v67 offset:3488
	ds_read_b128 v[42:45], v67 offset:3504
	ds_read_b128 v[46:49], v67 offset:3520
	ds_read_b128 v[50:53], v67 offset:3536
	ds_read_b128 v[54:57], v67 offset:3552
	ds_read_b128 v[58:61], v67 offset:3568
	v_cvt_f32_f16_e32 v18, v27
	v_cvt_f32_f16_e32 v22, v19
	v_pk_mul_f32 v[100:101], v[18:19], v[14:15] op_sel_hi:[0,1]
	v_exp_f32_e32 v100, v100
	v_exp_f32_e32 v101, v101
	v_pk_mul_f32 v[116:117], v[18:19], v[16:17] op_sel_hi:[0,1]
	v_exp_f32_e32 v116, v116
	v_exp_f32_e32 v117, v117
	v_mul_f32_e32 v22, v18, v22
	v_pk_mul_f32 v[100:101], v[100:101], v[106:107]
	s_waitcnt lgkmcnt(14)
	v_pk_fma_f32 v[100:101], v[22:23], v[62:63], v[100:101] op_sel_hi:[0,1,1]
	s_waitcnt lgkmcnt(12)
	v_pk_fma_f32 v[62:63], v[82:83], v[100:101], 0 op_sel_hi:[1,1,0]
	v_pk_mul_f32 v[82:83], v[116:117], v[108:109]
	s_nop 0
	v_pk_fma_f32 v[106:107], v[22:23], v[64:65], v[82:83] op_sel_hi:[0,1,1]
	v_pk_mul_f32 v[64:65], v[18:19], v[10:11] op_sel_hi:[0,1]
	v_exp_f32_e32 v64, v64
	v_exp_f32_e32 v65, v65
	v_pk_mul_f32 v[82:83], v[18:19], v[12:13] op_sel_hi:[0,1]
	v_exp_f32_e32 v82, v82
	v_exp_f32_e32 v83, v83
	v_pk_mul_f32 v[64:65], v[64:65], v[110:111]
	v_pk_fma_f32 v[62:63], v[84:85], v[106:107], v[62:63]
	v_pk_fma_f32 v[108:109], v[22:23], v[70:71], v[64:65] op_sel_hi:[0,1,1]
	v_pk_mul_f32 v[64:65], v[82:83], v[112:113]
	v_pk_mul_f32 v[70:71], v[18:19], v[8:9] op_sel_hi:[0,1]
	v_pk_fma_f32 v[110:111], v[22:23], v[72:73], v[64:65] op_sel_hi:[0,1,1]
	v_pk_mul_f32 v[64:65], v[18:19], v[6:7] op_sel_hi:[0,1]
	v_exp_f32_e32 v64, v64
	v_exp_f32_e32 v65, v65
	v_exp_f32_e32 v70, v70
	v_exp_f32_e32 v71, v71
	s_waitcnt lgkmcnt(11)
	v_pk_fma_f32 v[62:63], v[86:87], v[108:109], v[62:63]
	v_pk_mul_f32 v[64:65], v[64:65], v[114:115]
	v_pk_fma_f32 v[62:63], v[88:89], v[110:111], v[62:63]
	v_pk_fma_f32 v[112:113], v[22:23], v[74:75], v[64:65] op_sel_hi:[0,1,1]
	v_pk_mul_f32 v[64:65], v[70:71], v[102:103]
	v_pk_mul_f32 v[70:71], v[18:19], v[4:5] op_sel_hi:[0,1]
	v_pk_fma_f32 v[102:103], v[22:23], v[76:77], v[64:65] op_sel_hi:[0,1,1]
	v_pk_mul_f32 v[64:65], v[18:19], v[2:3] op_sel_hi:[0,1]
	v_exp_f32_e32 v64, v64
	v_exp_f32_e32 v65, v65
	v_exp_f32_e32 v70, v70
	v_exp_f32_e32 v71, v71
	s_waitcnt lgkmcnt(10)
	v_pk_fma_f32 v[62:63], v[90:91], v[112:113], v[62:63]
	v_pk_mul_f32 v[64:65], v[64:65], v[104:105]
	v_pk_fma_f32 v[62:63], v[92:93], v[102:103], v[62:63]
	v_pk_fma_f32 v[104:105], v[22:23], v[78:79], v[64:65] op_sel_hi:[0,1,1]
	v_pk_mul_f32 v[64:65], v[70:71], v[98:99]
	s_waitcnt lgkmcnt(9)
	v_pk_fma_f32 v[62:63], v[94:95], v[104:105], v[62:63]
	v_pk_fma_f32 v[98:99], v[22:23], v[80:81], v[64:65] op_sel_hi:[0,1,1]
	v_pk_fma_f32 v[62:63], v[96:97], v[98:99], v[62:63]
	s_nop 0
	v_add_f32_e32 v18, v62, v63
	v_fma_mix_f32 v18, v1, v19, v18 op_sel_hi:[0,1,0]
	v_fma_mixlo_f16 v18, v18, v23, 0 op_sel_hi:[0,1,0]
	ds_write_b16 v68, v18 offset:31136
	ds_read_b128 v[62:65], v67 offset:3584
	ds_read_b128 v[70:73], v67 offset:3600
	ds_read_b128 v[74:77], v67 offset:3616
	ds_read_b128 v[78:81], v67 offset:3632
	ds_read_b128 v[82:85], v67 offset:3648
	ds_read_b128 v[86:89], v67 offset:3664
	ds_read_b128 v[90:93], v67 offset:3680
	ds_read_b128 v[94:97], v67 offset:3696
	v_cvt_f32_f16_sdwa v18, v27 dst_sel:DWORD dst_unused:UNUSED_PAD src0_sel:WORD_1
	v_cvt_f32_f16_sdwa v22, v19 dst_sel:DWORD dst_unused:UNUSED_PAD src0_sel:WORD_1
	v_pk_mul_f32 v[26:27], v[18:19], v[14:15] op_sel_hi:[0,1]
	v_exp_f32_e32 v26, v26
	v_exp_f32_e32 v27, v27
	v_pk_mul_f32 v[114:115], v[18:19], v[16:17] op_sel_hi:[0,1]
	v_exp_f32_e32 v114, v114
	v_exp_f32_e32 v115, v115
	v_mul_f32_e32 v22, v18, v22
	v_pk_mul_f32 v[26:27], v[26:27], v[100:101]
	s_waitcnt lgkmcnt(14)
	v_pk_fma_f32 v[26:27], v[22:23], v[30:31], v[26:27] op_sel_hi:[0,1,1]
	s_waitcnt lgkmcnt(12)
	v_pk_fma_f32 v[30:31], v[46:47], v[26:27], 0 op_sel_hi:[1,1,0]
	v_pk_mul_f32 v[46:47], v[114:115], v[106:107]
	s_nop 0
	v_pk_fma_f32 v[100:101], v[22:23], v[32:33], v[46:47] op_sel_hi:[0,1,1]
	v_pk_mul_f32 v[32:33], v[18:19], v[10:11] op_sel_hi:[0,1]
	v_exp_f32_e32 v32, v32
	v_exp_f32_e32 v33, v33
	v_pk_mul_f32 v[46:47], v[18:19], v[12:13] op_sel_hi:[0,1]
	v_exp_f32_e32 v46, v46
	v_exp_f32_e32 v47, v47
	v_pk_mul_f32 v[32:33], v[32:33], v[108:109]
	v_pk_fma_f32 v[30:31], v[48:49], v[100:101], v[30:31]
	v_pk_fma_f32 v[106:107], v[22:23], v[34:35], v[32:33] op_sel_hi:[0,1,1]
	v_pk_mul_f32 v[32:33], v[46:47], v[110:111]
	v_pk_mul_f32 v[34:35], v[18:19], v[8:9] op_sel_hi:[0,1]
	v_pk_fma_f32 v[108:109], v[22:23], v[36:37], v[32:33] op_sel_hi:[0,1,1]
	v_pk_mul_f32 v[32:33], v[18:19], v[6:7] op_sel_hi:[0,1]
	v_exp_f32_e32 v32, v32
	v_exp_f32_e32 v33, v33
	v_exp_f32_e32 v34, v34
	v_exp_f32_e32 v35, v35
	s_waitcnt lgkmcnt(11)
	v_pk_fma_f32 v[30:31], v[50:51], v[106:107], v[30:31]
	v_pk_mul_f32 v[32:33], v[32:33], v[112:113]
	v_pk_fma_f32 v[30:31], v[52:53], v[108:109], v[30:31]
	v_pk_fma_f32 v[110:111], v[22:23], v[38:39], v[32:33] op_sel_hi:[0,1,1]
	v_pk_mul_f32 v[32:33], v[34:35], v[102:103]
	v_pk_mul_f32 v[34:35], v[18:19], v[4:5] op_sel_hi:[0,1]
	v_pk_fma_f32 v[102:103], v[22:23], v[40:41], v[32:33] op_sel_hi:[0,1,1]
	v_pk_mul_f32 v[32:33], v[18:19], v[2:3] op_sel_hi:[0,1]
	v_exp_f32_e32 v32, v32
	v_exp_f32_e32 v33, v33
	v_exp_f32_e32 v34, v34
	v_exp_f32_e32 v35, v35
	s_waitcnt lgkmcnt(10)
	v_pk_fma_f32 v[30:31], v[54:55], v[110:111], v[30:31]
	v_pk_mul_f32 v[32:33], v[32:33], v[104:105]
	v_pk_fma_f32 v[30:31], v[56:57], v[102:103], v[30:31]
	v_pk_fma_f32 v[104:105], v[22:23], v[42:43], v[32:33] op_sel_hi:[0,1,1]
	v_pk_mul_f32 v[32:33], v[34:35], v[98:99]
	s_waitcnt lgkmcnt(9)
	v_pk_fma_f32 v[30:31], v[58:59], v[104:105], v[30:31]
	v_pk_fma_f32 v[98:99], v[22:23], v[44:45], v[32:33] op_sel_hi:[0,1,1]
	v_pk_fma_f32 v[30:31], v[60:61], v[98:99], v[30:31]
	s_nop 0
	v_add_f32_e32 v18, v30, v31
	v_fma_mix_f32 v18, v1, v19, v18 op_sel:[0,1,0] op_sel_hi:[0,1,0]
	v_fma_mixlo_f16 v18, v18, v23, 0 op_sel:[0,1,0] op_sel_hi:[0,1,0]
	ds_write_b16 v68, v18 offset:32176
	ds_read_b128 v[30:33], v67 offset:3712
	ds_read_b128 v[34:37], v67 offset:3728
	ds_read_b128 v[38:41], v67 offset:3744
	ds_read_b128 v[42:45], v67 offset:3760
	ds_read_b128 v[46:49], v67 offset:3776
	ds_read_b128 v[50:53], v67 offset:3792
	ds_read_b128 v[54:57], v67 offset:3808
	ds_read_b128 v[58:61], v67 offset:3824
	v_cvt_f32_f16_e32 v18, v28
	v_cvt_f32_f16_e32 v19, v20
	v_pk_mul_f32 v[112:113], v[18:19], v[14:15] op_sel_hi:[0,1]
	v_exp_f32_e32 v112, v112
	v_exp_f32_e32 v113, v113
	v_pk_mul_f32 v[114:115], v[18:19], v[16:17] op_sel_hi:[0,1]
	v_exp_f32_e32 v114, v114
	v_exp_f32_e32 v115, v115
	v_mul_f32_e32 v22, v18, v19
	v_pk_mul_f32 v[26:27], v[112:113], v[26:27]
	s_waitcnt lgkmcnt(14)
	v_pk_fma_f32 v[26:27], v[22:23], v[62:63], v[26:27] op_sel_hi:[0,1,1]
	s_waitcnt lgkmcnt(12)
	v_pk_fma_f32 v[62:63], v[82:83], v[26:27], 0 op_sel_hi:[1,1,0]
	v_pk_mul_f32 v[82:83], v[114:115], v[100:101]
	s_nop 0
	v_pk_fma_f32 v[100:101], v[22:23], v[64:65], v[82:83] op_sel_hi:[0,1,1]
	v_pk_mul_f32 v[64:65], v[18:19], v[10:11] op_sel_hi:[0,1]
	v_exp_f32_e32 v64, v64
	v_exp_f32_e32 v65, v65
	v_pk_mul_f32 v[82:83], v[18:19], v[12:13] op_sel_hi:[0,1]
	v_exp_f32_e32 v82, v82
	v_exp_f32_e32 v83, v83
	v_pk_mul_f32 v[64:65], v[64:65], v[106:107]
	v_pk_fma_f32 v[62:63], v[84:85], v[100:101], v[62:63]
	v_pk_fma_f32 v[106:107], v[22:23], v[70:71], v[64:65] op_sel_hi:[0,1,1]
	v_pk_mul_f32 v[64:65], v[82:83], v[108:109]
	v_pk_mul_f32 v[70:71], v[18:19], v[8:9] op_sel_hi:[0,1]
	v_pk_fma_f32 v[108:109], v[22:23], v[72:73], v[64:65] op_sel_hi:[0,1,1]
	v_pk_mul_f32 v[64:65], v[18:19], v[6:7] op_sel_hi:[0,1]
	v_exp_f32_e32 v64, v64
	v_exp_f32_e32 v65, v65
	v_exp_f32_e32 v70, v70
	v_exp_f32_e32 v71, v71
	s_waitcnt lgkmcnt(11)
	v_pk_fma_f32 v[62:63], v[86:87], v[106:107], v[62:63]
	v_pk_mul_f32 v[64:65], v[64:65], v[110:111]
	v_pk_fma_f32 v[62:63], v[88:89], v[108:109], v[62:63]
	v_pk_fma_f32 v[110:111], v[22:23], v[74:75], v[64:65] op_sel_hi:[0,1,1]
	v_pk_mul_f32 v[64:65], v[70:71], v[102:103]
	s_waitcnt lgkmcnt(10)
	v_pk_fma_f32 v[62:63], v[90:91], v[110:111], v[62:63]
	v_pk_fma_f32 v[102:103], v[22:23], v[76:77], v[64:65] op_sel_hi:[0,1,1]
	v_pk_mul_f32 v[64:65], v[18:19], v[2:3] op_sel_hi:[0,1]
	v_exp_f32_e32 v64, v64
	v_exp_f32_e32 v65, v65
	v_pk_mul_f32 v[18:19], v[18:19], v[4:5] op_sel_hi:[0,1]
	v_exp_f32_e32 v18, v18
	v_exp_f32_e32 v19, v19
	v_pk_mul_f32 v[64:65], v[64:65], v[104:105]
	v_pk_fma_f32 v[62:63], v[92:93], v[102:103], v[62:63]
	v_pk_fma_f32 v[104:105], v[22:23], v[78:79], v[64:65] op_sel_hi:[0,1,1]
	v_pk_mul_f32 v[18:19], v[18:19], v[98:99]
	s_waitcnt lgkmcnt(9)
	v_pk_fma_f32 v[62:63], v[94:95], v[104:105], v[62:63]
	v_pk_fma_f32 v[18:19], v[22:23], v[80:81], v[18:19] op_sel_hi:[0,1,1]
	v_pk_fma_f32 v[22:23], v[96:97], v[18:19], v[62:63]
	s_nop 0
	v_add_f32_e32 v22, v22, v23
	v_fma_mix_f32 v22, v1, v20, v22 op_sel_hi:[0,1,0]
	v_fma_mixlo_f16 v22, v22, v24, 0 op_sel_hi:[0,1,0]
	ds_write_b16 v68, v22 offset:33216
	ds_read_b128 v[62:65], v67 offset:3840
	ds_read_b128 v[70:73], v67 offset:3856
	ds_read_b128 v[74:77], v67 offset:3872
	ds_read_b128 v[78:81], v67 offset:3888
	ds_read_b128 v[82:85], v67 offset:3904
	ds_read_b128 v[86:89], v67 offset:3920
	ds_read_b128 v[90:93], v67 offset:3936
	ds_read_b128 v[94:97], v67 offset:3952
	v_cvt_f32_f16_sdwa v22, v28 dst_sel:DWORD dst_unused:UNUSED_PAD src0_sel:WORD_1
	v_cvt_f32_f16_sdwa v23, v20 dst_sel:DWORD dst_unused:UNUSED_PAD src0_sel:WORD_1
	v_pk_mul_f32 v[98:99], v[22:23], v[14:15] op_sel_hi:[0,1]
	v_exp_f32_e32 v98, v98
	v_exp_f32_e32 v99, v99
	v_pk_mul_f32 v[112:113], v[22:23], v[16:17] op_sel_hi:[0,1]
	v_exp_f32_e32 v112, v112
	v_exp_f32_e32 v113, v113
	v_mul_f32_e32 v28, v22, v23
	v_pk_mul_f32 v[26:27], v[98:99], v[26:27]
	s_waitcnt lgkmcnt(14)
	v_pk_fma_f32 v[26:27], v[28:29], v[30:31], v[26:27] op_sel_hi:[0,1,1]
	s_waitcnt lgkmcnt(12)
	v_pk_fma_f32 v[30:31], v[46:47], v[26:27], 0 op_sel_hi:[1,1,0]
	v_pk_mul_f32 v[46:47], v[112:113], v[100:101]
	s_nop 0
	v_pk_fma_f32 v[98:99], v[28:29], v[32:33], v[46:47] op_sel_hi:[0,1,1]
	v_pk_mul_f32 v[32:33], v[22:23], v[10:11] op_sel_hi:[0,1]
	v_exp_f32_e32 v32, v32
	v_exp_f32_e32 v33, v33
	v_pk_mul_f32 v[46:47], v[22:23], v[12:13] op_sel_hi:[0,1]
	v_exp_f32_e32 v46, v46
	v_exp_f32_e32 v47, v47
	v_pk_mul_f32 v[32:33], v[32:33], v[106:107]
	v_pk_fma_f32 v[30:31], v[48:49], v[98:99], v[30:31]
	v_pk_fma_f32 v[100:101], v[28:29], v[34:35], v[32:33] op_sel_hi:[0,1,1]
	v_pk_mul_f32 v[32:33], v[46:47], v[108:109]
	v_pk_mul_f32 v[34:35], v[22:23], v[8:9] op_sel_hi:[0,1]
	v_pk_fma_f32 v[106:107], v[28:29], v[36:37], v[32:33] op_sel_hi:[0,1,1]
	v_pk_mul_f32 v[32:33], v[22:23], v[6:7] op_sel_hi:[0,1]
	v_exp_f32_e32 v32, v32
	v_exp_f32_e32 v33, v33
	v_exp_f32_e32 v34, v34
	v_exp_f32_e32 v35, v35
	s_waitcnt lgkmcnt(11)
	v_pk_fma_f32 v[30:31], v[50:51], v[100:101], v[30:31]
	v_pk_mul_f32 v[32:33], v[32:33], v[110:111]
	v_pk_fma_f32 v[30:31], v[52:53], v[106:107], v[30:31]
	v_pk_fma_f32 v[108:109], v[28:29], v[38:39], v[32:33] op_sel_hi:[0,1,1]
	v_pk_mul_f32 v[32:33], v[34:35], v[102:103]
	s_waitcnt lgkmcnt(10)
	v_pk_fma_f32 v[30:31], v[54:55], v[108:109], v[30:31]
	v_pk_fma_f32 v[102:103], v[28:29], v[40:41], v[32:33] op_sel_hi:[0,1,1]
	v_pk_mul_f32 v[32:33], v[22:23], v[2:3] op_sel_hi:[0,1]
	v_exp_f32_e32 v32, v32
	v_exp_f32_e32 v33, v33
	v_pk_mul_f32 v[22:23], v[22:23], v[4:5] op_sel_hi:[0,1]
	v_exp_f32_e32 v22, v22
	v_exp_f32_e32 v23, v23
	v_pk_mul_f32 v[32:33], v[32:33], v[104:105]
	v_pk_fma_f32 v[30:31], v[56:57], v[102:103], v[30:31]
	v_pk_fma_f32 v[104:105], v[28:29], v[42:43], v[32:33] op_sel_hi:[0,1,1]
	v_pk_mul_f32 v[18:19], v[22:23], v[18:19]
	s_waitcnt lgkmcnt(9)
	v_pk_fma_f32 v[30:31], v[58:59], v[104:105], v[30:31]
	v_pk_fma_f32 v[18:19], v[28:29], v[44:45], v[18:19] op_sel_hi:[0,1,1]
	v_pk_fma_f32 v[22:23], v[60:61], v[18:19], v[30:31]
	s_nop 0
	v_add_f32_e32 v22, v22, v23
	v_fma_mix_f32 v20, v1, v20, v22 op_sel:[0,1,0] op_sel_hi:[0,1,0]
	v_fma_mixlo_f16 v20, v20, v24, 0 op_sel:[0,1,0] op_sel_hi:[0,1,0]
	ds_write_b16 v68, v20 offset:34256
	ds_read_b128 v[30:33], v67 offset:3968
	ds_read_b128 v[34:37], v67 offset:3984
	ds_read_b128 v[38:41], v67 offset:4000
	ds_read_b128 v[42:45], v67 offset:4016
	ds_read_b128 v[46:49], v67 offset:4032
	ds_read_b128 v[50:53], v67 offset:4048
	ds_read_b128 v[54:57], v67 offset:4064
	ds_read_b128 v[58:61], v67 offset:4080
	v_cvt_f32_f16_e32 v20, v29
	v_cvt_f32_f16_e32 v22, v21
	v_pk_mul_f32 v[110:111], v[20:21], v[14:15] op_sel_hi:[0,1]
	v_exp_f32_e32 v110, v110
	v_exp_f32_e32 v111, v111
	v_pk_mul_f32 v[112:113], v[20:21], v[16:17] op_sel_hi:[0,1]
	v_exp_f32_e32 v112, v112
	v_exp_f32_e32 v113, v113
	v_mul_f32_e32 v22, v20, v22
	v_pk_mul_f32 v[26:27], v[110:111], v[26:27]
	s_waitcnt lgkmcnt(14)
	v_pk_fma_f32 v[26:27], v[22:23], v[62:63], v[26:27] op_sel_hi:[0,1,1]
	s_waitcnt lgkmcnt(12)
	v_pk_fma_f32 v[62:63], v[82:83], v[26:27], 0 op_sel_hi:[1,1,0]
	v_pk_mul_f32 v[82:83], v[112:113], v[98:99]
	s_nop 0
	v_pk_fma_f32 v[64:65], v[22:23], v[64:65], v[82:83] op_sel_hi:[0,1,1]
	v_pk_mul_f32 v[82:83], v[20:21], v[10:11] op_sel_hi:[0,1]
	v_pk_fma_f32 v[62:63], v[84:85], v[64:65], v[62:63]
	v_exp_f32_e32 v82, v82
	v_exp_f32_e32 v83, v83
	v_pk_mul_f32 v[84:85], v[20:21], v[12:13] op_sel_hi:[0,1]
	v_exp_f32_e32 v84, v84
	v_exp_f32_e32 v85, v85
	v_pk_mul_f32 v[82:83], v[82:83], v[100:101]
	s_nop 0
	v_pk_fma_f32 v[70:71], v[22:23], v[70:71], v[82:83] op_sel_hi:[0,1,1]
	v_pk_mul_f32 v[82:83], v[84:85], v[106:107]
	v_pk_mul_f32 v[84:85], v[20:21], v[8:9] op_sel_hi:[0,1]
	v_pk_fma_f32 v[72:73], v[22:23], v[72:73], v[82:83] op_sel_hi:[0,1,1]
	v_pk_mul_f32 v[82:83], v[20:21], v[6:7] op_sel_hi:[0,1]
	v_exp_f32_e32 v82, v82
	v_exp_f32_e32 v83, v83
	v_exp_f32_e32 v84, v84
	v_exp_f32_e32 v85, v85
	s_waitcnt lgkmcnt(11)
	v_pk_fma_f32 v[62:63], v[86:87], v[70:71], v[62:63]
	v_pk_mul_f32 v[82:83], v[82:83], v[108:109]
	v_pk_fma_f32 v[62:63], v[88:89], v[72:73], v[62:63]
	v_pk_fma_f32 v[74:75], v[22:23], v[74:75], v[82:83] op_sel_hi:[0,1,1]
	v_pk_mul_f32 v[82:83], v[84:85], v[102:103]
	v_pk_mul_f32 v[84:85], v[20:21], v[4:5] op_sel_hi:[0,1]
	v_pk_fma_f32 v[76:77], v[22:23], v[76:77], v[82:83] op_sel_hi:[0,1,1]
	v_pk_mul_f32 v[82:83], v[20:21], v[2:3] op_sel_hi:[0,1]
	v_exp_f32_e32 v82, v82
	v_exp_f32_e32 v83, v83
	v_exp_f32_e32 v84, v84
	v_exp_f32_e32 v85, v85
	s_waitcnt lgkmcnt(10)
	v_pk_fma_f32 v[62:63], v[90:91], v[74:75], v[62:63]
	v_pk_mul_f32 v[82:83], v[82:83], v[104:105]
	v_pk_fma_f32 v[62:63], v[92:93], v[76:77], v[62:63]
	v_pk_fma_f32 v[78:79], v[22:23], v[78:79], v[82:83] op_sel_hi:[0,1,1]
	v_pk_mul_f32 v[18:19], v[84:85], v[18:19]
	s_waitcnt lgkmcnt(9)
	v_pk_fma_f32 v[62:63], v[94:95], v[78:79], v[62:63]
	v_pk_fma_f32 v[18:19], v[22:23], v[80:81], v[18:19] op_sel_hi:[0,1,1]
	v_pk_fma_f32 v[22:23], v[96:97], v[18:19], v[62:63]
	s_nop 0
	v_add_f32_e32 v20, v22, v23
	v_fma_mix_f32 v20, v1, v21, v20 op_sel_hi:[0,1,0]
	v_fma_mixlo_f16 v20, v20, v25, 0 op_sel_hi:[0,1,0]
	ds_write_b16 v68, v20 offset:35296
	v_cvt_f32_f16_sdwa v20, v29 dst_sel:DWORD dst_unused:UNUSED_PAD src0_sel:WORD_1
	v_cvt_f32_f16_sdwa v22, v21 dst_sel:DWORD dst_unused:UNUSED_PAD src0_sel:WORD_1
	v_pk_mul_f32 v[14:15], v[20:21], v[14:15] op_sel_hi:[0,1]
	v_exp_f32_e32 v14, v14
	v_exp_f32_e32 v15, v15
	v_pk_mul_f32 v[16:17], v[20:21], v[16:17] op_sel_hi:[0,1]
	v_exp_f32_e32 v16, v16
	v_exp_f32_e32 v17, v17
	v_pk_mul_f32 v[10:11], v[20:21], v[10:11] op_sel_hi:[0,1]
	v_exp_f32_e32 v10, v10
	v_exp_f32_e32 v11, v11
	v_pk_mul_f32 v[12:13], v[20:21], v[12:13] op_sel_hi:[0,1]
	v_exp_f32_e32 v12, v12
	v_exp_f32_e32 v13, v13
	v_pk_mul_f32 v[6:7], v[20:21], v[6:7] op_sel_hi:[0,1]
	v_mul_f32_e32 v22, v20, v22
	v_pk_mul_f32 v[14:15], v[14:15], v[26:27]
	v_exp_f32_e32 v6, v6
	v_exp_f32_e32 v7, v7
	v_pk_mul_f32 v[8:9], v[20:21], v[8:9] op_sel_hi:[0,1]
	s_waitcnt lgkmcnt(8)
	v_pk_fma_f32 v[14:15], v[22:23], v[30:31], v[14:15] op_sel_hi:[0,1,1]
	v_pk_mul_f32 v[16:17], v[16:17], v[64:65]
	v_exp_f32_e32 v8, v8
	v_exp_f32_e32 v9, v9
	v_pk_mul_f32 v[2:3], v[20:21], v[2:3] op_sel_hi:[0,1]
	s_waitcnt lgkmcnt(4)
	v_pk_fma_f32 v[14:15], v[46:47], v[14:15], 0 op_sel_hi:[1,1,0]
	v_pk_fma_f32 v[16:17], v[22:23], v[32:33], v[16:17] op_sel_hi:[0,1,1]
	v_pk_mul_f32 v[10:11], v[10:11], v[70:71]
	v_exp_f32_e32 v2, v2
	v_exp_f32_e32 v3, v3
	v_pk_mul_f32 v[4:5], v[20:21], v[4:5] op_sel_hi:[0,1]
	v_pk_fma_f32 v[14:15], v[48:49], v[16:17], v[14:15]
	v_pk_fma_f32 v[10:11], v[22:23], v[34:35], v[10:11] op_sel_hi:[0,1,1]
	v_pk_mul_f32 v[12:13], v[12:13], v[72:73]
	v_exp_f32_e32 v4, v4
	v_exp_f32_e32 v5, v5
	s_waitcnt lgkmcnt(3)
	v_pk_fma_f32 v[10:11], v[50:51], v[10:11], v[14:15]
	v_pk_fma_f32 v[12:13], v[22:23], v[36:37], v[12:13] op_sel_hi:[0,1,1]
	v_pk_mul_f32 v[6:7], v[6:7], v[74:75]
	v_pk_fma_f32 v[10:11], v[52:53], v[12:13], v[10:11]
	v_pk_fma_f32 v[6:7], v[22:23], v[38:39], v[6:7] op_sel_hi:[0,1,1]
	v_pk_mul_f32 v[8:9], v[8:9], v[76:77]
	s_waitcnt lgkmcnt(2)
	v_pk_fma_f32 v[6:7], v[54:55], v[6:7], v[10:11]
	v_pk_fma_f32 v[8:9], v[22:23], v[40:41], v[8:9] op_sel_hi:[0,1,1]
	v_pk_mul_f32 v[2:3], v[2:3], v[78:79]
	v_pk_fma_f32 v[6:7], v[56:57], v[8:9], v[6:7]
	v_pk_fma_f32 v[2:3], v[22:23], v[42:43], v[2:3] op_sel_hi:[0,1,1]
	v_pk_mul_f32 v[4:5], v[4:5], v[18:19]
	s_waitcnt lgkmcnt(1)
	v_pk_fma_f32 v[2:3], v[58:59], v[2:3], v[6:7]
	v_pk_fma_f32 v[4:5], v[22:23], v[44:45], v[4:5] op_sel_hi:[0,1,1]
	v_pk_fma_f32 v[2:3], v[60:61], v[4:5], v[2:3]
	s_nop 0
	v_add_f32_e32 v2, v2, v3
	v_fma_mix_f32 v1, v1, v21, v2 op_sel:[0,1,0] op_sel_hi:[0,1,0]
	v_fma_mixlo_f16 v1, v1, v25, 0 op_sel:[0,1,0] op_sel_hi:[0,1,0]
	ds_write_b16 v68, v1 offset:36336
	v_lshlrev_b32_e32 v1, 9, v0
	v_and_b32_e32 v2, 0x38000, v1
	v_mov_b32_e32 v3, v67
	v_and_b32_e32 v1, 63, v0
	s_bfe_u32 s14, s2, 0x40003
	v_lshl_add_u64 v[2:3], s[18:19], 0, v[2:3]
	v_lshlrev_b32_e32 v58, 4, v1
	v_mov_b32_e32 v59, v67
	s_lshl_b32 s13, s14, 6
	v_lshl_add_u64 v[20:21], v[2:3], 0, v[58:59]
	s_lshl_b32 s26, s14, 10
	s_add_i32 s12, s13, 64
	v_lshl_add_u64 v[2:3], v[20:21], 0, s[26:27]
	s_and_b32 s15, s12, 0x3c0
	v_add_co_u32_e32 v4, vcc, s52, v2
	s_lshl_b32 s26, s15, 4
	s_lshl_b32 s12, s12, 4
	v_addc_co_u32_e32 v5, vcc, 0, v3, vcc
	global_load_dwordx4 v[28:31], v[2:3], off
	global_load_dwordx4 v[32:35], v[4:5], off
	v_lshl_add_u64 v[2:3], v[20:21], 0, s[26:27]
	s_or_b32 s26, s12, 0x4000
	s_add_i32 s12, s13, 0x80
	s_and_b32 s15, s12, 0x3c0
	v_lshl_add_u64 v[4:5], v[20:21], 0, s[26:27]
	s_lshl_b32 s26, s15, 4
	s_lshl_b32 s12, s12, 4
	global_load_dwordx4 v[36:39], v[2:3], off
	global_load_dwordx4 v[40:43], v[4:5], off
	v_lshl_add_u64 v[2:3], v[20:21], 0, s[26:27]
	s_or_b32 s26, s12, 0x4000
	s_add_i32 s12, s13, 0xc0
	s_and_b32 s15, s12, 0x3c0
	v_lshl_add_u64 v[4:5], v[20:21], 0, s[26:27]
	s_lshl_b32 s26, s15, 4
	s_lshl_b32 s12, s12, 4
	global_load_dwordx4 v[44:47], v[2:3], off
	global_load_dwordx4 v[48:51], v[4:5], off
	v_lshl_add_u64 v[2:3], v[20:21], 0, s[26:27]
	s_or_b32 s26, s12, 0x4000
	s_add_i32 s12, s13, 0x100
	s_and_b32 s15, s12, 0x3c0
	v_lshl_add_u64 v[4:5], v[20:21], 0, s[26:27]
	s_lshl_b32 s26, s15, 4
	s_lshl_b32 s12, s12, 4
	global_load_dwordx4 v[52:55], v[2:3], off
	global_load_dwordx4 v[60:63], v[4:5], off
	v_lshl_add_u64 v[2:3], v[20:21], 0, s[26:27]
	s_or_b32 s26, s12, 0x4000
	s_add_i32 s12, s13, 0x140
	s_and_b32 s15, s12, 0x3c0
	v_lshl_add_u64 v[4:5], v[20:21], 0, s[26:27]
	s_lshl_b32 s26, s15, 4
	s_lshl_b32 s12, s12, 4
	global_load_dwordx4 v[68:71], v[2:3], off
	global_load_dwordx4 v[72:75], v[4:5], off
	v_lshl_add_u64 v[2:3], v[20:21], 0, s[26:27]
	s_or_b32 s26, s12, 0x4000
	s_add_i32 s12, s13, 0x180
	s_and_b32 s15, s12, 0x3c0
	v_lshl_add_u64 v[4:5], v[20:21], 0, s[26:27]
	s_lshl_b32 s26, s15, 4
	s_lshl_b32 s12, s12, 4
	global_load_dwordx4 v[76:79], v[2:3], off
	global_load_dwordx4 v[82:85], v[4:5], off
	v_lshl_add_u64 v[2:3], v[20:21], 0, s[26:27]
	s_or_b32 s26, s12, 0x4000
	s_add_i32 s12, s13, 0x1c0
	s_and_b32 s15, s12, 0x3c0
	v_lshl_add_u64 v[4:5], v[20:21], 0, s[26:27]
	s_lshl_b32 s26, s15, 4
	s_lshl_b32 s12, s12, 4
	v_lshl_add_u64 v[18:19], v[20:21], 0, s[26:27]
	s_or_b32 s26, s12, 0x4000
	s_xor_b32 s15, s13, 0x200
	v_lshl_add_u64 v[22:23], v[20:21], 0, s[26:27]
	s_lshl_b32 s26, s15, 4
	global_load_dwordx4 v[14:17], v[2:3], off
	global_load_dwordx4 v[10:13], v[4:5], off
	global_load_dwordx4 v[6:9], v[18:19], off
	s_nop 0
	global_load_dwordx4 v[2:5], v[22:23], off
	v_lshl_add_u64 v[18:19], v[20:21], 0, s[26:27]
	v_add_co_u32_e32 v22, vcc, s52, v18
	s_waitcnt lgkmcnt(0)
	s_barrier
	v_addc_co_u32_e32 v23, vcc, 0, v19, vcc
	global_load_dwordx4 v[86:89], v[18:19], off
	global_load_dwordx4 v[90:93], v[22:23], off
	v_lshrrev_b32_e32 v118, 6, v0
	v_lshlrev_b32_e32 v22, 7, v118
	v_mov_b32_e32 v23, v67
	v_and_b32_e32 v81, 15, v0
	v_lshl_add_u64 v[24:25], s[4:5], 0, v[22:23]
	v_and_b32_e32 v18, 48, v0
	v_mov_b32_e32 v19, v67
	s_movk_i32 s12, 0x410
	v_lshl_add_u64 v[56:57], v[24:25], 0, v[18:19]
	v_mad_u32_u24 v19, v81, s12, v18
	v_add_u32_e32 v23, s13, v19
	ds_read_b128 v[94:97], v23 offset:4096
	ds_read_b128 v[98:101], v23 offset:20736
	v_or_b32_e32 v26, s28, v81
	v_mov_b32_e32 v27, v67
	v_lshlrev_b64 v[24:25], 10, v[26:27]
	v_or_b32_e32 v26, 16, v26
	v_lshlrev_b64 v[26:27], 10, v[26:27]
	v_lshrrev_b32_e32 v23, 1, v0
	v_lshl_add_u64 v[24:25], v[56:57], 0, v[24:25]
	v_lshl_add_u64 v[26:27], v[56:57], 0, v[26:27]
	v_and_b32_e32 v80, 24, v23
	s_lshl_b32 s14, s14, 5
	s_setprio 1
	s_waitcnt vmcnt(17) lgkmcnt(1)
	v_mfma_f32_16x16x32_f16 v[102:105], v[28:31], v[94:97], 0
	s_waitcnt lgkmcnt(0)
	v_mfma_f32_16x16x32_f16 v[28:31], v[28:31], v[98:101], 0
	s_waitcnt vmcnt(16)
	v_mfma_f32_16x16x32_f16 v[94:97], v[32:35], v[94:97], 0
	v_mfma_f32_16x16x32_f16 v[32:35], v[32:35], v[98:101], 0
	s_setprio 0
	s_add_i32 s16, s13, 0x240
	s_and_b32 s17, s16, 0x3c0
	s_lshl_b32 s26, s17, 4
	s_lshl_b32 s16, s16, 4
	v_lshl_add_u64 v[56:57], v[20:21], 0, s[26:27]
	s_or_b32 s26, s16, 0x4000
	v_lshl_add_u64 v[64:65], v[20:21], 0, s[26:27]
	global_load_dwordx4 v[98:101], v[56:57], off
	global_load_dwordx4 v[106:109], v[64:65], off
	s_add_i32 s16, s14, 32
	s_and_b32 s16, s16, 0x1e0
	v_lshl_add_u32 v23, s16, 1, v19
	ds_read_b128 v[110:113], v23 offset:4096
	ds_read_b128 v[114:117], v23 offset:20736
	s_setprio 1
	s_waitcnt vmcnt(17) lgkmcnt(1)
	v_mfma_f32_16x16x32_f16 v[102:105], v[36:39], v[110:113], v[102:105]
	s_waitcnt lgkmcnt(0)
	v_mfma_f32_16x16x32_f16 v[28:31], v[36:39], v[114:117], v[28:31]
	s_waitcnt vmcnt(16)
	v_mfma_f32_16x16x32_f16 v[36:39], v[40:43], v[110:113], v[94:97]
	v_mfma_f32_16x16x32_f16 v[32:35], v[40:43], v[114:117], v[32:35]
	s_setprio 0
	s_add_i32 s16, s13, 0x280
	s_and_b32 s17, s16, 0x3c0
	s_lshl_b32 s26, s17, 4
	s_lshl_b32 s16, s16, 4
	v_lshl_add_u64 v[56:57], v[20:21], 0, s[26:27]
	s_or_b32 s26, s16, 0x4000
	v_lshl_add_u64 v[64:65], v[20:21], 0, s[26:27]
	global_load_dwordx4 v[40:43], v[56:57], off
	global_load_dwordx4 v[94:97], v[64:65], off
	s_add_i32 s16, s14, 64
	s_and_b32 s16, s16, 0x1e0
	v_lshl_add_u32 v23, s16, 1, v19
	ds_read_b128 v[110:113], v23 offset:4096
	ds_read_b128 v[114:117], v23 offset:20736
	s_setprio 1
	s_waitcnt vmcnt(17) lgkmcnt(1)
	v_mfma_f32_16x16x32_f16 v[102:105], v[44:47], v[110:113], v[102:105]
	s_waitcnt lgkmcnt(0)
	v_mfma_f32_16x16x32_f16 v[28:31], v[44:47], v[114:117], v[28:31]
	s_waitcnt vmcnt(16)
	v_mfma_f32_16x16x32_f16 v[36:39], v[48:51], v[110:113], v[36:39]
	v_mfma_f32_16x16x32_f16 v[32:35], v[48:51], v[114:117], v[32:35]
	s_setprio 0
	s_add_i32 s16, s13, 0x2c0
	s_and_b32 s17, s16, 0x3c0
	s_lshl_b32 s26, s17, 4
	s_lshl_b32 s16, s16, 4
	v_lshl_add_u64 v[56:57], v[20:21], 0, s[26:27]
	s_or_b32 s26, s16, 0x4000
	v_lshl_add_u64 v[64:65], v[20:21], 0, s[26:27]
	global_load_dwordx4 v[44:47], v[56:57], off
	global_load_dwordx4 v[48:51], v[64:65], off
	s_add_i32 s16, s14, 0x60
	s_and_b32 s16, s16, 0x1e0
	v_lshl_add_u32 v23, s16, 1, v19
	ds_read_b128 v[110:113], v23 offset:4096
	ds_read_b128 v[114:117], v23 offset:20736
	s_setprio 1
	s_waitcnt vmcnt(17) lgkmcnt(1)
	v_mfma_f32_16x16x32_f16 v[102:105], v[52:55], v[110:113], v[102:105]
	s_waitcnt lgkmcnt(0)
	v_mfma_f32_16x16x32_f16 v[28:31], v[52:55], v[114:117], v[28:31]
	s_waitcnt vmcnt(16)
	v_mfma_f32_16x16x32_f16 v[36:39], v[60:63], v[110:113], v[36:39]
	v_mfma_f32_16x16x32_f16 v[32:35], v[60:63], v[114:117], v[32:35]
	s_setprio 0
	s_add_i32 s16, s13, 0x300
	s_and_b32 s17, s16, 0x3c0
	s_lshl_b32 s26, s17, 4
	s_lshl_b32 s16, s16, 4
	v_lshl_add_u64 v[56:57], v[20:21], 0, s[26:27]
	s_or_b32 s26, s16, 0x4000
	v_lshl_add_u64 v[64:65], v[20:21], 0, s[26:27]
	global_load_dwordx4 v[52:55], v[56:57], off
	global_load_dwordx4 v[60:63], v[64:65], off
	s_add_i32 s16, s14, 0x80
	s_and_b32 s16, s16, 0x1e0
	v_lshl_add_u32 v23, s16, 1, v19
	ds_read_b128 v[110:113], v23 offset:4096
	ds_read_b128 v[114:117], v23 offset:20736
	s_setprio 1
	s_waitcnt vmcnt(17) lgkmcnt(1)
	v_mfma_f32_16x16x32_f16 v[102:105], v[68:71], v[110:113], v[102:105]
	s_waitcnt lgkmcnt(0)
	v_mfma_f32_16x16x32_f16 v[28:31], v[68:71], v[114:117], v[28:31]
	s_waitcnt vmcnt(16)
	v_mfma_f32_16x16x32_f16 v[36:39], v[72:75], v[110:113], v[36:39]
	v_mfma_f32_16x16x32_f16 v[32:35], v[72:75], v[114:117], v[32:35]
	s_setprio 0
	s_add_i32 s16, s13, 0x340
	s_and_b32 s17, s16, 0x3c0
	s_lshl_b32 s26, s17, 4
	s_lshl_b32 s16, s16, 4
	v_lshl_add_u64 v[56:57], v[20:21], 0, s[26:27]
	s_or_b32 s26, s16, 0x4000
	v_lshl_add_u64 v[64:65], v[20:21], 0, s[26:27]
	global_load_dwordx4 v[68:71], v[56:57], off
	global_load_dwordx4 v[72:75], v[64:65], off
	s_add_i32 s16, s14, 0xa0
	s_and_b32 s16, s16, 0x1e0
	v_lshl_add_u32 v23, s16, 1, v19
	ds_read_b128 v[110:113], v23 offset:4096
	ds_read_b128 v[114:117], v23 offset:20736
	s_setprio 1
	s_waitcnt vmcnt(17) lgkmcnt(1)
	v_mfma_f32_16x16x32_f16 v[102:105], v[76:79], v[110:113], v[102:105]
	s_waitcnt lgkmcnt(0)
	v_mfma_f32_16x16x32_f16 v[28:31], v[76:79], v[114:117], v[28:31]
	s_waitcnt vmcnt(16)
	v_mfma_f32_16x16x32_f16 v[36:39], v[82:85], v[110:113], v[36:39]
	v_mfma_f32_16x16x32_f16 v[32:35], v[82:85], v[114:117], v[32:35]
	s_setprio 0
	s_add_i32 s16, s13, 0x380
	s_and_b32 s17, s16, 0x3c0
	s_lshl_b32 s26, s17, 4
	s_lshl_b32 s16, s16, 4
	v_lshl_add_u64 v[56:57], v[20:21], 0, s[26:27]
	s_or_b32 s26, s16, 0x4000
	v_lshl_add_u64 v[64:65], v[20:21], 0, s[26:27]
	global_load_dwordx4 v[76:79], v[56:57], off
	global_load_dwordx4 v[82:85], v[64:65], off
	s_add_i32 s16, s14, 0xc0
	s_and_b32 s16, s16, 0x1e0
	v_lshl_add_u32 v23, s16, 1, v19
	ds_read_b128 v[110:113], v23 offset:4096
	ds_read_b128 v[114:117], v23 offset:20736
	s_setprio 1
	s_waitcnt vmcnt(17) lgkmcnt(1)
	v_mfma_f32_16x16x32_f16 v[102:105], v[14:17], v[110:113], v[102:105]
	s_waitcnt lgkmcnt(0)
	v_mfma_f32_16x16x32_f16 v[14:17], v[14:17], v[114:117], v[28:31]
	s_waitcnt vmcnt(16)
	v_mfma_f32_16x16x32_f16 v[28:31], v[10:13], v[110:113], v[36:39]
	v_mfma_f32_16x16x32_f16 v[10:13], v[10:13], v[114:117], v[32:35]
	s_setprio 0
	s_addk_i32 s13, 0x3c0
	s_and_b32 s16, s13, 0x3c0
	s_lshl_b32 s26, s16, 4
	s_lshl_b32 s13, s13, 4
	v_lshl_add_u64 v[56:57], v[20:21], 0, s[26:27]
	s_or_b32 s26, s13, 0x4000
	v_lshl_add_u64 v[20:21], v[20:21], 0, s[26:27]
	global_load_dwordx4 v[32:35], v[56:57], off
	global_load_dwordx4 v[36:39], v[20:21], off
	s_add_i32 s13, s14, 0xe0
	s_and_b32 s13, s13, 0x1e0
	v_lshl_add_u32 v20, s13, 1, v19
	ds_read_b128 v[110:113], v20 offset:4096
	ds_read_b128 v[114:117], v20 offset:20736
	s_setprio 1
	s_waitcnt vmcnt(17) lgkmcnt(1)
	v_mfma_f32_16x16x32_f16 v[102:105], v[6:9], v[110:113], v[102:105]
	s_waitcnt lgkmcnt(0)
	v_mfma_f32_16x16x32_f16 v[6:9], v[6:9], v[114:117], v[14:17]
	s_waitcnt vmcnt(16)
	v_mfma_f32_16x16x32_f16 v[14:17], v[2:5], v[110:113], v[28:31]
	v_mfma_f32_16x16x32_f16 v[2:5], v[2:5], v[114:117], v[10:13]
	s_setprio 0
	v_add_u32_e32 v20, s15, v19
	s_nop 0
	ds_read_b128 v[10:13], v20 offset:4096
	ds_read_b128 v[28:31], v20 offset:20736
	s_setprio 1
	s_waitcnt vmcnt(15) lgkmcnt(1)
	v_mfma_f32_16x16x32_f16 v[102:105], v[86:89], v[10:13], v[102:105]
	s_waitcnt lgkmcnt(0)
	v_mfma_f32_16x16x32_f16 v[6:9], v[86:89], v[28:31], v[6:9]
	s_waitcnt vmcnt(14)
	v_mfma_f32_16x16x32_f16 v[10:13], v[90:93], v[10:13], v[14:17]
	v_mfma_f32_16x16x32_f16 v[2:5], v[90:93], v[28:31], v[2:5]
	s_setprio 0
	s_add_i32 s13, s14, 0x120
	s_and_b32 s13, s13, 0x1e0
	v_lshl_add_u32 v20, s13, 1, v19
	ds_read_b128 v[14:17], v20 offset:4096
	ds_read_b128 v[28:31], v20 offset:20736
	s_setprio 1
	s_waitcnt vmcnt(13) lgkmcnt(1)
	v_mfma_f32_16x16x32_f16 v[86:89], v[98:101], v[14:17], v[102:105]
	s_waitcnt lgkmcnt(0)
	v_mfma_f32_16x16x32_f16 v[6:9], v[98:101], v[28:31], v[6:9]
	s_waitcnt vmcnt(12)
	v_mfma_f32_16x16x32_f16 v[10:13], v[106:109], v[14:17], v[10:13]
	v_mfma_f32_16x16x32_f16 v[2:5], v[106:109], v[28:31], v[2:5]
	s_setprio 0
	s_add_i32 s13, s14, 0x140
	s_and_b32 s13, s13, 0x1e0
	v_lshl_add_u32 v20, s13, 1, v19
	ds_read_b128 v[14:17], v20 offset:4096
	ds_read_b128 v[28:31], v20 offset:20736
	s_setprio 1
	s_waitcnt vmcnt(11) lgkmcnt(1)
	v_mfma_f32_16x16x32_f16 v[86:89], v[40:43], v[14:17], v[86:89]
	s_waitcnt lgkmcnt(0)
	v_mfma_f32_16x16x32_f16 v[6:9], v[40:43], v[28:31], v[6:9]
	s_waitcnt vmcnt(10)
	v_mfma_f32_16x16x32_f16 v[10:13], v[94:97], v[14:17], v[10:13]
	v_mfma_f32_16x16x32_f16 v[2:5], v[94:97], v[28:31], v[2:5]
	s_setprio 0
	s_add_i32 s13, s14, 0x160
	s_and_b32 s13, s13, 0x1e0
	v_lshl_add_u32 v20, s13, 1, v19
	ds_read_b128 v[14:17], v20 offset:4096
	ds_read_b128 v[28:31], v20 offset:20736
	s_setprio 1
	s_waitcnt vmcnt(9) lgkmcnt(1)
	v_mfma_f32_16x16x32_f16 v[40:43], v[44:47], v[14:17], v[86:89]
	s_waitcnt lgkmcnt(0)
	v_mfma_f32_16x16x32_f16 v[6:9], v[44:47], v[28:31], v[6:9]
	s_waitcnt vmcnt(8)
	v_mfma_f32_16x16x32_f16 v[10:13], v[48:51], v[14:17], v[10:13]
	v_mfma_f32_16x16x32_f16 v[2:5], v[48:51], v[28:31], v[2:5]
	s_setprio 0
	s_add_i32 s13, s14, 0x180
	s_and_b32 s13, s13, 0x1e0
	v_lshl_add_u32 v20, s13, 1, v19
	ds_read_b128 v[14:17], v20 offset:4096
	ds_read_b128 v[28:31], v20 offset:20736
	s_setprio 1
	s_waitcnt vmcnt(7) lgkmcnt(1)
	v_mfma_f32_16x16x32_f16 v[40:43], v[52:55], v[14:17], v[40:43]
	s_waitcnt lgkmcnt(0)
	v_mfma_f32_16x16x32_f16 v[6:9], v[52:55], v[28:31], v[6:9]
	s_waitcnt vmcnt(6)
	v_mfma_f32_16x16x32_f16 v[10:13], v[60:63], v[14:17], v[10:13]
	v_mfma_f32_16x16x32_f16 v[2:5], v[60:63], v[28:31], v[2:5]
	s_setprio 0
	s_add_i32 s13, s14, 0x1a0
	s_and_b32 s13, s13, 0x1e0
	v_lshl_add_u32 v20, s13, 1, v19
	ds_read_b128 v[14:17], v20 offset:4096
	ds_read_b128 v[28:31], v20 offset:20736
	s_setprio 1
	s_waitcnt vmcnt(5) lgkmcnt(1)
	v_mfma_f32_16x16x32_f16 v[40:43], v[68:71], v[14:17], v[40:43]
	s_waitcnt lgkmcnt(0)
	v_mfma_f32_16x16x32_f16 v[6:9], v[68:71], v[28:31], v[6:9]
	s_waitcnt vmcnt(4)
	v_mfma_f32_16x16x32_f16 v[10:13], v[72:75], v[14:17], v[10:13]
	v_mfma_f32_16x16x32_f16 v[2:5], v[72:75], v[28:31], v[2:5]
	s_setprio 0
	s_add_i32 s13, s14, 0x1c0
	s_and_b32 s13, s13, 0x1e0
	v_lshl_add_u32 v20, s13, 1, v19
	ds_read_b128 v[14:17], v20 offset:4096
	ds_read_b128 v[28:31], v20 offset:20736
	s_setprio 1
	s_waitcnt vmcnt(3) lgkmcnt(1)
	v_mfma_f32_16x16x32_f16 v[40:43], v[76:79], v[14:17], v[40:43]
	s_waitcnt lgkmcnt(0)
	v_mfma_f32_16x16x32_f16 v[6:9], v[76:79], v[28:31], v[6:9]
	s_waitcnt vmcnt(2)
	v_mfma_f32_16x16x32_f16 v[10:13], v[82:85], v[14:17], v[10:13]
	v_mfma_f32_16x16x32_f16 v[2:5], v[82:85], v[28:31], v[2:5]
	s_setprio 0
	s_addk_i32 s14, 0x1e0
	s_and_b32 s13, s14, 0x1e0
	v_lshl_add_u32 v20, s13, 1, v19
	ds_read_b128 v[14:17], v20 offset:4096
	ds_read_b128 v[28:31], v20 offset:20736
	s_setprio 1
	s_waitcnt vmcnt(1) lgkmcnt(1)
	v_mfma_f32_16x16x32_f16 v[40:43], v[32:35], v[14:17], v[40:43]
	s_waitcnt lgkmcnt(0)
	v_mfma_f32_16x16x32_f16 v[6:9], v[32:35], v[28:31], v[6:9]
	s_waitcnt vmcnt(0)
	v_mfma_f32_16x16x32_f16 v[10:13], v[36:39], v[14:17], v[10:13]
	v_mfma_f32_16x16x32_f16 v[2:5], v[36:39], v[28:31], v[2:5]
	s_setprio 0
	v_add_u32_e32 v19, v19, v22
	v_lshlrev_b32_e32 v20, 15, v118
	v_mov_b32_e32 v21, v67
	s_bfe_u32 s22, s2, 0x30003
	v_lshl_add_u64 v[20:21], s[10:11], 0, v[20:21]
	s_lshl_b32 s26, s22, 10
	v_lshl_add_u64 v[64:65], v[20:21], 0, v[58:59]
	v_lshl_add_u64 v[52:53], v[64:65], 0, s[26:27]
	v_add_co_u32_e32 v76, vcc, s29, v52
	s_lshl_b32 s53, s22, 6
	s_nop 0
	v_addc_co_u32_e32 v77, vcc, 0, v53, vcc
	s_mov_b32 s14, 0x14000
	v_mov_b32_e32 v22, 0x14000
	v_mul_u32_u24_e32 v23, 0x210, v81
	s_add_i32 s38, s53, 64
	v_lshlrev_b32_e32 v83, 2, v118
	s_movk_i32 s16, 0x1040
	s_movk_i32 s18, 0x840
	v_lshl_or_b32 v1, v1, 3, v22
	v_add3_u32 v84, v23, v18, s14
	s_and_b32 s14, s38, 0x1c0
	s_movk_i32 s20, 0x210
	s_mov_b32 s19, s27
	v_mad_u32_u24 v56, v118, s16, v58
	v_or_b32_e32 v22, 1, v83
	v_mad_u32_u24 v98, v118, s18, v1
	s_lshl_b32 s18, s14, 4
	v_mad_u32_u24 v99, v22, s12, v58
	v_mad_u32_u24 v85, v22, s20, v1
	v_lshl_add_u64 v[54:55], v[64:65], 0, s[18:19]
	s_add_i32 s12, s53, 0xc0
	s_and_b32 s2, s3, 0x7ffffff
	s_lshl_b32 s3, s22, 5
	s_and_b32 s39, s12, 0x1c0
	s_lshl_b32 s14, s39, 4
	s_add_i32 s39, s3, 32
	s_and_b32 s39, s39, 0xe0
	v_lshl_add_u32 v82, s39, 1, v84
	s_add_i32 s11, s53, 0x80
	s_lshl_b32 s16, s38, 4
	s_mov_b32 s21, s27
	s_and_b32 s30, s11, 0x1c0
	s_lshl_b32 s11, s11, 4
	s_or_b32 s20, s16, 0x2000
	s_mov_b32 s23, s27
	s_mov_b32 s31, s27
	s_mov_b32 s35, s27
	s_or_b32 s22, s16, 0x6000
	s_lshl_b32 s30, s30, 4
	s_or_b32 s34, s11, 0x2000
	v_lshl_add_u64 v[26:27], v[64:65], 0, s[20:21]
	v_lshl_add_u64 v[28:29], v[64:65], 0, s[22:23]
	v_lshl_add_u64 v[30:31], v[64:65], 0, s[30:31]
	v_lshl_add_u64 v[32:33], v[64:65], 0, s[34:35]
	s_mov_b64 s[40:41], 0x40000
	v_lshl_add_u64 v[60:61], v[64:65], 0, s[40:41]
	s_mov_b32 s37, s27
	s_or_b32 s36, s11, 0x6000
	v_lshl_add_u64 v[74:75], v[64:65], 0, s[36:37]
	s_mov_b32 s15, s27
	s_lshl_b32 s12, s12, 4
	v_lshl_add_u64 v[70:71], v[64:65], 0, s[14:15]
	s_mov_b32 s17, s27
	s_or_b32 s16, s12, 0x2000
	s_mov_b32 s13, s27
	s_or_b32 s12, s12, 0x6000
	v_lshl_add_u64 v[72:73], v[64:65], 0, s[16:17]
	v_lshl_add_u64 v[68:69], v[64:65], 0, s[12:13]
	v_add_u32_e32 v1, s53, v84
	s_xor_b32 s10, s26, 0x1000
	s_mov_b32 s11, s27
	s_mov_b32 s49, s27
	s_mov_b32 s51, s27
	s_mov_b32 s47, s27
	v_pk_add_f32 v[14:15], v[180:181], v[40:41]
	v_pk_add_f32 v[16:17], v[182:183], v[42:43]
	v_pk_add_f32 v[10:11], v[184:185], v[10:11]
	v_pk_add_f32 v[12:13], v[186:187], v[12:13]
	v_pk_add_f32 v[6:7], v[188:189], v[6:7]
	v_pk_add_f32 v[8:9], v[190:191], v[8:9]
	v_pk_add_f32 v[2:3], v[192:193], v[2:3]
	v_pk_add_f32 v[4:5], v[194:195], v[4:5]
	ds_write_b128 v19, v[14:17] offset:37376
	ds_write_b128 v19, v[10:13] offset:37440
	ds_write_b128 v19, v[6:9] offset:54016
	ds_write_b128 v19, v[2:5] offset:54080
	v_mov_b64_e32 v[34:35], v[204:205]
	v_mov_b64_e32 v[36:37], v[206:207]
	v_mov_b64_e32 v[38:39], v[208:209]
	v_mov_b64_e32 v[40:41], v[210:211]
	v_add_co_u32_e32 v2, vcc, s52, v52
	s_waitcnt lgkmcnt(0)
	s_nop 0
	v_addc_co_u32_e32 v3, vcc, 0, v53, vcc
	v_add_co_u32_e32 v4, vcc, s33, v52
	s_barrier
	s_nop 0
	v_addc_co_u32_e32 v5, vcc, 0, v53, vcc
	global_load_dwordx4 v[14:17], v[2:3], off
	global_load_dwordx4 v[18:21], v[4:5], off
	global_load_dwordx4 v[22:25], v[52:53], off
	global_load_dwordx4 v[10:13], v[54:55], off
	ds_read_b128 v[2:5], v56 offset:37376
	ds_read_b128 v[6:9], v99 offset:37376
	v_add_co_u32_e32 v78, vcc, s52, v54
	s_mov_b32 s43, s27
	s_waitcnt lgkmcnt(1)
	v_add_f32_e32 v42, v2, v3
	v_add_f32_e32 v42, v42, v4
	v_add_f32_e32 v42, v42, v5
	v_addc_co_u32_e32 v79, vcc, 0, v55, vcc
	s_nop 0
	v_add_f32_dpp v42, v42, v42 quad_perm:[1,0,3,2] row_mask:0xf bank_mask:0xf bound_ctrl:1
	s_mov_b32 s45, s27
	s_mov_b32 s41, s27
	v_add_f32_dpp v42, v42, v42 quad_perm:[2,3,0,1] row_mask:0xf bank_mask:0xf bound_ctrl:1
	v_lshl_add_u64 v[62:63], v[64:65], 0, s[10:11]
	v_lshl_add_u64 v[58:59], s[4:5], 0, v[58:59]
	v_add_f32_dpp v42, v42, v42 row_half_mirror row_mask:0xf bank_mask:0xf bound_ctrl:1
	v_lshl_add_u64 v[152:153], v[60:61], 0, s[26:27]
	v_lshl_add_u64 v[154:155], v[60:61], 0, s[18:19]
	v_add_f32_dpp v42, v42, v42 row_mirror row_mask:0xf bank_mask:0xf bound_ctrl:1
	v_lshl_add_u64 v[156:157], v[60:61], 0, s[20:21]
	v_readlane_b32 s8, v42, 16
	v_readlane_b32 s9, v42, 48
	v_readlane_b32 s6, v42, 0
	v_readlane_b32 s7, v42, 32
	v_mov_b32_e32 v42, s8
	v_mov_b32_e32 v43, s9
	v_pk_add_f32 v[42:43], s[6:7], v[42:43]
	s_mov_b32 s6, 0x3b800000
	v_add_f32_e32 v42, v42, v43
	v_mul_f32_e32 v42, 0x3b800000, v42
	v_pk_add_f32 v[86:87], v[2:3], v[42:43] op_sel_hi:[1,0] neg_lo:[0,1] neg_hi:[0,1]
	v_pk_add_f32 v[88:89], v[4:5], v[42:43] op_sel_hi:[1,0] neg_lo:[0,1] neg_hi:[0,1]
	v_pk_mul_f32 v[42:43], v[86:87], v[86:87]
	v_pk_mul_f32 v[44:45], v[88:89], v[88:89]
	v_add_f32_e32 v42, v42, v43
	v_add_f32_e32 v42, v44, v42
	s_waitcnt lgkmcnt(0)
	v_add_f32_e32 v44, v6, v7
	v_add_f32_e32 v42, v45, v42
	v_add_f32_e32 v44, v44, v8
	v_add_f32_e32 v44, v44, v9
	v_add_f32_dpp v42, v42, v42 quad_perm:[1,0,3,2] row_mask:0xf bank_mask:0xf bound_ctrl:1
	v_lshl_add_u64 v[158:159], v[60:61], 0, s[22:23]
	v_add_f32_dpp v44, v44, v44 quad_perm:[1,0,3,2] row_mask:0xf bank_mask:0xf bound_ctrl:1
	v_add_f32_dpp v42, v42, v42 quad_perm:[2,3,0,1] row_mask:0xf bank_mask:0xf bound_ctrl:1
	v_lshl_add_u64 v[160:161], v[60:61], 0, s[30:31]
	v_add_f32_dpp v44, v44, v44 quad_perm:[2,3,0,1] row_mask:0xf bank_mask:0xf bound_ctrl:1
	v_add_f32_dpp v42, v42, v42 row_half_mirror row_mask:0xf bank_mask:0xf bound_ctrl:1
	v_lshl_add_u64 v[162:163], v[60:61], 0, s[34:35]
	v_add_f32_dpp v44, v44, v44 row_half_mirror row_mask:0xf bank_mask:0xf bound_ctrl:1
	v_add_f32_dpp v42, v42, v42 row_mirror row_mask:0xf bank_mask:0xf bound_ctrl:1
	v_lshl_add_u64 v[164:165], v[60:61], 0, s[36:37]
	v_readlane_b32 s7, v42, 16
	v_readlane_b32 s39, v42, 48
	v_add_f32_dpp v44, v44, v44 row_mirror row_mask:0xf bank_mask:0xf bound_ctrl:1
	v_readlane_b32 s8, v42, 0
	v_readlane_b32 s9, v42, 32
	v_mov_b32_e32 v42, s7
	v_mov_b32_e32 v43, s39
	v_readlane_b32 s7, v44, 16
	v_readlane_b32 s39, v44, 48
	v_pk_add_f32 v[42:43], s[8:9], v[42:43]
	v_readlane_b32 s8, v44, 0
	v_readlane_b32 s9, v44, 32
	v_mov_b32_e32 v44, s7
	v_mov_b32_e32 v45, s39
	v_pk_add_f32 v[44:45], s[8:9], v[44:45]
	s_nop 0
	v_add_f32_e32 v44, v44, v45
	v_mul_f32_e32 v44, 0x3b800000, v44
	v_pk_add_f32 v[90:91], v[6:7], v[44:45] op_sel_hi:[1,0] neg_lo:[0,1] neg_hi:[0,1]
	v_pk_add_f32 v[92:93], v[8:9], v[44:45] op_sel_hi:[1,0] neg_lo:[0,1] neg_hi:[0,1]
	v_pk_mul_f32 v[46:47], v[90:91], v[90:91]
	v_pk_mul_f32 v[44:45], v[92:93], v[92:93]
	v_add_f32_e32 v46, v46, v47
	v_add_f32_e32 v44, v44, v46
	v_add_f32_e32 v44, v45, v44
	v_mov_b32_e32 v47, v42
	s_nop 0
	v_add_f32_dpp v44, v44, v44 quad_perm:[1,0,3,2] row_mask:0xf bank_mask:0xf bound_ctrl:1
	s_nop 1
	v_add_f32_dpp v44, v44, v44 quad_perm:[2,3,0,1] row_mask:0xf bank_mask:0xf bound_ctrl:1
	s_nop 1
	v_add_f32_dpp v44, v44, v44 row_half_mirror row_mask:0xf bank_mask:0xf bound_ctrl:1
	s_nop 1
	v_add_f32_dpp v44, v44, v44 row_mirror row_mask:0xf bank_mask:0xf bound_ctrl:1
	s_nop 0
	v_readlane_b32 s7, v44, 16
	v_readlane_b32 s39, v44, 48
	v_readlane_b32 s8, v44, 0
	v_readlane_b32 s9, v44, 32
	v_mov_b32_e32 v44, s7
	v_mov_b32_e32 v45, s39
	v_pk_add_f32 v[44:45], s[8:9], v[44:45]
	s_mov_b32 s8, 0x3727c5ac
	v_mov_b32_e32 v46, v44
	v_mov_b32_e32 v42, v45
	v_pk_add_f32 v[42:43], v[46:47], v[42:43]
	v_mov_b64_e32 v[94:95], s[8:9]
	v_pk_fma_f32 v[96:97], v[42:43], s[6:7], v[94:95] op_sel_hi:[1,0,0]
	s_mov_b32 s7, 0x800000
	v_mul_f32_e32 v42, 0x4b800000, v97
	v_cmp_gt_f32_e32 vcc, s7, v97
	s_nop 1
	v_cndmask_b32_e32 v42, v97, v42, vcc
	v_rsq_f32_e32 v97, v42
	global_load_dwordx4 v[54:57], v[26:27], off
	global_load_dwordx4 v[50:53], v[28:29], off
	global_load_dwordx4 v[46:49], v[30:31], off
	global_load_dwordx4 v[42:45], v[32:33], off
	v_mul_f32_e32 v26, 0x45800000, v97
	v_cndmask_b32_e32 v26, v97, v26, vcc
	v_pk_mul_f32 v[28:29], v[86:87], v[26:27] op_sel_hi:[1,0]
	v_cmp_gt_f32_e32 vcc, s7, v96
	s_waitcnt vmcnt(8)
	v_pk_fma_f32 v[28:29], v[34:35], v[28:29], v[38:39]
	v_pk_mul_f32 v[26:27], v[88:89], v[26:27] op_sel_hi:[1,0]
	v_cvt_pk_f16_f32 v28, v28, v29
	v_mul_f32_e32 v29, 0x4b800000, v96
	v_cndmask_b32_e32 v29, v96, v29, vcc
	v_rsq_f32_e32 v32, v29
	v_pk_fma_f32 v[26:27], v[36:37], v[26:27], v[40:41]
	s_nop 0
	v_cvt_pk_f16_f32 v29, v26, v27
	v_mul_f32_e32 v26, 0x45800000, v32
	v_cndmask_b32_e32 v26, v32, v26, vcc
	ds_write_b64 v98, v[28:29]
	v_pk_mul_f32 v[28:29], v[90:91], v[26:27] op_sel_hi:[1,0]
	v_pk_mul_f32 v[26:27], v[92:93], v[26:27] op_sel_hi:[1,0]
	v_pk_fma_f32 v[28:29], v[34:35], v[28:29], v[38:39]
	v_pk_fma_f32 v[26:27], v[36:37], v[26:27], v[40:41]
	v_cvt_pk_f16_f32 v28, v28, v29
	v_cvt_pk_f16_f32 v29, v26, v27
	ds_write_b64 v85, v[28:29]
	ds_read_b128 v[26:29], v99 offset:38416
	v_add_co_u32_e32 v102, vcc, s52, v30
	s_nop 1
	v_addc_co_u32_e32 v103, vcc, 0, v31, vcc
	ds_read_b128 v[30:33], v99 offset:39456
	s_waitcnt lgkmcnt(1)
	v_add_f32_e32 v86, v26, v27
	v_add_f32_e32 v86, v86, v28
	v_add_f32_e32 v86, v86, v29
	s_nop 1
	v_add_f32_dpp v86, v86, v86 quad_perm:[1,0,3,2] row_mask:0xf bank_mask:0xf bound_ctrl:1
	s_nop 1
	v_add_f32_dpp v86, v86, v86 quad_perm:[2,3,0,1] row_mask:0xf bank_mask:0xf bound_ctrl:1
	s_nop 1
	v_add_f32_dpp v86, v86, v86 row_half_mirror row_mask:0xf bank_mask:0xf bound_ctrl:1
	s_nop 1
	v_add_f32_dpp v86, v86, v86 row_mirror row_mask:0xf bank_mask:0xf bound_ctrl:1
	s_nop 0
	v_readlane_b32 s39, v86, 16
	v_readlane_b32 s40, v86, 48
	v_readlane_b32 s8, v86, 0
	v_readlane_b32 s9, v86, 32
	v_mov_b32_e32 v86, s39
	v_mov_b32_e32 v87, s40
	v_pk_add_f32 v[86:87], s[8:9], v[86:87]
	s_nop 0
	v_add_f32_e32 v86, v86, v87
	v_mul_f32_e32 v86, 0x3b800000, v86
	v_pk_add_f32 v[104:105], v[26:27], v[86:87] op_sel_hi:[1,0] neg_lo:[0,1] neg_hi:[0,1]
	v_pk_add_f32 v[106:107], v[28:29], v[86:87] op_sel_hi:[1,0] neg_lo:[0,1] neg_hi:[0,1]
	v_pk_mul_f32 v[88:89], v[104:105], v[104:105]
	v_pk_mul_f32 v[86:87], v[106:107], v[106:107]
	v_add_f32_e32 v88, v88, v89
	v_add_f32_e32 v86, v86, v88
	s_waitcnt lgkmcnt(0)
	v_add_f32_e32 v88, v30, v31
	v_add_f32_e32 v86, v87, v86
	v_add_f32_e32 v88, v88, v32
	v_add_f32_e32 v88, v88, v33
	v_add_f32_dpp v86, v86, v86 quad_perm:[1,0,3,2] row_mask:0xf bank_mask:0xf bound_ctrl:1
	s_nop 0
	v_add_f32_dpp v88, v88, v88 quad_perm:[1,0,3,2] row_mask:0xf bank_mask:0xf bound_ctrl:1
	v_add_f32_dpp v86, v86, v86 quad_perm:[2,3,0,1] row_mask:0xf bank_mask:0xf bound_ctrl:1
	s_nop 0
	v_add_f32_dpp v88, v88, v88 quad_perm:[2,3,0,1] row_mask:0xf bank_mask:0xf bound_ctrl:1
	v_add_f32_dpp v86, v86, v86 row_half_mirror row_mask:0xf bank_mask:0xf bound_ctrl:1
	s_nop 0
	v_add_f32_dpp v88, v88, v88 row_half_mirror row_mask:0xf bank_mask:0xf bound_ctrl:1
	v_add_f32_dpp v86, v86, v86 row_mirror row_mask:0xf bank_mask:0xf bound_ctrl:1
	s_nop 0
	v_readlane_b32 s39, v86, 16
	v_readlane_b32 s40, v86, 48
	v_add_f32_dpp v88, v88, v88 row_mirror row_mask:0xf bank_mask:0xf bound_ctrl:1
	v_readlane_b32 s8, v86, 0
	v_readlane_b32 s9, v86, 32
	v_mov_b32_e32 v86, s39
	v_mov_b32_e32 v87, s40
	v_readlane_b32 s39, v88, 16
	v_readlane_b32 s40, v88, 48
	v_pk_add_f32 v[86:87], s[8:9], v[86:87]
	v_readlane_b32 s8, v88, 0
	v_readlane_b32 s9, v88, 32
	v_mov_b32_e32 v88, s39
	v_mov_b32_e32 v89, s40
	v_pk_add_f32 v[88:89], s[8:9], v[88:89]
	s_nop 0
	v_add_f32_e32 v88, v88, v89
	v_mul_f32_e32 v88, 0x3b800000, v88
	v_pk_add_f32 v[108:109], v[30:31], v[88:89] op_sel_hi:[1,0] neg_lo:[0,1] neg_hi:[0,1]
	v_pk_add_f32 v[110:111], v[32:33], v[88:89] op_sel_hi:[1,0] neg_lo:[0,1] neg_hi:[0,1]
	v_pk_mul_f32 v[90:91], v[108:109], v[108:109]
	v_pk_mul_f32 v[88:89], v[110:111], v[110:111]
	v_add_f32_e32 v90, v90, v91
	v_add_f32_e32 v88, v88, v90
	v_add_f32_e32 v88, v89, v88
	v_mov_b32_e32 v91, v86
	s_nop 0
	v_add_f32_dpp v88, v88, v88 quad_perm:[1,0,3,2] row_mask:0xf bank_mask:0xf bound_ctrl:1
	s_nop 1
	v_add_f32_dpp v88, v88, v88 quad_perm:[2,3,0,1] row_mask:0xf bank_mask:0xf bound_ctrl:1
	s_nop 1
	v_add_f32_dpp v88, v88, v88 row_half_mirror row_mask:0xf bank_mask:0xf bound_ctrl:1
	s_nop 1
	v_add_f32_dpp v88, v88, v88 row_mirror row_mask:0xf bank_mask:0xf bound_ctrl:1
	s_nop 0
	v_readlane_b32 s39, v88, 16
	v_readlane_b32 s40, v88, 48
	v_readlane_b32 s8, v88, 0
	v_readlane_b32 s9, v88, 32
	v_mov_b32_e32 v88, s39
	v_mov_b32_e32 v89, s40
	v_pk_add_f32 v[88:89], s[8:9], v[88:89]
	s_mov_b32 s9, s27
	v_mov_b32_e32 v90, v88
	v_mov_b32_e32 v86, v89
	v_pk_add_f32 v[86:87], v[90:91], v[86:87]
	s_mov_b32 s39, s27
	v_pk_fma_f32 v[112:113], v[86:87], s[6:7], v[94:95] op_sel_hi:[1,0,0]
	s_add_i32 s6, s53, 0x140
	v_mul_f32_e32 v86, 0x4b800000, v113
	v_cmp_gt_f32_e32 vcc, s7, v113
	s_nop 1
	v_cndmask_b32_e32 v86, v113, v86, vcc
	v_rsq_f32_e32 v113, v86
	global_load_dwordx4 v[86:89], v[78:79], off
	global_load_dwordx4 v[90:93], v[102:103], off
	global_load_dwordx4 v[94:97], v[76:77], off
	global_load_dwordx4 v[98:101], v[74:75], off
	v_mul_f32_e32 v74, 0x45800000, v113
	v_cndmask_b32_e32 v74, v113, v74, vcc
	v_pk_mul_f32 v[76:77], v[104:105], v[74:75] op_sel_hi:[1,0]
	v_mul_f32_e32 v75, 0x4b800000, v112
	v_cmp_gt_f32_e32 vcc, s7, v112
	v_pk_fma_f32 v[76:77], v[34:35], v[76:77], v[38:39]
	s_and_b32 s7, s6, 0x1c0
	v_cndmask_b32_e32 v75, v112, v75, vcc
	v_rsq_f32_e32 v78, v75
	v_pk_mul_f32 v[74:75], v[106:107], v[74:75] op_sel_hi:[1,0]
	v_cvt_pk_f16_f32 v76, v76, v77
	v_pk_fma_f32 v[74:75], v[36:37], v[74:75], v[40:41]
	s_lshl_b32 s6, s6, 4
	v_cvt_pk_f16_f32 v77, v74, v75
	v_mul_f32_e32 v74, 0x45800000, v78
	v_cndmask_b32_e32 v74, v78, v74, vcc
	v_pk_mul_f32 v[78:79], v[108:109], v[74:75] op_sel_hi:[1,0]
	s_or_b32 s50, s6, 0x2000
	v_pk_fma_f32 v[34:35], v[34:35], v[78:79], v[38:39]
	v_pk_mul_f32 v[38:39], v[110:111], v[74:75] op_sel_hi:[1,0]
	v_add_co_u32_e32 v78, vcc, s52, v70
	v_pk_fma_f32 v[36:37], v[36:37], v[38:39], v[40:41]
	v_cvt_pk_f16_f32 v34, v34, v35
	v_cvt_pk_f16_f32 v35, v36, v37
	v_addc_co_u32_e32 v79, vcc, 0, v71, vcc
	ds_write2_b64 v85, v[76:77], v[34:35] offset0:66 offset1:132
	s_waitcnt lgkmcnt(0)
	s_barrier
	global_load_dwordx4 v[34:37], v[70:71], off
	global_load_dwordx4 v[38:41], v[72:73], off
	s_nop 0
	global_load_dwordx4 v[70:73], v[78:79], off
	global_load_dwordx4 v[74:77], v[68:69], off
	s_or_b32 s46, s6, 0x6000
	s_sub_i32 s6, s38, s3
	s_and_b32 s6, s6, 0xe0
	v_lshl_add_u32 v172, s6, 1, v84
	s_add_i32 s6, s53, 0x180
	s_lshl_b32 s48, s7, 4
	s_and_b32 s7, s6, 0x1c0
	s_lshl_b32 s6, s6, 4
	s_or_b32 s44, s6, 0x2000
	s_or_b32 s40, s6, 0x6000
	s_add_i32 s6, s3, 0x60
	s_and_b32 s6, s6, 0xe0
	v_lshl_add_u32 v173, s6, 1, v84
	s_add_i32 s6, s53, 0x1c0
	s_xor_b32 s53, s53, 0x100
	v_add_u32_e32 v174, s53, v84
	s_add_i32 s53, s3, 0xa0
	s_lshl_b32 s42, s7, 4
	s_and_b32 s7, s6, 0x1c0
	s_lshl_b32 s6, s6, 4
	s_and_b32 s53, s53, 0xe0
	s_lshl_b32 s8, s7, 4
	s_or_b32 s38, s6, 0x2000
	s_or_b32 s6, s6, 0x6000
	s_mov_b32 s7, s27
	v_lshl_add_u32 v175, s53, 1, v84
	s_add_i32 s53, s3, 0xc0
	s_addk_i32 s3, 0xe0
	v_lshl_add_u64 v[68:69], v[64:65], 0, s[48:49]
	v_lshl_add_u64 v[78:79], v[64:65], 0, s[50:51]
	v_lshl_add_u64 v[138:139], v[64:65], 0, s[46:47]
	v_lshl_add_u64 v[140:141], v[64:65], 0, s[42:43]
	v_lshl_add_u64 v[142:143], v[64:65], 0, s[44:45]
	v_lshl_add_u64 v[144:145], v[64:65], 0, s[40:41]
	v_lshl_add_u64 v[146:147], v[64:65], 0, s[8:9]
	v_lshl_add_u64 v[148:149], v[64:65], 0, s[38:39]
	v_lshl_add_u64 v[150:151], v[64:65], 0, s[6:7]
	s_and_b32 s53, s53, 0xe0
	s_and_b32 s3, s3, 0xe0
	v_add_u32_e32 v64, s28, v83
	v_mov_b32_e32 v65, v67
	v_lshl_add_u32 v176, s53, 1, v84
	v_lshl_add_u32 v177, s3, 1, v84
	v_lshlrev_b64 v[84:85], 10, v[64:65]
	ds_read_b128 v[102:105], v1
	ds_read_b128 v[106:109], v1 offset:8448
	v_lshl_add_u64 v[166:167], v[58:59], 0, v[84:85]
	v_or_b32_e32 v84, 1, v64
	v_mov_b32_e32 v85, v67
	v_lshlrev_b64 v[84:85], 10, v[84:85]
	v_lshl_add_u64 v[168:169], v[58:59], 0, v[84:85]
	v_or_b32_e32 v84, 2, v64
	v_mov_b32_e32 v85, v67
	v_or_b32_e32 v64, 3, v64
	v_lshlrev_b64 v[84:85], 10, v[84:85]
	v_lshlrev_b64 v[64:65], 10, v[64:65]
	v_lshl_add_u64 v[170:171], v[58:59], 0, v[84:85]
	v_lshl_add_u64 v[58:59], v[58:59], 0, v[64:65]
	s_setprio 1
	s_waitcnt vmcnt(13) lgkmcnt(1)
	v_mfma_f32_16x16x32_f16 v[110:113], v[102:105], v[22:25], 0
	s_waitcnt lgkmcnt(0)
	v_mfma_f32_16x16x32_f16 v[22:25], v[106:109], v[22:25], 0
	s_waitcnt vmcnt(5)
	v_mfma_f32_16x16x32_f16 v[114:117], v[102:105], v[94:97], 0
	v_mfma_f32_16x16x32_f16 v[94:97], v[106:109], v[94:97], 0
	v_mfma_f32_16x16x32_f16 v[118:121], v[102:105], v[14:17], 0
	v_mfma_f32_16x16x32_f16 v[14:17], v[106:109], v[14:17], 0
	v_mfma_f32_16x16x32_f16 v[102:105], v[102:105], v[18:21], 0
	v_mfma_f32_16x16x32_f16 v[18:21], v[106:109], v[18:21], 0
	s_setprio 0
	v_add_co_u32_e32 v64, vcc, s29, v62
	global_load_dwordx4 v[106:109], v[62:63], off
	s_nop 0
	v_addc_co_u32_e32 v65, vcc, 0, v63, vcc
	v_add_co_u32_e32 v84, vcc, s52, v62
	s_nop 1
	v_addc_co_u32_e32 v85, vcc, 0, v63, vcc
	v_add_co_u32_e32 v62, vcc, s33, v62
	global_load_dwordx4 v[122:125], v[64:65], off
	global_load_dwordx4 v[126:129], v[84:85], off
	v_addc_co_u32_e32 v63, vcc, 0, v63, vcc
	global_load_dwordx4 v[62:65], v[62:63], off
	ds_read_b128 v[130:133], v82
	ds_read_b128 v[134:137], v82 offset:8448
	s_setprio 1
	s_waitcnt lgkmcnt(1)
	v_mfma_f32_16x16x32_f16 v[110:113], v[130:133], v[10:13], v[110:113]
	s_waitcnt lgkmcnt(0)
	v_mfma_f32_16x16x32_f16 v[10:13], v[134:137], v[10:13], v[22:25]
	v_mfma_f32_16x16x32_f16 v[22:25], v[130:133], v[54:57], v[114:117]
	v_mfma_f32_16x16x32_f16 v[54:57], v[134:137], v[54:57], v[94:97]
	v_mfma_f32_16x16x32_f16 v[94:97], v[130:133], v[86:89], v[118:121]
	v_mfma_f32_16x16x32_f16 v[14:17], v[134:137], v[86:89], v[14:17]
	v_mfma_f32_16x16x32_f16 v[84:87], v[130:133], v[50:53], v[102:105]
	v_mfma_f32_16x16x32_f16 v[18:21], v[134:137], v[50:53], v[18:21]
	s_setprio 0
	global_load_dwordx4 v[50:53], v[68:69], off
	global_load_dwordx4 v[102:105], v[78:79], off
	v_add_co_u32_e32 v68, vcc, s52, v68
	s_nop 1
	v_addc_co_u32_e32 v69, vcc, 0, v69, vcc
	global_load_dwordx4 v[114:117], v[68:69], off
	global_load_dwordx4 v[118:121], v[138:139], off
	ds_read_b128 v[130:133], v172
	ds_read_b128 v[134:137], v172 offset:8448
	s_setprio 1
	s_waitcnt lgkmcnt(1)
	v_mfma_f32_16x16x32_f16 v[110:113], v[130:133], v[46:49], v[110:113]
	s_waitcnt lgkmcnt(0)
	v_mfma_f32_16x16x32_f16 v[10:13], v[134:137], v[46:49], v[10:13]
	v_mfma_f32_16x16x32_f16 v[22:25], v[130:133], v[42:45], v[22:25]
	v_mfma_f32_16x16x32_f16 v[42:45], v[134:137], v[42:45], v[54:57]
	v_mfma_f32_16x16x32_f16 v[46:49], v[130:133], v[90:93], v[94:97]
	v_mfma_f32_16x16x32_f16 v[14:17], v[134:137], v[90:93], v[14:17]
	s_waitcnt vmcnt(12)
	v_mfma_f32_16x16x32_f16 v[54:57], v[130:133], v[98:101], v[84:87]
	v_mfma_f32_16x16x32_f16 v[18:21], v[134:137], v[98:101], v[18:21]
	s_setprio 0
	v_add_co_u32_e32 v68, vcc, s52, v140
	global_load_dwordx4 v[84:87], v[140:141], off
	global_load_dwordx4 v[88:91], v[142:143], off
	v_addc_co_u32_e32 v69, vcc, 0, v141, vcc
	global_load_dwordx4 v[92:95], v[68:69], off
	global_load_dwordx4 v[96:99], v[144:145], off
	ds_read_b128 v[130:133], v173
	ds_read_b128 v[134:137], v173 offset:8448
	s_setprio 1
	s_waitcnt vmcnt(15) lgkmcnt(1)
	v_mfma_f32_16x16x32_f16 v[110:113], v[130:133], v[34:37], v[110:113]
	s_waitcnt lgkmcnt(0)
	v_mfma_f32_16x16x32_f16 v[10:13], v[134:137], v[34:37], v[10:13]
	s_waitcnt vmcnt(14)
	v_mfma_f32_16x16x32_f16 v[22:25], v[130:133], v[38:41], v[22:25]
	v_mfma_f32_16x16x32_f16 v[34:37], v[134:137], v[38:41], v[42:45]
	s_waitcnt vmcnt(13)
	v_mfma_f32_16x16x32_f16 v[38:41], v[130:133], v[70:73], v[46:49]
	v_mfma_f32_16x16x32_f16 v[14:17], v[134:137], v[70:73], v[14:17]
	s_waitcnt vmcnt(12)
	v_mfma_f32_16x16x32_f16 v[42:45], v[130:133], v[74:77], v[54:57]
	v_mfma_f32_16x16x32_f16 v[18:21], v[134:137], v[74:77], v[18:21]
	s_setprio 0
	v_add_co_u32_e32 v68, vcc, s52, v146
	global_load_dwordx4 v[46:49], v[146:147], off
	global_load_dwordx4 v[54:57], v[148:149], off
	v_addc_co_u32_e32 v69, vcc, 0, v147, vcc
	global_load_dwordx4 v[68:71], v[68:69], off
	s_nop 0
	global_load_dwordx4 v[72:75], v[150:151], off
	ds_read_b128 v[76:79], v174
	ds_read_b128 v[130:133], v174 offset:8448
	s_setprio 1
	s_waitcnt vmcnt(15) lgkmcnt(1)
	v_mfma_f32_16x16x32_f16 v[110:113], v[76:79], v[106:109], v[110:113]
	s_waitcnt lgkmcnt(0)
	v_mfma_f32_16x16x32_f16 v[10:13], v[130:133], v[106:109], v[10:13]
	s_waitcnt vmcnt(14)
	v_mfma_f32_16x16x32_f16 v[22:25], v[76:79], v[122:125], v[22:25]
	v_mfma_f32_16x16x32_f16 v[34:37], v[130:133], v[122:125], v[34:37]
	s_waitcnt vmcnt(13)
	v_mfma_f32_16x16x32_f16 v[38:41], v[76:79], v[126:129], v[38:41]
	v_mfma_f32_16x16x32_f16 v[14:17], v[130:133], v[126:129], v[14:17]
	s_waitcnt vmcnt(12)
	v_mfma_f32_16x16x32_f16 v[42:45], v[76:79], v[62:65], v[42:45]
	v_mfma_f32_16x16x32_f16 v[18:21], v[130:133], v[62:65], v[18:21]
	s_setprio 0
	ds_read_b128 v[62:65], v175
	ds_read_b128 v[76:79], v175 offset:8448
	s_setprio 1
	s_waitcnt vmcnt(11) lgkmcnt(1)
	v_mfma_f32_16x16x32_f16 v[106:109], v[62:65], v[50:53], v[110:113]
	s_waitcnt lgkmcnt(0)
	v_mfma_f32_16x16x32_f16 v[10:13], v[76:79], v[50:53], v[10:13]
	s_waitcnt vmcnt(10)
	v_mfma_f32_16x16x32_f16 v[22:25], v[62:65], v[102:105], v[22:25]
	v_mfma_f32_16x16x32_f16 v[34:37], v[76:79], v[102:105], v[34:37]
	s_waitcnt vmcnt(9)
	v_mfma_f32_16x16x32_f16 v[38:41], v[62:65], v[114:117], v[38:41]
	v_mfma_f32_16x16x32_f16 v[14:17], v[76:79], v[114:117], v[14:17]
	s_waitcnt vmcnt(8)
	v_mfma_f32_16x16x32_f16 v[42:45], v[62:65], v[118:121], v[42:45]
	v_mfma_f32_16x16x32_f16 v[18:21], v[76:79], v[118:121], v[18:21]
	s_setprio 0
	ds_read_b128 v[50:53], v176
	ds_read_b128 v[62:65], v176 offset:8448
	s_setprio 1
	s_waitcnt vmcnt(7) lgkmcnt(1)
	v_mfma_f32_16x16x32_f16 v[76:79], v[50:53], v[84:87], v[106:109]
	s_waitcnt lgkmcnt(0)
	v_mfma_f32_16x16x32_f16 v[10:13], v[62:65], v[84:87], v[10:13]
	s_waitcnt vmcnt(6)
	v_mfma_f32_16x16x32_f16 v[22:25], v[50:53], v[88:91], v[22:25]
	v_mfma_f32_16x16x32_f16 v[34:37], v[62:65], v[88:91], v[34:37]
	s_waitcnt vmcnt(5)
	v_mfma_f32_16x16x32_f16 v[38:41], v[50:53], v[92:95], v[38:41]
	v_mfma_f32_16x16x32_f16 v[14:17], v[62:65], v[92:95], v[14:17]
	s_waitcnt vmcnt(4)
	v_mfma_f32_16x16x32_f16 v[42:45], v[50:53], v[96:99], v[42:45]
	v_mfma_f32_16x16x32_f16 v[18:21], v[62:65], v[96:99], v[18:21]
	s_setprio 0
	ds_read_b128 v[50:53], v177
	ds_read_b128 v[62:65], v177 offset:8448
	s_setprio 1
	s_waitcnt vmcnt(3) lgkmcnt(1)
	v_mfma_f32_16x16x32_f16 v[76:79], v[50:53], v[46:49], v[76:79]
	s_waitcnt lgkmcnt(0)
	v_mfma_f32_16x16x32_f16 v[10:13], v[62:65], v[46:49], v[10:13]
	s_waitcnt vmcnt(2)
	v_mfma_f32_16x16x32_f16 v[22:25], v[50:53], v[54:57], v[22:25]
	v_mfma_f32_16x16x32_f16 v[34:37], v[62:65], v[54:57], v[34:37]
	s_waitcnt vmcnt(1)
	v_mfma_f32_16x16x32_f16 v[38:41], v[50:53], v[68:71], v[38:41]
	v_mfma_f32_16x16x32_f16 v[14:17], v[62:65], v[68:71], v[14:17]
	s_waitcnt vmcnt(0)
	v_mfma_f32_16x16x32_f16 v[42:45], v[50:53], v[72:75], v[42:45]
	v_mfma_f32_16x16x32_f16 v[18:21], v[62:65], v[72:75], v[18:21]
	s_setprio 0
	v_add_co_u32_e32 v108, vcc, s29, v152
	v_and_b32_e32 v67, 0x1c0, v0
	s_nop 0
	v_addc_co_u32_e32 v109, vcc, 0, v153, vcc
	v_add_co_u32_e32 v46, vcc, s52, v152
	s_movk_i32 s4, 0x50
	s_nop 0
	v_addc_co_u32_e32 v47, vcc, 0, v153, vcc
	v_add_co_u32_e32 v68, vcc, s33, v152
	v_or_b32_e32 v116, 16, v67
	s_nop 0
	v_addc_co_u32_e32 v69, vcc, 0, v153, vcc
	v_add_co_u32_e32 v110, vcc, s52, v154
	global_load_dwordx4 v[46:49], v[46:47], off
	s_nop 0
	global_load_dwordx4 v[50:53], v[68:69], off
	global_load_dwordx4 v[54:57], v[152:153], off
	global_load_dwordx4 v[62:65], v[154:155], off
	v_addc_co_u32_e32 v111, vcc, 0, v155, vcc
	v_add_co_u32_e32 v112, vcc, s52, v160
	global_load_dwordx4 v[68:71], v[156:157], off
	global_load_dwordx4 v[72:75], v[158:159], off
	global_load_dwordx4 v[84:87], v[160:161], off
	global_load_dwordx4 v[88:91], v[162:163], off
	v_addc_co_u32_e32 v113, vcc, 0, v161, vcc
	global_load_dwordx4 v[92:95], v[110:111], off
	global_load_dwordx4 v[96:99], v[112:113], off
	global_load_dwordx4 v[100:103], v[108:109], off
	global_load_dwordx4 v[104:107], v[164:165], off
	s_nop 0
	global_store_dwordx4 v[166:167], v[2:5], off
	global_store_dwordx4 v[168:169], v[6:9], off
	global_store_dwordx4 v[170:171], v[26:29], off
	global_store_dwordx4 v[58:59], v[30:33], off
	v_and_b32_e32 v4, 0x1cf, v0
	v_cvt_pk_f16_f32 v3, v78, v79
	v_cvt_pk_f16_f32 v2, v76, v77
	v_mad_u32_u24 v4, v4, s4, v80
	v_or_b32_e32 v5, v116, v81
	v_or_b32_e32 v117, 32, v67
	ds_write_b64 v4, v[2:3]
	v_cvt_pk_f16_f32 v3, v24, v25
	v_cvt_pk_f16_f32 v2, v22, v23
	v_mad_u32_u24 v5, v5, s4, v80
	v_or_b32_e32 v6, v117, v81
	v_or_b32_e32 v118, 48, v67
	ds_write_b64 v5, v[2:3]
	v_cvt_pk_f16_f32 v3, v40, v41
	v_cvt_pk_f16_f32 v2, v38, v39
	v_mad_u32_u24 v6, v6, s4, v80
	v_or_b32_e32 v7, v118, v81
	ds_write_b64 v6, v[2:3]
	v_cvt_pk_f16_f32 v3, v44, v45
	v_cvt_pk_f16_f32 v2, v42, v43
	v_mad_u32_u24 v7, v7, s4, v80
	ds_write_b64 v7, v[2:3]
	v_cvt_pk_f16_f32 v3, v12, v13
	v_cvt_pk_f16_f32 v2, v10, v11
	ds_write_b64 v4, v[2:3] offset:32
	v_cvt_pk_f16_f32 v3, v36, v37
	v_cvt_pk_f16_f32 v2, v34, v35
	ds_write_b64 v5, v[2:3] offset:32
	v_cvt_pk_f16_f32 v3, v16, v17
	v_cvt_pk_f16_f32 v2, v14, v15
	v_lshl_add_u64 v[10:11], v[60:61], 0, s[14:15]
	ds_write_b64 v6, v[2:3] offset:32
	v_cvt_pk_f16_f32 v2, v18, v19
	v_add_co_u32_e32 v18, vcc, s52, v10
	v_cvt_pk_f16_f32 v3, v20, v21
	v_lshl_add_u64 v[12:13], v[60:61], 0, s[16:17]
	v_addc_co_u32_e32 v19, vcc, 0, v11, vcc
	ds_write_b64 v7, v[2:3] offset:32
	s_waitcnt lgkmcnt(0)
	s_barrier
	global_load_dwordx4 v[2:5], v[10:11], off
	global_load_dwordx4 v[6:9], v[12:13], off
	v_lshl_add_u64 v[20:21], v[60:61], 0, s[12:13]
	global_load_dwordx4 v[10:13], v[18:19], off
	global_load_dwordx4 v[14:17], v[20:21], off
	ds_read_b128 v[18:21], v1
	ds_read_b128 v[22:25], v1 offset:8448
	s_mov_b32 s3, s27
	s_setprio 1
	s_waitcnt vmcnt(17) lgkmcnt(1)
	v_mfma_f32_16x16x32_f16 v[26:29], v[18:21], v[54:57], 0
	s_waitcnt lgkmcnt(0)
	v_mfma_f32_16x16x32_f16 v[30:33], v[22:25], v[54:57], 0
	s_waitcnt vmcnt(9)
	v_mfma_f32_16x16x32_f16 v[34:37], v[18:21], v[100:103], 0
	v_mfma_f32_16x16x32_f16 v[38:41], v[22:25], v[100:103], 0
	v_mfma_f32_16x16x32_f16 v[42:45], v[18:21], v[46:49], 0
	v_mfma_f32_16x16x32_f16 v[46:49], v[22:25], v[46:49], 0
	v_mfma_f32_16x16x32_f16 v[18:21], v[18:21], v[50:53], 0
	v_mfma_f32_16x16x32_f16 v[22:25], v[22:25], v[50:53], 0
	s_setprio 0
	v_lshl_add_u64 v[58:59], v[60:61], 0, s[10:11]
	v_add_co_u32_e32 v76, vcc, s29, v58
	s_nop 1
	v_addc_co_u32_e32 v77, vcc, 0, v59, vcc
	v_add_co_u32_e32 v108, vcc, s52, v58
	global_load_dwordx4 v[50:53], v[58:59], off
	global_load_dwordx4 v[54:57], v[76:77], off
	v_addc_co_u32_e32 v109, vcc, 0, v59, vcc
	v_add_co_u32_e32 v58, vcc, s33, v58
	s_nop 1
	v_addc_co_u32_e32 v59, vcc, 0, v59, vcc
	global_load_dwordx4 v[76:79], v[108:109], off
	global_load_dwordx4 v[100:103], v[58:59], off
	ds_read_b128 v[108:111], v82
	ds_read_b128 v[112:115], v82 offset:8448
	s_setprio 1
	s_waitcnt lgkmcnt(1)
	v_mfma_f32_16x16x32_f16 v[26:29], v[108:111], v[62:65], v[26:29]
	s_waitcnt lgkmcnt(0)
	v_mfma_f32_16x16x32_f16 v[30:33], v[112:115], v[62:65], v[30:33]
	v_mfma_f32_16x16x32_f16 v[34:37], v[108:111], v[68:71], v[34:37]
	v_mfma_f32_16x16x32_f16 v[38:41], v[112:115], v[68:71], v[38:41]
	v_mfma_f32_16x16x32_f16 v[42:45], v[108:111], v[92:95], v[42:45]
	v_mfma_f32_16x16x32_f16 v[46:49], v[112:115], v[92:95], v[46:49]
	v_mfma_f32_16x16x32_f16 v[18:21], v[108:111], v[72:75], v[18:21]
	v_mfma_f32_16x16x32_f16 v[22:25], v[112:115], v[72:75], v[22:25]
	s_setprio 0
	v_lshl_add_u64 v[58:59], v[60:61], 0, s[48:49]
	v_lshl_add_u64 v[72:73], v[60:61], 0, s[50:51]
	global_load_dwordx4 v[62:65], v[58:59], off
	global_load_dwordx4 v[68:71], v[72:73], off
	v_add_co_u32_e32 v58, vcc, s52, v58
	v_lshl_add_u64 v[82:83], v[60:61], 0, s[46:47]
	s_nop 0
	v_addc_co_u32_e32 v59, vcc, 0, v59, vcc
	global_load_dwordx4 v[72:75], v[58:59], off
	global_load_dwordx4 v[92:95], v[82:83], off
	ds_read_b128 v[108:111], v172
	ds_read_b128 v[112:115], v172 offset:8448
	s_setprio 1
	s_waitcnt lgkmcnt(1)
	v_mfma_f32_16x16x32_f16 v[26:29], v[108:111], v[84:87], v[26:29]
	s_waitcnt lgkmcnt(0)
	v_mfma_f32_16x16x32_f16 v[30:33], v[112:115], v[84:87], v[30:33]
	v_mfma_f32_16x16x32_f16 v[34:37], v[108:111], v[88:91], v[34:37]
	v_mfma_f32_16x16x32_f16 v[38:41], v[112:115], v[88:91], v[38:41]
	v_mfma_f32_16x16x32_f16 v[42:45], v[108:111], v[96:99], v[42:45]
	v_mfma_f32_16x16x32_f16 v[46:49], v[112:115], v[96:99], v[46:49]
	s_waitcnt vmcnt(16)
	v_mfma_f32_16x16x32_f16 v[18:21], v[108:111], v[104:107], v[18:21]
	v_mfma_f32_16x16x32_f16 v[22:25], v[112:115], v[104:107], v[22:25]
	s_setprio 0
	v_lshl_add_u64 v[58:59], v[60:61], 0, s[42:43]
	v_lshl_add_u64 v[90:91], v[60:61], 0, s[44:45]
	global_load_dwordx4 v[82:85], v[58:59], off
	global_load_dwordx4 v[86:89], v[90:91], off
	v_add_co_u32_e32 v58, vcc, s52, v58
	v_lshl_add_u64 v[90:91], v[60:61], 0, s[40:41]
	s_nop 0
	v_addc_co_u32_e32 v59, vcc, 0, v59, vcc
	global_load_dwordx4 v[96:99], v[58:59], off
	global_load_dwordx4 v[104:107], v[90:91], off
	ds_read_b128 v[108:111], v173
	ds_read_b128 v[112:115], v173 offset:8448
	s_setprio 1
	s_waitcnt vmcnt(15) lgkmcnt(1)
	v_mfma_f32_16x16x32_f16 v[26:29], v[108:111], v[2:5], v[26:29]
	s_waitcnt lgkmcnt(0)
	v_mfma_f32_16x16x32_f16 v[2:5], v[112:115], v[2:5], v[30:33]
	s_waitcnt vmcnt(14)
	v_mfma_f32_16x16x32_f16 v[30:33], v[108:111], v[6:9], v[34:37]
	v_mfma_f32_16x16x32_f16 v[6:9], v[112:115], v[6:9], v[38:41]
	s_waitcnt vmcnt(13)
	v_mfma_f32_16x16x32_f16 v[34:37], v[108:111], v[10:13], v[42:45]
	v_mfma_f32_16x16x32_f16 v[10:13], v[112:115], v[10:13], v[46:49]
	s_waitcnt vmcnt(12)
	v_mfma_f32_16x16x32_f16 v[18:21], v[108:111], v[14:17], v[18:21]
	v_mfma_f32_16x16x32_f16 v[14:17], v[112:115], v[14:17], v[22:25]
	s_setprio 0
	v_lshl_add_u64 v[42:43], v[60:61], 0, s[8:9]
	v_add_co_u32_e32 v58, vcc, s52, v42
	v_lshl_add_u64 v[44:45], v[60:61], 0, s[38:39]
	s_nop 0
	v_addc_co_u32_e32 v59, vcc, 0, v43, vcc
	global_load_dwordx4 v[22:25], v[42:43], off
	global_load_dwordx4 v[38:41], v[44:45], off
	v_lshl_add_u64 v[60:61], v[60:61], 0, s[6:7]
	global_load_dwordx4 v[42:45], v[58:59], off
	global_load_dwordx4 v[46:49], v[60:61], off
	ds_read_b128 v[58:61], v174
	ds_read_b128 v[108:111], v174 offset:8448
	s_setprio 1
	s_waitcnt vmcnt(15) lgkmcnt(1)
	v_mfma_f32_16x16x32_f16 v[26:29], v[58:61], v[50:53], v[26:29]
	s_waitcnt lgkmcnt(0)
	v_mfma_f32_16x16x32_f16 v[2:5], v[108:111], v[50:53], v[2:5]
	s_waitcnt vmcnt(14)
	v_mfma_f32_16x16x32_f16 v[30:33], v[58:61], v[54:57], v[30:33]
	v_mfma_f32_16x16x32_f16 v[6:9], v[108:111], v[54:57], v[6:9]
	s_waitcnt vmcnt(13)
	v_mfma_f32_16x16x32_f16 v[34:37], v[58:61], v[76:79], v[34:37]
	v_mfma_f32_16x16x32_f16 v[10:13], v[108:111], v[76:79], v[10:13]
	s_waitcnt vmcnt(12)
	v_mfma_f32_16x16x32_f16 v[18:21], v[58:61], v[100:103], v[18:21]
	v_mfma_f32_16x16x32_f16 v[14:17], v[108:111], v[100:103], v[14:17]
	s_setprio 0
	ds_read_b128 v[50:53], v175
	ds_read_b128 v[54:57], v175 offset:8448
	s_setprio 1
	s_waitcnt vmcnt(11) lgkmcnt(1)
	v_mfma_f32_16x16x32_f16 v[26:29], v[50:53], v[62:65], v[26:29]
	s_waitcnt lgkmcnt(0)
	v_mfma_f32_16x16x32_f16 v[2:5], v[54:57], v[62:65], v[2:5]
	s_waitcnt vmcnt(10)
	v_mfma_f32_16x16x32_f16 v[30:33], v[50:53], v[68:71], v[30:33]
	v_mfma_f32_16x16x32_f16 v[6:9], v[54:57], v[68:71], v[6:9]
	s_waitcnt vmcnt(9)
	v_mfma_f32_16x16x32_f16 v[34:37], v[50:53], v[72:75], v[34:37]
	v_mfma_f32_16x16x32_f16 v[10:13], v[54:57], v[72:75], v[10:13]
	s_waitcnt vmcnt(8)
	v_mfma_f32_16x16x32_f16 v[18:21], v[50:53], v[92:95], v[18:21]
	v_mfma_f32_16x16x32_f16 v[14:17], v[54:57], v[92:95], v[14:17]
	s_setprio 0
	ds_read_b128 v[50:53], v176
	ds_read_b128 v[54:57], v176 offset:8448
	s_setprio 1
	s_waitcnt vmcnt(7) lgkmcnt(1)
	v_mfma_f32_16x16x32_f16 v[26:29], v[50:53], v[82:85], v[26:29]
	s_waitcnt lgkmcnt(0)
	v_mfma_f32_16x16x32_f16 v[2:5], v[54:57], v[82:85], v[2:5]
	s_waitcnt vmcnt(6)
	v_mfma_f32_16x16x32_f16 v[30:33], v[50:53], v[86:89], v[30:33]
	v_mfma_f32_16x16x32_f16 v[6:9], v[54:57], v[86:89], v[6:9]
	s_waitcnt vmcnt(5)
	v_mfma_f32_16x16x32_f16 v[34:37], v[50:53], v[96:99], v[34:37]
	v_mfma_f32_16x16x32_f16 v[58:61], v[54:57], v[96:99], v[10:13]
	s_waitcnt vmcnt(4)
	v_mfma_f32_16x16x32_f16 v[18:21], v[50:53], v[104:107], v[18:21]
	v_mfma_f32_16x16x32_f16 v[50:53], v[54:57], v[104:107], v[14:17]
	s_setprio 0
	ds_read_b128 v[54:57], v177
	ds_read_b128 v[62:65], v177 offset:8448
	s_setprio 1
	s_waitcnt vmcnt(3) lgkmcnt(1)
	v_mfma_f32_16x16x32_f16 v[26:29], v[54:57], v[22:25], v[26:29]
	s_waitcnt lgkmcnt(0)
	v_mfma_f32_16x16x32_f16 v[14:17], v[62:65], v[22:25], v[2:5]
	s_waitcnt vmcnt(2)
	v_mfma_f32_16x16x32_f16 v[22:25], v[54:57], v[38:41], v[30:33]
	v_mfma_f32_16x16x32_f16 v[10:13], v[62:65], v[38:41], v[6:9]
	s_waitcnt vmcnt(1)
	v_mfma_f32_16x16x32_f16 v[30:33], v[54:57], v[42:45], v[34:37]
	v_mfma_f32_16x16x32_f16 v[6:9], v[62:65], v[42:45], v[58:61]
	s_waitcnt vmcnt(0)
	v_mfma_f32_16x16x32_f16 v[34:37], v[54:57], v[46:49], v[18:21]
	v_mfma_f32_16x16x32_f16 v[2:5], v[62:65], v[46:49], v[50:53]
	s_setprio 0
	s_nop 1
	v_mul_u32_u24_e32 v52, 0x50, v0
	ds_read_b128 v[18:21], v52
	s_lshl_b64 s[2:3], s[2:3], 15
	v_or_b32_e32 v0, s2, v66
	v_mov_b32_e32 v1, s3
	v_lshl_add_u64 v[50:51], s[24:25], 0, v[0:1]
	ds_read_b128 v[38:41], v52 offset:16
	ds_read_b128 v[42:45], v52 offset:32
	ds_read_b128 v[46:49], v52 offset:48
	s_waitcnt lgkmcnt(3)
	global_store_dwordx4 v[50:51], v[18:21], off
	s_nop 1
	v_add_co_u32_e32 v18, vcc, s29, v50
	s_nop 1
	v_addc_co_u32_e32 v19, vcc, 0, v51, vcc
	s_waitcnt lgkmcnt(2)
	global_store_dwordx4 v[18:19], v[38:41], off
	v_or_b32_e32 v18, 0x4000, v0
	v_mov_b32_e32 v19, s3
	v_lshl_add_u64 v[20:21], s[24:25], 0, v[18:19]
	s_waitcnt lgkmcnt(1)
	global_store_dwordx4 v[20:21], v[42:45], off
	v_mul_f32_e32 v20, 0xbfb8aa3b, v26
	v_exp_f32_e32 v38, v20
	v_add_co_u32_e32 v20, vcc, s33, v50
	v_or_b32_e32 v39, 0x200, v81
	s_nop 0
	v_addc_co_u32_e32 v21, vcc, 0, v51, vcc
	s_waitcnt lgkmcnt(0)
	global_store_dwordx4 v[20:21], v[46:49], off
	v_add_f32_e32 v20, 1.0, v38
	v_rcp_f32_e32 v20, v20
	v_mul_f32_e32 v21, 0xbfb8aa3b, v27
	v_mul_f32_e32 v38, 0xbfb8aa3b, v28
	v_exp_f32_e32 v21, v21
	v_exp_f32_e32 v38, v38
	v_fma_mixlo_f16 v40, v26, v20, 0
	v_mul_f32_e32 v26, 0xbfb8aa3b, v29
	v_add_f32_e32 v20, 1.0, v21
	v_add_f32_e32 v21, 1.0, v38
	v_exp_f32_e32 v38, v26
	v_rcp_f32_e32 v20, v20
	v_rcp_f32_e32 v21, v21
	v_mov_b32_e32 v26, v27
	v_mov_b32_e32 v27, v28
	v_add_f32_e32 v28, 1.0, v38
	v_rcp_f32_e32 v28, v28
	v_pk_mul_f32 v[20:21], v[26:27], v[20:21]
	v_or_b32_e32 v27, v39, v67
	v_cvt_pk_f16_f32 v21, v20, v21
	v_fma_mixlo_f16 v26, v29, v28, 0
	v_pack_b32_f16 v20, v40, v21
	v_alignbit_b32 v21, v26, v21, 16
	v_mul_f32_e32 v26, 0xbfb8aa3b, v22
	v_exp_f32_e32 v26, v26
	v_mad_u32_u24 v27, v27, s4, v80
	ds_write_b64 v27, v[20:21]
	v_mul_f32_e32 v21, 0xbfb8aa3b, v23
	v_add_f32_e32 v20, 1.0, v26
	v_rcp_f32_e32 v20, v20
	v_mul_f32_e32 v26, 0xbfb8aa3b, v24
	v_exp_f32_e32 v21, v21
	v_exp_f32_e32 v26, v26
	v_fma_mixlo_f16 v28, v22, v20, 0
	v_mul_f32_e32 v22, 0xbfb8aa3b, v25
	v_add_f32_e32 v20, 1.0, v21
	v_add_f32_e32 v21, 1.0, v26
	v_exp_f32_e32 v26, v22
	v_rcp_f32_e32 v20, v20
	v_rcp_f32_e32 v21, v21
	v_mov_b32_e32 v22, v23
	v_mov_b32_e32 v23, v24
	v_add_f32_e32 v24, 1.0, v26
	v_rcp_f32_e32 v24, v24
	v_pk_mul_f32 v[20:21], v[22:23], v[20:21]
	v_or_b32_e32 v23, v116, v39
	v_cvt_pk_f16_f32 v21, v20, v21
	v_fma_mixlo_f16 v22, v25, v24, 0
	v_pack_b32_f16 v20, v28, v21
	v_alignbit_b32 v21, v22, v21, 16
	v_mul_f32_e32 v22, 0xbfb8aa3b, v30
	v_exp_f32_e32 v22, v22
	v_mad_u32_u24 v24, v23, s4, v80
	ds_write_b64 v24, v[20:21]
	v_mul_f32_e32 v21, 0xbfb8aa3b, v31
	v_add_f32_e32 v20, 1.0, v22
	v_mul_f32_e32 v22, 0xbfb8aa3b, v32
	v_rcp_f32_e32 v20, v20
	v_exp_f32_e32 v21, v21
	v_exp_f32_e32 v22, v22
	v_mov_b32_e32 v23, v32
	v_fma_mixlo_f16 v25, v30, v20, 0
	v_add_f32_e32 v20, 1.0, v21
	v_add_f32_e32 v21, 1.0, v22
	v_mul_f32_e32 v22, 0xbfb8aa3b, v33
	v_exp_f32_e32 v26, v22
	v_rcp_f32_e32 v20, v20
	v_rcp_f32_e32 v21, v21
	v_mov_b32_e32 v22, v31
	v_add_f32_e32 v26, 1.0, v26
	v_rcp_f32_e32 v26, v26
	v_pk_mul_f32 v[20:21], v[22:23], v[20:21]
	v_or_b32_e32 v23, v117, v39
	v_cvt_pk_f16_f32 v21, v20, v21
	v_fma_mixlo_f16 v22, v33, v26, 0
	v_pack_b32_f16 v20, v25, v21
	v_alignbit_b32 v21, v22, v21, 16
	v_mul_f32_e32 v22, 0xbfb8aa3b, v34
	v_exp_f32_e32 v22, v22
	v_mad_u32_u24 v25, v23, s4, v80
	ds_write_b64 v25, v[20:21]
	v_mul_f32_e32 v21, 0xbfb8aa3b, v35
	v_add_f32_e32 v20, 1.0, v22
	v_mul_f32_e32 v22, 0xbfb8aa3b, v36
	v_rcp_f32_e32 v20, v20
	v_exp_f32_e32 v21, v21
	v_exp_f32_e32 v22, v22
	v_mov_b32_e32 v23, v36
	v_fma_mixlo_f16 v26, v34, v20, 0
	v_add_f32_e32 v20, 1.0, v21
	v_add_f32_e32 v21, 1.0, v22
	v_mul_f32_e32 v22, 0xbfb8aa3b, v37
	v_exp_f32_e32 v28, v22
	v_rcp_f32_e32 v20, v20
	v_rcp_f32_e32 v21, v21
	v_mov_b32_e32 v22, v35
	v_add_f32_e32 v28, 1.0, v28
	v_rcp_f32_e32 v28, v28
	v_pk_mul_f32 v[20:21], v[22:23], v[20:21]
	v_or_b32_e32 v23, v118, v39
	v_cvt_pk_f16_f32 v21, v20, v21
	v_fma_mixlo_f16 v22, v37, v28, 0
	v_pack_b32_f16 v20, v26, v21
	v_alignbit_b32 v21, v22, v21, 16
	v_mul_f32_e32 v22, 0xbfb8aa3b, v14
	v_exp_f32_e32 v22, v22
	v_mad_u32_u24 v23, v23, s4, v80
	ds_write_b64 v23, v[20:21]
	v_mul_f32_e32 v21, 0xbfb8aa3b, v15
	v_add_f32_e32 v20, 1.0, v22
	v_rcp_f32_e32 v20, v20
	v_exp_f32_e32 v21, v21
	v_mul_f32_e32 v22, 0xbfb8aa3b, v16
	v_exp_f32_e32 v22, v22
	v_fma_mixlo_f16 v26, v14, v20, 0
	v_add_f32_e32 v14, 1.0, v21
	v_rcp_f32_e32 v20, v14
	v_add_f32_e32 v14, 1.0, v22
	v_rcp_f32_e32 v21, v14
	v_mov_b32_e32 v14, v15
	v_mul_f32_e32 v15, 0xbfb8aa3b, v17
	v_exp_f32_e32 v22, v15
	v_mov_b32_e32 v15, v16
	v_pk_mul_f32 v[14:15], v[14:15], v[20:21]
	v_mul_f32_e32 v20, 0xbfb8aa3b, v10
	v_cvt_pk_f16_f32 v15, v14, v15
	v_add_f32_e32 v14, 1.0, v22
	v_rcp_f32_e32 v16, v14
	v_exp_f32_e32 v20, v20
	v_pack_b32_f16 v14, v26, v15
	v_lshl_add_u64 v[0:1], s[0:1], 0, v[0:1]
	v_fma_mixlo_f16 v16, v17, v16, 0
	v_alignbit_b32 v15, v16, v15, 16
	ds_write_b64 v27, v[14:15] offset:32
	v_add_f32_e32 v14, 1.0, v20
	v_mul_f32_e32 v15, 0xbfb8aa3b, v11
	v_rcp_f32_e32 v14, v14
	v_exp_f32_e32 v15, v15
	v_mul_f32_e32 v16, 0xbfb8aa3b, v12
	v_exp_f32_e32 v16, v16
	v_fma_mixlo_f16 v17, v10, v14, 0
	v_add_f32_e32 v10, 1.0, v15
	v_rcp_f32_e32 v14, v10
	v_add_f32_e32 v10, 1.0, v16
	v_rcp_f32_e32 v15, v10
	v_mov_b32_e32 v10, v11
	v_mul_f32_e32 v11, 0xbfb8aa3b, v13
	v_exp_f32_e32 v16, v11
	v_mov_b32_e32 v11, v12
	v_pk_mul_f32 v[10:11], v[10:11], v[14:15]
	v_mul_f32_e32 v14, 0xbfb8aa3b, v6
	v_cvt_pk_f16_f32 v11, v10, v11
	v_add_f32_e32 v10, 1.0, v16
	v_rcp_f32_e32 v12, v10
	v_exp_f32_e32 v14, v14
	v_pack_b32_f16 v10, v17, v11
	v_fma_mixlo_f16 v12, v13, v12, 0
	v_alignbit_b32 v11, v12, v11, 16
	ds_write_b64 v24, v[10:11] offset:32
	v_add_f32_e32 v10, 1.0, v14
	v_mul_f32_e32 v11, 0xbfb8aa3b, v7
	v_rcp_f32_e32 v10, v10
	v_exp_f32_e32 v11, v11
	v_mul_f32_e32 v12, 0xbfb8aa3b, v8
	v_exp_f32_e32 v12, v12
	v_fma_mixlo_f16 v13, v6, v10, 0
	v_add_f32_e32 v6, 1.0, v11
	v_rcp_f32_e32 v10, v6
	v_add_f32_e32 v6, 1.0, v12
	v_rcp_f32_e32 v11, v6
	v_mov_b32_e32 v6, v7
	v_mul_f32_e32 v7, 0xbfb8aa3b, v9
	v_exp_f32_e32 v12, v7
	v_mov_b32_e32 v7, v8
	v_pk_mul_f32 v[6:7], v[6:7], v[10:11]
	v_mul_f32_e32 v10, 0xbfb8aa3b, v2
	v_cvt_pk_f16_f32 v7, v6, v7
	v_add_f32_e32 v6, 1.0, v12
	v_rcp_f32_e32 v8, v6
	v_exp_f32_e32 v10, v10
	v_pack_b32_f16 v6, v13, v7
	v_fma_mixlo_f16 v8, v9, v8, 0
	v_alignbit_b32 v7, v8, v7, 16
	ds_write_b64 v25, v[6:7] offset:32
	v_add_f32_e32 v6, 1.0, v10
	v_mul_f32_e32 v7, 0xbfb8aa3b, v3
	v_rcp_f32_e32 v6, v6
	v_exp_f32_e32 v7, v7
	v_mul_f32_e32 v8, 0xbfb8aa3b, v4
	v_exp_f32_e32 v8, v8
	v_fma_mixlo_f16 v9, v2, v6, 0
	v_add_f32_e32 v2, 1.0, v7
	v_mul_f32_e32 v7, 0xbfb8aa3b, v5
	v_rcp_f32_e32 v6, v2
	v_add_f32_e32 v2, 1.0, v8
	v_exp_f32_e32 v8, v7
	v_rcp_f32_e32 v7, v2
	v_mov_b32_e32 v2, v3
	v_mov_b32_e32 v3, v4
	v_add_f32_e32 v4, 1.0, v8
	v_rcp_f32_e32 v4, v4
	v_pk_mul_f32 v[2:3], v[2:3], v[6:7]
	v_fma_mixlo_f16 v4, v5, v4, 0
	v_cvt_pk_f16_f32 v3, v2, v3
	v_pack_b32_f16 v2, v9, v3
	v_alignbit_b32 v3, v4, v3, 16
	ds_write_b64 v23, v[2:3] offset:32
	s_waitcnt lgkmcnt(0)
	s_barrier
	ds_read_b128 v[2:5], v52 offset:40960
	ds_read_b128 v[6:9], v52 offset:40976
	ds_read_b128 v[10:13], v52 offset:40992
	ds_read_b128 v[14:17], v52 offset:41008
	s_waitcnt lgkmcnt(3)
	global_store_dwordx4 v[0:1], v[2:5], off
	s_nop 1
	v_add_co_u32_e32 v2, vcc, 0x2000, v0
	s_nop 1
	v_addc_co_u32_e32 v3, vcc, 0, v1, vcc
	v_add_co_u32_e32 v0, vcc, 0x6000, v0
	s_waitcnt lgkmcnt(2)
	global_store_dwordx4 v[2:3], v[6:9], off
	v_lshl_add_u64 v[2:3], s[0:1], 0, v[18:19]
	v_addc_co_u32_e32 v1, vcc, 0, v1, vcc
	s_waitcnt lgkmcnt(1)
	global_store_dwordx4 v[2:3], v[10:13], off
	s_waitcnt lgkmcnt(0)
	global_store_dwordx4 v[0:1], v[14:17], off
	s_endpgm
	.p2align	8

	.amdhsa_kernel _Z4k_k2ILb0EEvPKDF16_S1_PKfS3_S3_S1_S1_PfS3_S3_S1_PDF16_PKiS4_S4_
		.amdhsa_group_segment_fixed_size 98816
		.amdhsa_private_segment_fixed_size 0
		.amdhsa_kernarg_size 120
		.amdhsa_user_sgpr_count 2
		.amdhsa_user_sgpr_dispatch_ptr 0
		.amdhsa_user_sgpr_queue_ptr 0
		.amdhsa_user_sgpr_kernarg_segment_ptr 1
		.amdhsa_user_sgpr_dispatch_id 0
		.amdhsa_user_sgpr_kernarg_preload_length 0
		.amdhsa_user_sgpr_kernarg_preload_offset 0
		.amdhsa_user_sgpr_private_segment_size 0
		.amdhsa_uses_dynamic_stack 0
		.amdhsa_enable_private_segment 0
		.amdhsa_system_sgpr_workgroup_id_x 1
		.amdhsa_system_sgpr_workgroup_id_y 0
		.amdhsa_system_sgpr_workgroup_id_z 0
		.amdhsa_system_sgpr_workgroup_info 0
		.amdhsa_system_vgpr_workitem_id 0
		.amdhsa_next_free_vgpr 212
		.amdhsa_next_free_sgpr 96
		.amdhsa_accum_offset 212
		.amdhsa_reserve_vcc 1
		.amdhsa_float_round_mode_32 0
		.amdhsa_float_round_mode_16_64 0
		.amdhsa_float_denorm_mode_32 3
		.amdhsa_float_denorm_mode_16_64 3
		.amdhsa_dx10_clamp 1
		.amdhsa_ieee_mode 1
		.amdhsa_fp16_overflow 0
		.amdhsa_tg_split 0
		.amdhsa_exception_fp_ieee_invalid_op 0
		.amdhsa_exception_fp_denorm_src 0
		.amdhsa_exception_fp_ieee_div_zero 0
		.amdhsa_exception_fp_ieee_overflow 0
		.amdhsa_exception_fp_ieee_underflow 0
		.amdhsa_exception_fp_ieee_inexact 0
		.amdhsa_exception_int_div_zero 0
	.end_amdhsa_kernel

.LBB6_10:
	v_mov_b32_e32 v4, 0
	ds_read_b128 v[0:3], v4 offset:12288
	ds_read_b128 v[4:7], v4 offset:12304
	s_load_dwordx2 s[0:1], s[0:1], 0x70
	s_lshl_b32 s2, s2, 2
	s_waitcnt lgkmcnt(0)
	v_add_f32_e32 v0, 0, v0
	v_add_f32_e32 v0, v0, v1
	v_add_f32_e32 v0, v0, v2
	v_add_f32_e32 v0, v0, v3
	v_add_f32_e32 v0, v0, v4
	v_add_f32_e32 v0, v0, v5
	v_add_f32_e32 v0, v0, v6
	v_add_f32_e32 v0, v0, v7
	v_mov_b32_e32 v1, s2
	global_store_dword v1, v0, s[0:1]
	s_endpgm
	.p2align	8

	.text
	.p2alignl 8, 3212836864
	.fill 256, 4, 3212836864

amdhsa.kernels:
  - .agpr_count:     0
    .args:
      - .actual_access:  read_only
        .address_space:  global
        .offset:         0
        .size:           8
        .value_kind:     global_buffer
      - .actual_access:  write_only
        .address_space:  global
        .offset:         8
        .size:           8
        .value_kind:     global_buffer
      - .offset:         16
        .size:           4
        .value_kind:     by_value
      - .offset:         20
        .size:           4
        .value_kind:     by_value
      - .actual_access:  read_only
        .address_space:  global
        .offset:         24
        .size:           8
        .value_kind:     global_buffer
      - .actual_access:  write_only
        .address_space:  global
        .offset:         32
        .size:           8
        .value_kind:     global_buffer
      - .offset:         40
        .size:           4
        .value_kind:     by_value
      - .offset:         44
        .size:           4
        .value_kind:     by_value
      - .actual_access:  read_only
        .address_space:  global
        .offset:         48
        .size:           8
        .value_kind:     global_buffer
      - .actual_access:  write_only
        .address_space:  global
        .offset:         56
        .size:           8
        .value_kind:     global_buffer
      - .offset:         64
        .size:           4
        .value_kind:     by_value
      - .offset:         68
        .size:           4
        .value_kind:     by_value
      - .actual_access:  read_only
        .address_space:  global
        .offset:         72
        .size:           8
        .value_kind:     global_buffer
      - .actual_access:  write_only
        .address_space:  global
        .offset:         80
        .size:           8
        .value_kind:     global_buffer
      - .offset:         88
        .size:           4
        .value_kind:     by_value
      - .actual_access:  read_only
        .address_space:  global
        .offset:         96
        .size:           8
        .value_kind:     global_buffer
      - .actual_access:  write_only
        .address_space:  global
        .offset:         104
        .size:           8
        .value_kind:     global_buffer
      - .offset:         112
        .size:           4
        .value_kind:     by_value
      - .offset:         120
        .size:           4
        .value_kind:     hidden_block_count_x
      - .offset:         124
        .size:           4
        .value_kind:     hidden_block_count_y
      - .offset:         128
        .size:           4
        .value_kind:     hidden_block_count_z
      - .offset:         132
        .size:           2
        .value_kind:     hidden_group_size_x
      - .offset:         134
        .size:           2
        .value_kind:     hidden_group_size_y
      - .offset:         136
        .size:           2
        .value_kind:     hidden_group_size_z
      - .offset:         138
        .size:           2
        .value_kind:     hidden_remainder_x
      - .offset:         140
        .size:           2
        .value_kind:     hidden_remainder_y
      - .offset:         142
        .size:           2
        .value_kind:     hidden_remainder_z
      - .offset:         160
        .size:           8
        .value_kind:     hidden_global_offset_x
      - .offset:         168
        .size:           8
        .value_kind:     hidden_global_offset_y
      - .offset:         176
        .size:           8
        .value_kind:     hidden_global_offset_z
      - .offset:         184
        .size:           2
        .value_kind:     hidden_grid_dims
    .group_segment_fixed_size: 0
    .kernarg_segment_align: 8
    .kernarg_segment_size: 376
    .language:       OpenCL C
    .language_version:
      - 2
      - 0
    .max_flat_workgroup_size: 1024
    .name:           _Z5k_swzPKfPDF16_iiS0_S1_iiS0_S1_iiS0_PfiS0_S1_i
    .private_segment_fixed_size: 0
    .sgpr_count:     32
    .sgpr_spill_count: 0
    .symbol:         _Z5k_swzPKfPDF16_iiS0_S1_iiS0_S1_iiS0_PfiS0_S1_i.kd
    .uniform_work_group_size: 1
    .uses_dynamic_stack: false
    .vgpr_count:     14
    .vgpr_spill_count: 0
    .wavefront_size: 64
  - .agpr_count:     0
    .args:
      - .actual_access:  read_only
        .address_space:  global
        .offset:         0
        .size:           8
        .value_kind:     global_buffer
      - .actual_access:  read_only
        .address_space:  global
        .offset:         8
        .size:           8
        .value_kind:     global_buffer
      - .actual_access:  write_only
        .address_space:  global
        .offset:         16
        .size:           8
        .value_kind:     global_buffer
      - .actual_access:  read_only
        .address_space:  global
        .offset:         24
        .size:           8
        .value_kind:     global_buffer
      - .actual_access:  read_only
        .address_space:  global
        .offset:         32
        .size:           8
        .value_kind:     global_buffer
      - .actual_access:  read_only
        .address_space:  global
        .offset:         40
        .size:           8
        .value_kind:     global_buffer
      - .actual_access:  write_only
        .address_space:  global
        .offset:         48
        .size:           8
        .value_kind:     global_buffer
    .group_segment_fixed_size: 98816
    .kernarg_segment_align: 8
    .kernarg_segment_size: 56
    .language:       OpenCL C
    .language_version:
      - 2
      - 0
    .max_flat_workgroup_size: 512
    .name:           _Z10k_ka_firstPKfPKiPfS0_S0_PKDF16_PDF16_
    .private_segment_fixed_size: 0
    .sgpr_count:     59
    .sgpr_spill_count: 0
    .symbol:         _Z10k_ka_firstPKfPKiPfS0_S0_PKDF16_PDF16_.kd
    .uniform_work_group_size: 1
    .uses_dynamic_stack: false
    .vgpr_count:     174
    .vgpr_spill_count: 0
    .wavefront_size: 64
  - .agpr_count:     0
    .args:
      - .actual_access:  read_only
        .address_space:  global
        .offset:         0
        .size:           8
        .value_kind:     global_buffer
      - .actual_access:  read_only
        .address_space:  global
        .offset:         8
        .size:           8
        .value_kind:     global_buffer
      - .actual_access:  read_only
        .address_space:  global
        .offset:         16
        .size:           8
        .value_kind:     global_buffer
      - .actual_access:  read_only
        .address_space:  global
        .offset:         24
        .size:           8
        .value_kind:     global_buffer
      - .actual_access:  read_only
        .address_space:  global
        .offset:         32
        .size:           8
        .value_kind:     global_buffer
      - .actual_access:  read_only
        .address_space:  global
        .offset:         40
        .size:           8
        .value_kind:     global_buffer
      - .actual_access:  write_only
        .address_space:  global
        .offset:         48
        .size:           8
        .value_kind:     global_buffer
      - .actual_access:  write_only
        .address_space:  global
        .offset:         56
        .size:           8
        .value_kind:     global_buffer
      - .actual_access:  write_only
        .address_space:  global
        .offset:         64
        .size:           8
        .value_kind:     global_buffer
      - .actual_access:  read_only
        .address_space:  global
        .offset:         72
        .size:           8
        .value_kind:     global_buffer
      - .actual_access:  write_only
        .address_space:  global
        .offset:         80
        .size:           8
        .value_kind:     global_buffer
      - .actual_access:  write_only
        .address_space:  global
        .offset:         88
        .size:           8
        .value_kind:     global_buffer
    .group_segment_fixed_size: 47616
    .kernarg_segment_align: 8
    .kernarg_segment_size: 96
    .language:       OpenCL C
    .language_version:
      - 2
      - 0
    .max_flat_workgroup_size: 512
    .name:           _Z12k_conv_xprojPKDF16_PKfS2_S0_S0_S2_PDF16_S3_PfS2_S3_S4_
    .private_segment_fixed_size: 0
    .sgpr_count:     32
    .sgpr_spill_count: 0
    .symbol:         _Z12k_conv_xprojPKDF16_PKfS2_S0_S0_S2_PDF16_S3_PfS2_S3_S4_.kd
    .uniform_work_group_size: 1
    .uses_dynamic_stack: false
    .vgpr_count:     160
    .vgpr_spill_count: 0
    .wavefront_size: 64
  - .agpr_count:     0
    .args:
      - .actual_access:  read_only
        .address_space:  global
        .offset:         0
        .size:           8
        .value_kind:     global_buffer
      - .actual_access:  read_only
        .address_space:  global
        .offset:         8
        .size:           8
        .value_kind:     global_buffer
      - .actual_access:  read_only
        .address_space:  global
        .offset:         16
        .size:           8
        .value_kind:     global_buffer
      - .actual_access:  write_only
        .address_space:  global
        .offset:         24
        .size:           8
        .value_kind:     global_buffer
    .group_segment_fixed_size: 16384
    .kernarg_segment_align: 8
    .kernarg_segment_size: 32
    .language:       OpenCL C
    .language_version:
      - 2
      - 0
    .max_flat_workgroup_size: 512
    .name:           _Z11k_scan_combPKDF16_PKfS2_PDF16_
    .private_segment_fixed_size: 0
    .sgpr_count:     18
    .sgpr_spill_count: 0
    .symbol:         _Z11k_scan_combPKDF16_PKfS2_PDF16_.kd
    .uniform_work_group_size: 1
    .uses_dynamic_stack: false
    .vgpr_count:     120
    .vgpr_spill_count: 0
    .wavefront_size: 64
  - .agpr_count:     0
    .args:
      - .actual_access:  read_only
        .address_space:  global
        .offset:         0
        .size:           8
        .value_kind:     global_buffer
      - .actual_access:  read_only
        .address_space:  global
        .offset:         8
        .size:           8
        .value_kind:     global_buffer
      - .actual_access:  read_only
        .address_space:  global
        .offset:         16
        .size:           8
        .value_kind:     global_buffer
      - .actual_access:  read_only
        .address_space:  global
        .offset:         24
        .size:           8
        .value_kind:     global_buffer
      - .actual_access:  write_only
        .address_space:  global
        .offset:         32
        .size:           8
        .value_kind:     global_buffer
    .group_segment_fixed_size: 32
    .kernarg_segment_align: 8
    .kernarg_segment_size: 40
    .language:       OpenCL C
    .language_version:
      - 2
      - 0
    .max_flat_workgroup_size: 256
    .name:           _Z6k_headPKfS0_S0_S0_Pf
    .private_segment_fixed_size: 0
    .sgpr_count:     30
    .sgpr_spill_count: 0
    .symbol:         _Z6k_headPKfS0_S0_S0_Pf.kd
    .uniform_work_group_size: 1
    .uses_dynamic_stack: false
    .vgpr_count:     24
    .vgpr_spill_count: 0
    .wavefront_size: 64
  - .agpr_count:     0
    .args:
      - .actual_access:  read_only
        .address_space:  global
        .offset:         0
        .size:           8
        .value_kind:     global_buffer
      - .actual_access:  read_only
        .address_space:  global
        .offset:         8
        .size:           8
        .value_kind:     global_buffer
      - .actual_access:  read_only
        .address_space:  global
        .offset:         16
        .size:           8
        .value_kind:     global_buffer
      - .actual_access:  read_only
        .address_space:  global
        .offset:         24
        .size:           8
        .value_kind:     global_buffer
      - .actual_access:  read_only
        .address_space:  global
        .offset:         32
        .size:           8
        .value_kind:     global_buffer
      - .actual_access:  read_only
        .address_space:  global
        .offset:         40
        .size:           8
        .value_kind:     global_buffer
      - .actual_access:  read_only
        .address_space:  global
        .offset:         48
        .size:           8
        .value_kind:     global_buffer
      - .address_space:  global
        .offset:         56
        .size:           8
        .value_kind:     global_buffer
      - .actual_access:  read_only
        .address_space:  global
        .offset:         64
        .size:           8
        .value_kind:     global_buffer
      - .actual_access:  read_only
        .address_space:  global
        .offset:         72
        .size:           8
        .value_kind:     global_buffer
      - .actual_access:  read_only
        .address_space:  global
        .offset:         80
        .size:           8
        .value_kind:     global_buffer
      - .address_space:  global
        .offset:         88
        .size:           8
        .value_kind:     global_buffer
      - .actual_access:  read_only
        .address_space:  global
        .offset:         96
        .size:           8
        .value_kind:     global_buffer
      - .actual_access:  read_only
        .address_space:  global
        .offset:         104
        .size:           8
        .value_kind:     global_buffer
      - .actual_access:  read_only
        .address_space:  global
        .offset:         112
        .size:           8
        .value_kind:     global_buffer
    .group_segment_fixed_size: 98816
    .kernarg_segment_align: 8
    .kernarg_segment_size: 120
    .language:       OpenCL C
    .language_version:
      - 2
      - 0
    .max_flat_workgroup_size: 512
    .name:           _Z4k_k2ILb0EEvPKDF16_S1_PKfS3_S3_S1_S1_PfS3_S3_S1_PDF16_PKiS4_S4_
    .private_segment_fixed_size: 0
    .sgpr_count:     64
    .sgpr_spill_count: 0
    .symbol:         _Z4k_k2ILb0EEvPKDF16_S1_PKfS3_S3_S1_S1_PfS3_S3_S1_PDF16_PKiS4_S4_.kd
    .uniform_work_group_size: 1
    .uses_dynamic_stack: false
    .vgpr_count:     212
    .vgpr_spill_count: 0
    .wavefront_size: 64
  - .agpr_count:     0
    .args:
      - .actual_access:  read_only
        .address_space:  global
        .offset:         0
        .size:           8
        .value_kind:     global_buffer
      - .actual_access:  read_only
        .address_space:  global
        .offset:         8
        .size:           8
        .value_kind:     global_buffer
      - .actual_access:  read_only
        .address_space:  global
        .offset:         16
        .size:           8
        .value_kind:     global_buffer
      - .actual_access:  read_only
        .address_space:  global
        .offset:         24
        .size:           8
        .value_kind:     global_buffer
      - .actual_access:  read_only
        .address_space:  global
        .offset:         32
        .size:           8
        .value_kind:     global_buffer
      - .actual_access:  read_only
        .address_space:  global
        .offset:         40
        .size:           8
        .value_kind:     global_buffer
      - .actual_access:  read_only
        .address_space:  global
        .offset:         48
        .size:           8
        .value_kind:     global_buffer
      - .actual_access:  read_only
        .address_space:  global
        .offset:         56
        .size:           8
        .value_kind:     global_buffer
      - .actual_access:  read_only
        .address_space:  global
        .offset:         64
        .size:           8
        .value_kind:     global_buffer
      - .actual_access:  read_only
        .address_space:  global
        .offset:         72
        .size:           8
        .value_kind:     global_buffer
      - .actual_access:  read_only
        .address_space:  global
        .offset:         80
        .size:           8
        .value_kind:     global_buffer
      - .actual_access:  read_only
        .address_space:  global
        .offset:         88
        .size:           8
        .value_kind:     global_buffer
      - .actual_access:  read_only
        .address_space:  global
        .offset:         96
        .size:           8
        .value_kind:     global_buffer
      - .actual_access:  write_only
        .address_space:  global
        .offset:         104
        .size:           8
        .value_kind:     global_buffer
      - .actual_access:  write_only
        .address_space:  global
        .offset:         112
        .size:           8
        .value_kind:     global_buffer
    .group_segment_fixed_size: 98816
    .kernarg_segment_align: 8
    .kernarg_segment_size: 120
    .language:       OpenCL C
    .language_version:
      - 2
      - 0
    .max_flat_workgroup_size: 512
    .name:           _Z4k_k2ILb1EEvPKDF16_S1_PKfS3_S3_S1_S1_PfS3_S3_S1_PDF16_PKiS4_S4_
    .private_segment_fixed_size: 0
    .sgpr_count:     44
    .sgpr_spill_count: 0
    .symbol:         _Z4k_k2ILb1EEvPKDF16_S1_PKfS3_S3_S1_S1_PfS3_S3_S1_PDF16_PKiS4_S4_.kd
    .uniform_work_group_size: 1
    .uses_dynamic_stack: false
    .vgpr_count:     160
    .vgpr_spill_count: 0
    .wavefront_size: 64
